# GEMM main loops: extra s_setprio 0/1 window after every 8 MFMAs (loader wave gets more issue slots)
# speedup vs baseline: 1.0085x; 1.0075x over previous
; #define PG8_STAGE(bufoff, gbase, voff) do { _Pragma("unroll") for (int _i = 0; _i < 2; ++_i) \
;         __builtin_amdgcn_global_load_lds((const unsigned*)((const char*)(gbase) + (voff)[_i]), (LAS unsigned*)(lds + (bufoff) + ldsw + _i * 8192), 16, 0, 0); } while (0)
; #define PG8_LDA(dst, b, h) do { _Pragma("unroll") for (int m = 0; m < 4; ++m) _Pragma("unroll") for (int k = 0; k < 2; ++k) dst[m][k] = *(const LAS bf16x8*)(lds + PG8_SA(b, h) + aoff + m * 2048 + k * 1024); } while (0)
; #define PG8_LDB(dst, b, h) do { _Pragma("unroll") for (int n = 0; n < 2; ++n) _Pragma("unroll") for (int k = 0; k < 2; ++k) dst[n][k] = *(const LAS bf16x8*)(lds + PG8_SB(b, h) + boff + n * 2048 + k * 1024); } while (0)
; #define PG8_MMA(ai, bj, At, Bt) do { __builtin_amdgcn_s_setprio(1); _Pragma("unroll") for (int m = 0; m < 4; ++m) _Pragma("unroll") for (int n = 0; n < 2; ++n) _Pragma("unroll") for (int k = 0; k < 2; ++k) \
;         acc[ai][bj][m][n] = __builtin_amdgcn_mfma_f32_16x16x32_bf16(Bt[n][k], At[m][k], acc[ai][bj][m][n], 0, 0, 0); __builtin_amdgcn_s_setprio(0); } while (0)
; #define PG8_WAIT_V(n) asm volatile("s_waitcnt vmcnt(" #n ")" ::: "memory")
; #define PG8_WAIT_L(n) asm volatile("s_waitcnt lgkmcnt(" #n ")" ::: "memory")
; #define PG8_BAR __builtin_amdgcn_s_barrier()
; template <class Epi, class Sched>
; __device__ __forceinline__ void gemm_phase(LAS unsigned char* lds, const Gemm g, const Sched& S, const Epi& E, const int tid, unsigned* last_sig = nullptr) {
;     ...
;         for (int t = 0; t < nt; t += 2) {
;             const bool last = (t == nt - 2);
;             const char* a1 = cA + (size_t)(t + 1) * kstep;
;             const char* a2 = last ? nA : cA + (size_t)(t + 2) * kstep; const char* b2 = last ? nB : cB + (size_t)(t + 2) * kstep;
;             const char* a3 = a2 + kstep; const char* b3 = b2 + kstep;
;             PG8_LDB(B0, 0, 0); PG8_LDB(B1, 0, 1); PG8_SCHED; PG8_LDA(At, 0, 0); PG8_STAGE(PG8_SA(1, 1), a1 + hstep, voffA);
;             PG8_WAIT_V(8); PG8_WAIT_L(0); PG8_BAR; PG8_MMA(0, 0, At, B0); PG8_MMA(0, 1, At, B1); PG8_BAR; PG8_SCHED;
;             PG8_LDA(At, 0, 1); PG8_STAGE(PG8_SB(0, 0), b2, voffB); PG8_STAGE(PG8_SB(0, 1), b2 + hstep, voffB); PG8_STAGE(PG8_SA(0, 0), a2, voffA);
;             PG8_WAIT_V(8); PG8_WAIT_L(0); PG8_BAR; PG8_MMA(1, 0, At, B0); PG8_MMA(1, 1, At, B1); PG8_BAR; PG8_SCHED;
.LBB0_172:
	s_add_u32 s14, s20, 0xfff80080
	s_addc_u32 s15, s21, -1
	s_add_i32 s60, 0, 0x10000
	s_cmp_eq_u32 s59, 28
	s_cselect_b32 s41, s13, s15
	s_cselect_b32 s40, s28, s14
	s_cselect_b32 s23, s11, s58
	s_cselect_b32 s22, s56, s57
	s_add_i32 s14, 0, 0x14000
	v_add_u32_e32 v160, s60, v145
	v_add_u32_e32 v176, s14, v145
	ds_read_b128 v[130:133], v160
	ds_read_b128 v[152:155], v160 offset:1024
	ds_read_b128 v[156:159], v160 offset:2048
	ds_read_b128 v[160:163], v160 offset:3072
	ds_read_b128 v[164:167], v176
	ds_read_b128 v[168:171], v176 offset:1024
	ds_read_b128 v[172:175], v176 offset:2048
	ds_read_b128 v[176:179], v176 offset:3072
	v_lshl_add_u64 v[184:185], s[20:21], 0, v[148:149]
	s_add_i32 m0, s44, 0xc000
	ds_read_b128 v[180:183], v147
	ds_read_b128 v[200:203], v147 offset:1024
	ds_read_b128 v[204:207], v147 offset:2048
	ds_read_b128 v[208:211], v147 offset:3072
	ds_read_b128 v[212:215], v147 offset:4096
	ds_read_b128 v[216:219], v147 offset:5120
	ds_read_b128 v[220:223], v147 offset:6144
	ds_read_b128 v[232:235], v147 offset:7168
	global_load_lds_dwordx4 v[184:185], off
	v_lshl_add_u64 v[184:185], s[20:21], 0, v[150:151]
	s_add_i32 m0, s44, 0xe000
	s_nop 0
	global_load_lds_dwordx4 v[184:185], off
	s_waitcnt vmcnt(8)
	s_waitcnt lgkmcnt(0)
	s_barrier
	s_setprio 1
	s_waitcnt lgkmcnt(0)
	v_mfma_f32_16x16x32_bf16 v[126:129], v[130:133], v[180:183], v[126:129]
	v_mfma_f32_16x16x32_bf16 v[122:125], v[156:159], v[180:183], v[122:125]
	v_mfma_f32_16x16x32_bf16 v[118:121], v[130:133], v[204:207], v[118:121]
	v_mfma_f32_16x16x32_bf16 v[110:113], v[156:159], v[204:207], v[110:113]
	v_mfma_f32_16x16x32_bf16 v[102:105], v[130:133], v[212:215], v[102:105]
	v_mfma_f32_16x16x32_bf16 v[94:97], v[156:159], v[212:215], v[94:97]
	v_mfma_f32_16x16x32_bf16 v[86:89], v[130:133], v[220:223], v[86:89]
	v_mfma_f32_16x16x32_bf16 v[78:81], v[156:159], v[220:223], v[78:81]
	s_setprio 0
	s_setprio 1
	v_mfma_f32_16x16x32_bf16 v[126:129], v[152:155], v[200:203], v[126:129]
	v_mfma_f32_16x16x32_bf16 v[122:125], v[160:163], v[200:203], v[122:125]
	v_mfma_f32_16x16x32_bf16 v[118:121], v[152:155], v[208:211], v[118:121]
	v_mfma_f32_16x16x32_bf16 v[110:113], v[160:163], v[208:211], v[110:113]
	v_mfma_f32_16x16x32_bf16 v[102:105], v[152:155], v[216:219], v[102:105]
	v_mfma_f32_16x16x32_bf16 v[94:97], v[160:163], v[216:219], v[94:97]
	v_mfma_f32_16x16x32_bf16 v[86:89], v[152:155], v[232:235], v[86:89]
	v_mfma_f32_16x16x32_bf16 v[78:81], v[160:163], v[232:235], v[78:81]
	s_setprio 0
	s_setprio 1
	v_mfma_f32_16x16x32_bf16 v[114:117], v[164:167], v[180:183], v[114:117]
	v_mfma_f32_16x16x32_bf16 v[106:109], v[172:175], v[180:183], v[106:109]
	v_mfma_f32_16x16x32_bf16 v[98:101], v[164:167], v[204:207], v[98:101]
	v_mfma_f32_16x16x32_bf16 v[90:93], v[172:175], v[204:207], v[90:93]
	v_mfma_f32_16x16x32_bf16 v[82:85], v[164:167], v[212:215], v[82:85]
	v_mfma_f32_16x16x32_bf16 v[74:77], v[172:175], v[212:215], v[74:77]
	v_mfma_f32_16x16x32_bf16 v[70:73], v[164:167], v[220:223], v[70:73]
	v_mfma_f32_16x16x32_bf16 v[66:69], v[172:175], v[220:223], v[66:69]
	s_setprio 0
	s_setprio 1
	v_mfma_f32_16x16x32_bf16 v[114:117], v[168:171], v[200:203], v[114:117]
	v_mfma_f32_16x16x32_bf16 v[106:109], v[176:179], v[200:203], v[106:109]
	v_mfma_f32_16x16x32_bf16 v[98:101], v[168:171], v[208:211], v[98:101]
	v_mfma_f32_16x16x32_bf16 v[90:93], v[176:179], v[208:211], v[90:93]
	v_mfma_f32_16x16x32_bf16 v[82:85], v[168:171], v[216:219], v[82:85]
	v_mfma_f32_16x16x32_bf16 v[74:77], v[176:179], v[216:219], v[74:77]
	v_mfma_f32_16x16x32_bf16 v[70:73], v[168:171], v[232:235], v[70:73]
	v_mfma_f32_16x16x32_bf16 v[66:69], v[176:179], v[232:235], v[66:69]
	s_setprio 0
	s_barrier
	s_add_i32 s15, s60, s43
	v_lshl_add_u64 v[184:185], s[22:23], 0, v[138:139]
	s_mov_b32 m0, s15
	ds_read_b128 v[180:183], v147 offset:16384
	ds_read_b128 v[200:203], v147 offset:17408
	ds_read_b128 v[204:207], v147 offset:18432
	ds_read_b128 v[208:211], v147 offset:19456
	ds_read_b128 v[212:215], v147 offset:20480
	ds_read_b128 v[216:219], v147 offset:21504
	ds_read_b128 v[220:223], v147 offset:22528
	ds_read_b128 v[232:235], v147 offset:23552
	global_load_lds_dwordx4 v[184:185], off
	s_add_i32 m0, s15, 0x2000
	s_add_u32 s60, s22, 0x80000
	v_lshl_add_u64 v[236:237], s[22:23], 0, v[134:135]
	s_addc_u32 s61, s23, 0
	s_add_i32 s14, s14, s43
	global_load_lds_dwordx4 v[236:237], off
	v_lshl_add_u64 v[238:239], s[60:61], 0, v[138:139]
	s_mov_b32 m0, s14
	v_lshl_add_u64 v[240:241], s[40:41], 0, v[136:137]
	global_load_lds_dwordx4 v[238:239], off
	v_lshl_add_u64 v[238:239], s[60:61], 0, v[134:135]
	s_add_i32 m0, s14, 0x2000
	s_nop 0
	global_load_lds_dwordx4 v[238:239], off
	v_lshl_add_u64 v[238:239], s[40:41], 0, v[140:141]
	s_mov_b32 m0, s44
	s_nop 0
	global_load_lds_dwordx4 v[238:239], off
	s_mov_b32 m0, s45
	s_nop 0
	global_load_lds_dwordx4 v[240:241], off
	s_waitcnt vmcnt(8)
	s_waitcnt lgkmcnt(0)
	s_barrier
; #define PG8_STAGE(bufoff, gbase, voff) do { _Pragma("unroll") for (int _i = 0; _i < 2; ++_i) \
;         __builtin_amdgcn_global_load_lds((const unsigned*)((const char*)(gbase) + (voff)[_i]), (LAS unsigned*)(lds + (bufoff) + ldsw + _i * 8192), 16, 0, 0); } while (0)
; #define PG8_LDA(dst, b, h) do { _Pragma("unroll") for (int m = 0; m < 4; ++m) _Pragma("unroll") for (int k = 0; k < 2; ++k) dst[m][k] = *(const LAS bf16x8*)(lds + PG8_SA(b, h) + aoff + m * 2048 + k * 1024); } while (0)
; #define PG8_LDB(dst, b, h) do { _Pragma("unroll") for (int n = 0; n < 2; ++n) _Pragma("unroll") for (int k = 0; k < 2; ++k) dst[n][k] = *(const LAS bf16x8*)(lds + PG8_SB(b, h) + boff + n * 2048 + k * 1024); } while (0)
; #define PG8_MMA(ai, bj, At, Bt) do { __builtin_amdgcn_s_setprio(1); _Pragma("unroll") for (int m = 0; m < 4; ++m) _Pragma("unroll") for (int n = 0; n < 2; ++n) _Pragma("unroll") for (int k = 0; k < 2; ++k) \
;         acc[ai][bj][m][n] = __builtin_amdgcn_mfma_f32_16x16x32_bf16(Bt[n][k], At[m][k], acc[ai][bj][m][n], 0, 0, 0); __builtin_amdgcn_s_setprio(0); } while (0)
; #define PG8_WAIT_V(n) asm volatile("s_waitcnt vmcnt(" #n ")" ::: "memory")
; #define PG8_WAIT_L(n) asm volatile("s_waitcnt lgkmcnt(" #n ")" ::: "memory")
; #define PG8_BAR __builtin_amdgcn_s_barrier()
; #define PG8_SCHED __builtin_amdgcn_sched_barrier(0)
; template <class Epi, class Sched>
; __device__ __forceinline__ void gemm_phase(LAS unsigned char* lds, const Gemm g, const Sched& S, const Epi& E, const int tid, unsigned* last_sig = nullptr) {
;     ...
;             PG8_WAIT_V(8); PG8_WAIT_L(0); PG8_BAR; PG8_MMA(1, 0, At, B0); PG8_MMA(1, 1, At, B1); PG8_BAR; PG8_SCHED;
;             PG8_LDB(B0, 1, 0); PG8_LDB(B1, 1, 1); PG8_SCHED; PG8_LDA(At, 1, 0); PG8_STAGE(PG8_SA(0, 1), a2 + hstep, voffA);
;             PG8_WAIT_V(8); PG8_WAIT_L(0); PG8_BAR; PG8_MMA(0, 0, At, B0); PG8_MMA(0, 1, At, B1); PG8_BAR; PG8_SCHED;
	s_setprio 1
	s_waitcnt lgkmcnt(0)
	v_mfma_f32_16x16x32_bf16 v[62:65], v[130:133], v[180:183], v[62:65]
	v_mfma_f32_16x16x32_bf16 v[58:61], v[156:159], v[180:183], v[58:61]
	v_mfma_f32_16x16x32_bf16 v[54:57], v[130:133], v[204:207], v[54:57]
	v_mfma_f32_16x16x32_bf16 v[46:49], v[156:159], v[204:207], v[46:49]
	v_mfma_f32_16x16x32_bf16 v[38:41], v[130:133], v[212:215], v[38:41]
	v_mfma_f32_16x16x32_bf16 v[30:33], v[156:159], v[212:215], v[30:33]
	v_mfma_f32_16x16x32_bf16 v[22:25], v[130:133], v[220:223], v[22:25]
	v_mfma_f32_16x16x32_bf16 v[14:17], v[156:159], v[220:223], v[14:17]
	s_setprio 0
	s_setprio 1
	v_mfma_f32_16x16x32_bf16 v[62:65], v[152:155], v[200:203], v[62:65]
	v_mfma_f32_16x16x32_bf16 v[58:61], v[160:163], v[200:203], v[58:61]
	v_mfma_f32_16x16x32_bf16 v[54:57], v[152:155], v[208:211], v[54:57]
	v_mfma_f32_16x16x32_bf16 v[46:49], v[160:163], v[208:211], v[46:49]
	v_mfma_f32_16x16x32_bf16 v[38:41], v[152:155], v[216:219], v[38:41]
	v_mfma_f32_16x16x32_bf16 v[30:33], v[160:163], v[216:219], v[30:33]
	v_mfma_f32_16x16x32_bf16 v[22:25], v[152:155], v[232:235], v[22:25]
	v_mfma_f32_16x16x32_bf16 v[14:17], v[160:163], v[232:235], v[14:17]
	s_setprio 0
	s_setprio 1
	v_mfma_f32_16x16x32_bf16 v[50:53], v[164:167], v[180:183], v[50:53]
	v_mfma_f32_16x16x32_bf16 v[42:45], v[172:175], v[180:183], v[42:45]
	v_mfma_f32_16x16x32_bf16 v[34:37], v[164:167], v[204:207], v[34:37]
	v_mfma_f32_16x16x32_bf16 v[26:29], v[172:175], v[204:207], v[26:29]
	v_mfma_f32_16x16x32_bf16 v[18:21], v[164:167], v[212:215], v[18:21]
	v_mfma_f32_16x16x32_bf16 v[10:13], v[172:175], v[212:215], v[10:13]
	v_mfma_f32_16x16x32_bf16 v[6:9], v[164:167], v[220:223], v[6:9]
	v_mfma_f32_16x16x32_bf16 v[2:5], v[172:175], v[220:223], v[2:5]
	s_setprio 0
	s_setprio 1
	v_mfma_f32_16x16x32_bf16 v[50:53], v[168:171], v[200:203], v[50:53]
	v_mfma_f32_16x16x32_bf16 v[42:45], v[176:179], v[200:203], v[42:45]
	v_mfma_f32_16x16x32_bf16 v[34:37], v[168:171], v[208:211], v[34:37]
	v_mfma_f32_16x16x32_bf16 v[26:29], v[176:179], v[208:211], v[26:29]
	v_mfma_f32_16x16x32_bf16 v[18:21], v[168:171], v[216:219], v[18:21]
	v_mfma_f32_16x16x32_bf16 v[10:13], v[176:179], v[216:219], v[10:13]
	v_mfma_f32_16x16x32_bf16 v[6:9], v[168:171], v[232:235], v[6:9]
	v_mfma_f32_16x16x32_bf16 v[2:5], v[176:179], v[232:235], v[2:5]
	s_setprio 0
	s_barrier
	s_add_i32 s14, 0, 0x18000
	s_add_i32 s15, 0, 0x1c000
	v_add_u32_e32 v160, s14, v145
	v_add_u32_e32 v176, s15, v145
	ds_read_b128 v[130:133], v160
	ds_read_b128 v[152:155], v160 offset:1024
	ds_read_b128 v[156:159], v160 offset:2048
	ds_read_b128 v[160:163], v160 offset:3072
	ds_read_b128 v[164:167], v176
	ds_read_b128 v[168:171], v176 offset:1024
	ds_read_b128 v[172:175], v176 offset:2048
	ds_read_b128 v[176:179], v176 offset:3072
	s_add_u32 s40, s40, 0x80000
	s_addc_u32 s41, s41, 0
	s_mov_b32 m0, s46
	v_lshl_add_u64 v[242:243], s[40:41], 0, v[140:141]
	ds_read_b128 v[180:183], v147 offset:32768
	ds_read_b128 v[200:203], v147 offset:33792
	ds_read_b128 v[204:207], v147 offset:34816
	ds_read_b128 v[208:211], v147 offset:35840
	ds_read_b128 v[212:215], v147 offset:36864
	ds_read_b128 v[216:219], v147 offset:37888
	ds_read_b128 v[220:223], v147 offset:38912
	ds_read_b128 v[232:235], v147 offset:39936
	global_load_lds_dwordx4 v[242:243], off
	v_lshl_add_u64 v[242:243], s[40:41], 0, v[136:137]
	s_mov_b32 m0, s47
	s_nop 0
	global_load_lds_dwordx4 v[242:243], off
	s_waitcnt vmcnt(8)
	s_waitcnt lgkmcnt(0)
	s_barrier
	s_setprio 1
	s_waitcnt lgkmcnt(0)
	v_mfma_f32_16x16x32_bf16 v[126:129], v[130:133], v[180:183], v[126:129]
	v_mfma_f32_16x16x32_bf16 v[122:125], v[156:159], v[180:183], v[122:125]
	v_mfma_f32_16x16x32_bf16 v[118:121], v[130:133], v[204:207], v[118:121]
	v_mfma_f32_16x16x32_bf16 v[110:113], v[156:159], v[204:207], v[110:113]
	v_mfma_f32_16x16x32_bf16 v[102:105], v[130:133], v[212:215], v[102:105]
	v_mfma_f32_16x16x32_bf16 v[94:97], v[156:159], v[212:215], v[94:97]
	v_mfma_f32_16x16x32_bf16 v[86:89], v[130:133], v[220:223], v[86:89]
	v_mfma_f32_16x16x32_bf16 v[78:81], v[156:159], v[220:223], v[78:81]
	s_setprio 0
	s_setprio 1
	v_mfma_f32_16x16x32_bf16 v[126:129], v[152:155], v[200:203], v[126:129]
	v_mfma_f32_16x16x32_bf16 v[122:125], v[160:163], v[200:203], v[122:125]
	v_mfma_f32_16x16x32_bf16 v[118:121], v[152:155], v[208:211], v[118:121]
	v_mfma_f32_16x16x32_bf16 v[110:113], v[160:163], v[208:211], v[110:113]
	v_mfma_f32_16x16x32_bf16 v[102:105], v[152:155], v[216:219], v[102:105]
	v_mfma_f32_16x16x32_bf16 v[94:97], v[160:163], v[216:219], v[94:97]
	v_mfma_f32_16x16x32_bf16 v[86:89], v[152:155], v[232:235], v[86:89]
	v_mfma_f32_16x16x32_bf16 v[78:81], v[160:163], v[232:235], v[78:81]
	s_setprio 0
	s_setprio 1
	v_mfma_f32_16x16x32_bf16 v[114:117], v[164:167], v[180:183], v[114:117]
	v_mfma_f32_16x16x32_bf16 v[106:109], v[172:175], v[180:183], v[106:109]
	v_mfma_f32_16x16x32_bf16 v[98:101], v[164:167], v[204:207], v[98:101]
	v_mfma_f32_16x16x32_bf16 v[90:93], v[172:175], v[204:207], v[90:93]
	v_mfma_f32_16x16x32_bf16 v[82:85], v[164:167], v[212:215], v[82:85]
	v_mfma_f32_16x16x32_bf16 v[74:77], v[172:175], v[212:215], v[74:77]
	v_mfma_f32_16x16x32_bf16 v[70:73], v[164:167], v[220:223], v[70:73]
	v_mfma_f32_16x16x32_bf16 v[66:69], v[172:175], v[220:223], v[66:69]
	s_setprio 0
	s_setprio 1
	v_mfma_f32_16x16x32_bf16 v[114:117], v[168:171], v[200:203], v[114:117]
	v_mfma_f32_16x16x32_bf16 v[106:109], v[176:179], v[200:203], v[106:109]
	v_mfma_f32_16x16x32_bf16 v[98:101], v[168:171], v[208:211], v[98:101]
	v_mfma_f32_16x16x32_bf16 v[90:93], v[176:179], v[208:211], v[90:93]
	v_mfma_f32_16x16x32_bf16 v[82:85], v[168:171], v[216:219], v[82:85]
	v_mfma_f32_16x16x32_bf16 v[74:77], v[176:179], v[216:219], v[74:77]
	v_mfma_f32_16x16x32_bf16 v[70:73], v[168:171], v[232:235], v[70:73]
	v_mfma_f32_16x16x32_bf16 v[66:69], v[176:179], v[232:235], v[66:69]
	s_setprio 0
	s_barrier
; #define PG8_STAGE(bufoff, gbase, voff) do { _Pragma("unroll") for (int _i = 0; _i < 2; ++_i) \
;         __builtin_amdgcn_global_load_lds((const unsigned*)((const char*)(gbase) + (voff)[_i]), (LAS unsigned*)(lds + (bufoff) + ldsw + _i * 8192), 16, 0, 0); } while (0)
; #define PG8_LDA(dst, b, h) do { _Pragma("unroll") for (int m = 0; m < 4; ++m) _Pragma("unroll") for (int k = 0; k < 2; ++k) dst[m][k] = *(const LAS bf16x8*)(lds + PG8_SA(b, h) + aoff + m * 2048 + k * 1024); } while (0)
; #define PG8_MMA(ai, bj, At, Bt) do { __builtin_amdgcn_s_setprio(1); _Pragma("unroll") for (int m = 0; m < 4; ++m) _Pragma("unroll") for (int n = 0; n < 2; ++n) _Pragma("unroll") for (int k = 0; k < 2; ++k) \
;         acc[ai][bj][m][n] = __builtin_amdgcn_mfma_f32_16x16x32_bf16(Bt[n][k], At[m][k], acc[ai][bj][m][n], 0, 0, 0); __builtin_amdgcn_s_setprio(0); } while (0)
; #define PG8_WAIT_V(n) asm volatile("s_waitcnt vmcnt(" #n ")" ::: "memory")
; #define PG8_WAIT_L(n) asm volatile("s_waitcnt lgkmcnt(" #n ")" ::: "memory")
; #define PG8_BAR __builtin_amdgcn_s_barrier()
; #define PG8_SCHED __builtin_amdgcn_sched_barrier(0)
; template <class Epi, class Sched>
; __device__ __forceinline__ void gemm_phase(LAS unsigned char* lds, const Gemm g, const Sched& S, const Epi& E, const int tid, unsigned* last_sig = nullptr) {
;     ...
;             PG8_LDA(At, 1, 1); PG8_STAGE(PG8_SB(1, 0), b3, voffB); PG8_STAGE(PG8_SB(1, 1), b3 + hstep, voffB); PG8_STAGE(PG8_SA(1, 0), a3, voffA);
;             PG8_WAIT_V(8); PG8_WAIT_L(0); PG8_BAR; PG8_MMA(1, 0, At, B0); PG8_MMA(1, 1, At, B1); PG8_BAR; PG8_SCHED;
;         }
;         if (wr == 0) PG8_BAR;
	s_add_i32 s14, s14, s43
	v_lshl_add_u64 v[184:185], v[184:185], 0, s[34:35]
	s_mov_b32 m0, s14
	ds_read_b128 v[180:183], v147 offset:49152
	ds_read_b128 v[200:203], v147 offset:50176
	ds_read_b128 v[204:207], v147 offset:51200
	ds_read_b128 v[208:211], v147 offset:52224
	ds_read_b128 v[212:215], v147 offset:53248
	ds_read_b128 v[216:219], v147 offset:54272
	ds_read_b128 v[220:223], v147 offset:55296
	ds_read_b128 v[232:235], v147 offset:56320
	global_load_lds_dwordx4 v[184:185], off
	s_add_i32 m0, s14, 0x2000
	s_add_u32 s22, s22, 0x80080
	v_lshl_add_u64 v[184:185], v[236:237], 0, s[34:35]
	s_addc_u32 s23, s23, 0
	s_add_i32 s14, s15, s43
	global_load_lds_dwordx4 v[184:185], off
	v_lshl_add_u64 v[184:185], s[22:23], 0, v[138:139]
	s_mov_b32 m0, s14
	s_nop 0
	global_load_lds_dwordx4 v[184:185], off
	v_lshl_add_u64 v[184:185], s[22:23], 0, v[134:135]
	s_add_i32 m0, s14, 0x2000
	s_nop 0
	global_load_lds_dwordx4 v[184:185], off
	v_lshl_add_u64 v[184:185], v[238:239], 0, s[34:35]
	s_mov_b32 m0, s49
	s_nop 0
	global_load_lds_dwordx4 v[184:185], off
	v_lshl_add_u64 v[184:185], v[240:241], 0, s[34:35]
	s_mov_b32 m0, s50
	s_nop 0
	global_load_lds_dwordx4 v[184:185], off
	s_waitcnt vmcnt(8)
	s_waitcnt lgkmcnt(0)
	s_barrier
	s_setprio 1
	s_waitcnt lgkmcnt(0)
	v_mfma_f32_16x16x32_bf16 v[62:65], v[130:133], v[180:183], v[62:65]
	v_mfma_f32_16x16x32_bf16 v[58:61], v[156:159], v[180:183], v[58:61]
	v_mfma_f32_16x16x32_bf16 v[54:57], v[130:133], v[204:207], v[54:57]
	v_mfma_f32_16x16x32_bf16 v[46:49], v[156:159], v[204:207], v[46:49]
	v_mfma_f32_16x16x32_bf16 v[38:41], v[130:133], v[212:215], v[38:41]
	v_mfma_f32_16x16x32_bf16 v[30:33], v[156:159], v[212:215], v[30:33]
	v_mfma_f32_16x16x32_bf16 v[22:25], v[130:133], v[220:223], v[22:25]
	v_mfma_f32_16x16x32_bf16 v[14:17], v[156:159], v[220:223], v[14:17]
	s_setprio 0
	s_setprio 1
	v_mfma_f32_16x16x32_bf16 v[62:65], v[152:155], v[200:203], v[62:65]
	v_mfma_f32_16x16x32_bf16 v[58:61], v[160:163], v[200:203], v[58:61]
	v_mfma_f32_16x16x32_bf16 v[54:57], v[152:155], v[208:211], v[54:57]
	v_mfma_f32_16x16x32_bf16 v[46:49], v[160:163], v[208:211], v[46:49]
	v_mfma_f32_16x16x32_bf16 v[38:41], v[152:155], v[216:219], v[38:41]
	v_mfma_f32_16x16x32_bf16 v[30:33], v[160:163], v[216:219], v[30:33]
	v_mfma_f32_16x16x32_bf16 v[22:25], v[152:155], v[232:235], v[22:25]
	v_mfma_f32_16x16x32_bf16 v[14:17], v[160:163], v[232:235], v[14:17]
	s_setprio 0
	s_setprio 1
	v_mfma_f32_16x16x32_bf16 v[50:53], v[164:167], v[180:183], v[50:53]
	v_mfma_f32_16x16x32_bf16 v[42:45], v[172:175], v[180:183], v[42:45]
	v_mfma_f32_16x16x32_bf16 v[34:37], v[164:167], v[204:207], v[34:37]
	v_mfma_f32_16x16x32_bf16 v[26:29], v[172:175], v[204:207], v[26:29]
	v_mfma_f32_16x16x32_bf16 v[18:21], v[164:167], v[212:215], v[18:21]
	v_mfma_f32_16x16x32_bf16 v[10:13], v[172:175], v[212:215], v[10:13]
	v_mfma_f32_16x16x32_bf16 v[6:9], v[164:167], v[220:223], v[6:9]
	v_mfma_f32_16x16x32_bf16 v[2:5], v[172:175], v[220:223], v[2:5]
	s_setprio 0
	s_setprio 1
	v_mfma_f32_16x16x32_bf16 v[50:53], v[168:171], v[200:203], v[50:53]
	v_mfma_f32_16x16x32_bf16 v[42:45], v[176:179], v[200:203], v[42:45]
	v_mfma_f32_16x16x32_bf16 v[34:37], v[168:171], v[208:211], v[34:37]
	v_mfma_f32_16x16x32_bf16 v[26:29], v[176:179], v[208:211], v[26:29]
	v_mfma_f32_16x16x32_bf16 v[18:21], v[168:171], v[216:219], v[18:21]
	v_mfma_f32_16x16x32_bf16 v[10:13], v[176:179], v[216:219], v[10:13]
	v_mfma_f32_16x16x32_bf16 v[6:9], v[168:171], v[232:235], v[6:9]
	v_mfma_f32_16x16x32_bf16 v[2:5], v[176:179], v[232:235], v[2:5]
	s_setprio 0
	s_barrier
	s_add_i32 s59, s59, 2
	s_add_u32 s20, s20, 0x100
	s_addc_u32 s21, s21, 0
	s_add_u32 s57, s57, 0x100
	s_addc_u32 s58, s58, 0
	s_cmp_gt_u32 s59, 29
	s_cbranch_scc0 .LBB0_172
	s_and_b64 vcc, exec, s[8:9]
	s_cbranch_vccnz .LBB0_177
	s_cmp_gt_i32 s54, 3
	s_mov_b64 s[20:21], -1
	s_cbranch_scc1 .LBB0_178

; #define PG8_STAGE(bufoff, gbase, voff) do { _Pragma("unroll") for (int _i = 0; _i < 2; ++_i) \
;         __builtin_amdgcn_global_load_lds((const unsigned*)((const char*)(gbase) + (voff)[_i]), (LAS unsigned*)(lds + (bufoff) + ldsw + _i * 8192), 16, 0, 0); } while (0)
; #define PG8_LDA(dst, b, h) do { _Pragma("unroll") for (int m = 0; m < 4; ++m) _Pragma("unroll") for (int k = 0; k < 2; ++k) dst[m][k] = *(const LAS bf16x8*)(lds + PG8_SA(b, h) + aoff + m * 2048 + k * 1024); } while (0)
; #define PG8_LDB(dst, b, h) do { _Pragma("unroll") for (int n = 0; n < 2; ++n) _Pragma("unroll") for (int k = 0; k < 2; ++k) dst[n][k] = *(const LAS bf16x8*)(lds + PG8_SB(b, h) + boff + n * 2048 + k * 1024); } while (0)
; #define PG8_MMA(ai, bj, At, Bt) do { __builtin_amdgcn_s_setprio(1); _Pragma("unroll") for (int m = 0; m < 4; ++m) _Pragma("unroll") for (int n = 0; n < 2; ++n) _Pragma("unroll") for (int k = 0; k < 2; ++k) \
;         acc[ai][bj][m][n] = __builtin_amdgcn_mfma_f32_16x16x32_bf16(Bt[n][k], At[m][k], acc[ai][bj][m][n], 0, 0, 0); __builtin_amdgcn_s_setprio(0); } while (0)
; #define PG8_WAIT_V(n) asm volatile("s_waitcnt vmcnt(" #n ")" ::: "memory")
; #define PG8_WAIT_L(n) asm volatile("s_waitcnt lgkmcnt(" #n ")" ::: "memory")
; #define PG8_BAR __builtin_amdgcn_s_barrier()
; template <class Epi, class Sched>
; __device__ __forceinline__ void gemm_phase(LAS unsigned char* lds, const Gemm g, const Sched& S, const Epi& E, const int tid, unsigned* last_sig = nullptr) {
;     ...
;         for (int t = 0; t < nt; t += 2) {
;             const bool last = (t == nt - 2);
;             const char* a1 = cA + (size_t)(t + 1) * kstep;
;             const char* a2 = last ? nA : cA + (size_t)(t + 2) * kstep; const char* b2 = last ? nB : cB + (size_t)(t + 2) * kstep;
;             const char* a3 = a2 + kstep; const char* b3 = b2 + kstep;
;             PG8_LDB(B0, 0, 0); PG8_LDB(B1, 0, 1); PG8_SCHED; PG8_LDA(At, 0, 0); PG8_STAGE(PG8_SA(1, 1), a1 + hstep, voffA);
;             PG8_WAIT_V(8); PG8_WAIT_L(0); PG8_BAR; PG8_MMA(0, 0, At, B0); PG8_MMA(0, 1, At, B1); PG8_BAR; PG8_SCHED;
;             PG8_LDA(At, 0, 1); PG8_STAGE(PG8_SB(0, 0), b2, voffB); PG8_STAGE(PG8_SB(0, 1), b2 + hstep, voffB); PG8_STAGE(PG8_SA(0, 0), a2, voffA);
;             PG8_WAIT_V(8); PG8_WAIT_L(0); PG8_BAR; PG8_MMA(1, 0, At, B0); PG8_MMA(1, 1, At, B1); PG8_BAR; PG8_SCHED;
.LBB0_334:
	s_add_u32 s6, s42, s4
	s_addc_u32 s7, s43, s5
	s_add_u32 s6, s6, 0x4cd67100
	s_addc_u32 s7, s7, 0
	s_add_u32 s14, s22, s4
	s_addc_u32 s15, s23, s5
	s_add_i32 s31, 0, 0x10000
	s_cmpk_eq_i32 s4, 0xf00
	s_cselect_b32 s9, s41, s7
	s_cselect_b32 s8, s40, s6
	v_add_u32_e32 v55, s31, v53
	s_cselect_b32 s7, s1, s15
	s_cselect_b32 s6, s0, s14
	s_add_i32 s14, 0, 0x14000
	ds_read_b128 v[148:151], v55
	ds_read_b128 v[154:157], v55 offset:1024
	ds_read_b128 v[158:161], v55 offset:2048
	ds_read_b128 v[162:165], v55 offset:3072
	v_add_u32_e32 v55, s14, v53
	ds_read_b128 v[166:169], v55
	ds_read_b128 v[170:173], v55 offset:1024
	ds_read_b128 v[174:177], v55 offset:2048
	ds_read_b128 v[178:181], v55 offset:3072
	v_lshl_add_u64 v[56:57], v[48:49], 0, s[4:5]
	s_add_i32 m0, s12, 0xc000
	ds_read_b128 v[182:185], v54
	ds_read_b128 v[200:203], v54 offset:1024
	ds_read_b128 v[204:207], v54 offset:2048
	ds_read_b128 v[208:211], v54 offset:3072
	ds_read_b128 v[212:215], v54 offset:4096
	ds_read_b128 v[216:219], v54 offset:5120
	ds_read_b128 v[220:223], v54 offset:6144
	ds_read_b128 v[232:235], v54 offset:7168
	global_load_lds_dwordx4 v[56:57], off
	v_lshl_add_u64 v[56:57], v[50:51], 0, s[4:5]
	s_add_i32 m0, s12, 0xe000
	s_nop 0
	global_load_lds_dwordx4 v[56:57], off
	s_waitcnt vmcnt(8)
	s_waitcnt lgkmcnt(0)
	s_barrier
	s_setprio 1
	s_waitcnt lgkmcnt(0)
	v_mfma_f32_16x16x32_bf16 v[142:145], v[148:151], v[182:185], v[142:145]
	v_mfma_f32_16x16x32_bf16 v[138:141], v[158:161], v[182:185], v[138:141]
	v_mfma_f32_16x16x32_bf16 v[126:129], v[148:151], v[204:207], v[126:129]
	v_mfma_f32_16x16x32_bf16 v[122:125], v[158:161], v[204:207], v[122:125]
	v_mfma_f32_16x16x32_bf16 v[110:113], v[148:151], v[212:215], v[110:113]
	v_mfma_f32_16x16x32_bf16 v[106:109], v[158:161], v[212:215], v[106:109]
	v_mfma_f32_16x16x32_bf16 v[94:97], v[148:151], v[220:223], v[94:97]
	v_mfma_f32_16x16x32_bf16 v[90:93], v[158:161], v[220:223], v[90:93]
	s_setprio 0
	s_setprio 1
	v_mfma_f32_16x16x32_bf16 v[142:145], v[154:157], v[200:203], v[142:145]
	v_mfma_f32_16x16x32_bf16 v[138:141], v[162:165], v[200:203], v[138:141]
	v_mfma_f32_16x16x32_bf16 v[126:129], v[154:157], v[208:211], v[126:129]
	v_mfma_f32_16x16x32_bf16 v[122:125], v[162:165], v[208:211], v[122:125]
	v_mfma_f32_16x16x32_bf16 v[110:113], v[154:157], v[216:219], v[110:113]
	v_mfma_f32_16x16x32_bf16 v[106:109], v[162:165], v[216:219], v[106:109]
	v_mfma_f32_16x16x32_bf16 v[94:97], v[154:157], v[232:235], v[94:97]
	v_mfma_f32_16x16x32_bf16 v[90:93], v[162:165], v[232:235], v[90:93]
	s_setprio 0
	s_setprio 1
	v_mfma_f32_16x16x32_bf16 v[134:137], v[166:169], v[182:185], v[134:137]
	v_mfma_f32_16x16x32_bf16 v[130:133], v[174:177], v[182:185], v[130:133]
	v_mfma_f32_16x16x32_bf16 v[118:121], v[166:169], v[204:207], v[118:121]
	v_mfma_f32_16x16x32_bf16 v[114:117], v[174:177], v[204:207], v[114:117]
	v_mfma_f32_16x16x32_bf16 v[102:105], v[166:169], v[212:215], v[102:105]
	v_mfma_f32_16x16x32_bf16 v[98:101], v[174:177], v[212:215], v[98:101]
	v_mfma_f32_16x16x32_bf16 v[86:89], v[166:169], v[220:223], v[86:89]
	v_mfma_f32_16x16x32_bf16 v[82:85], v[174:177], v[220:223], v[82:85]
	s_setprio 0
	s_setprio 1
	v_mfma_f32_16x16x32_bf16 v[134:137], v[170:173], v[200:203], v[134:137]
	v_mfma_f32_16x16x32_bf16 v[130:133], v[178:181], v[200:203], v[130:133]
	v_mfma_f32_16x16x32_bf16 v[118:121], v[170:173], v[208:211], v[118:121]
	v_mfma_f32_16x16x32_bf16 v[114:117], v[178:181], v[208:211], v[114:117]
	v_mfma_f32_16x16x32_bf16 v[102:105], v[170:173], v[216:219], v[102:105]
	v_mfma_f32_16x16x32_bf16 v[98:101], v[178:181], v[216:219], v[98:101]
	v_mfma_f32_16x16x32_bf16 v[86:89], v[170:173], v[232:235], v[86:89]
	v_mfma_f32_16x16x32_bf16 v[82:85], v[178:181], v[232:235], v[82:85]
	s_setprio 0
	s_barrier
	s_add_i32 s15, s31, s11
	v_lshl_add_u64 v[236:237], s[6:7], 0, v[186:187]
	s_mov_b32 m0, s15
	ds_read_b128 v[182:185], v54 offset:16384
	ds_read_b128 v[200:203], v54 offset:17408
	ds_read_b128 v[204:207], v54 offset:18432
	ds_read_b128 v[208:211], v54 offset:19456
	ds_read_b128 v[212:215], v54 offset:20480
	ds_read_b128 v[216:219], v54 offset:21504
	ds_read_b128 v[220:223], v54 offset:22528
	ds_read_b128 v[232:235], v54 offset:23552
	global_load_lds_dwordx4 v[236:237], off
	s_add_i32 m0, s15, 0x2000
	s_add_u32 s38, s6, 0x80000
	v_lshl_add_u64 v[238:239], s[6:7], 0, v[38:39]
	s_addc_u32 s39, s7, 0
	s_add_i32 s14, s14, s11
	global_load_lds_dwordx4 v[238:239], off
	v_lshl_add_u64 v[56:57], s[38:39], 0, v[186:187]
	s_mov_b32 m0, s14
	v_lshl_add_u64 v[240:241], s[8:9], 0, v[46:47]
	global_load_lds_dwordx4 v[56:57], off
	v_lshl_add_u64 v[56:57], s[38:39], 0, v[38:39]
	s_add_i32 m0, s14, 0x2000
	v_lshl_add_u64 v[242:243], s[8:9], 0, v[40:41]
	global_load_lds_dwordx4 v[56:57], off
	s_mov_b32 m0, s12
	s_nop 0
	global_load_lds_dwordx4 v[240:241], off
	s_mov_b32 m0, s13
	s_nop 0
	global_load_lds_dwordx4 v[242:243], off
	s_waitcnt vmcnt(8)
	s_waitcnt lgkmcnt(0)
	s_barrier
; #define PG8_STAGE(bufoff, gbase, voff) do { _Pragma("unroll") for (int _i = 0; _i < 2; ++_i) \
;         __builtin_amdgcn_global_load_lds((const unsigned*)((const char*)(gbase) + (voff)[_i]), (LAS unsigned*)(lds + (bufoff) + ldsw + _i * 8192), 16, 0, 0); } while (0)
; #define PG8_LDA(dst, b, h) do { _Pragma("unroll") for (int m = 0; m < 4; ++m) _Pragma("unroll") for (int k = 0; k < 2; ++k) dst[m][k] = *(const LAS bf16x8*)(lds + PG8_SA(b, h) + aoff + m * 2048 + k * 1024); } while (0)
; #define PG8_LDB(dst, b, h) do { _Pragma("unroll") for (int n = 0; n < 2; ++n) _Pragma("unroll") for (int k = 0; k < 2; ++k) dst[n][k] = *(const LAS bf16x8*)(lds + PG8_SB(b, h) + boff + n * 2048 + k * 1024); } while (0)
; #define PG8_MMA(ai, bj, At, Bt) do { __builtin_amdgcn_s_setprio(1); _Pragma("unroll") for (int m = 0; m < 4; ++m) _Pragma("unroll") for (int n = 0; n < 2; ++n) _Pragma("unroll") for (int k = 0; k < 2; ++k) \
;         acc[ai][bj][m][n] = __builtin_amdgcn_mfma_f32_16x16x32_bf16(Bt[n][k], At[m][k], acc[ai][bj][m][n], 0, 0, 0); __builtin_amdgcn_s_setprio(0); } while (0)
; #define PG8_WAIT_V(n) asm volatile("s_waitcnt vmcnt(" #n ")" ::: "memory")
; #define PG8_WAIT_L(n) asm volatile("s_waitcnt lgkmcnt(" #n ")" ::: "memory")
; #define PG8_BAR __builtin_amdgcn_s_barrier()
; #define PG8_SCHED __builtin_amdgcn_sched_barrier(0)
; template <class Epi, class Sched>
; __device__ __forceinline__ void gemm_phase(LAS unsigned char* lds, const Gemm g, const Sched& S, const Epi& E, const int tid, unsigned* last_sig = nullptr) {
;     ...
;             PG8_WAIT_V(8); PG8_WAIT_L(0); PG8_BAR; PG8_MMA(1, 0, At, B0); PG8_MMA(1, 1, At, B1); PG8_BAR; PG8_SCHED;
;             PG8_LDB(B0, 1, 0); PG8_LDB(B1, 1, 1); PG8_SCHED; PG8_LDA(At, 1, 0); PG8_STAGE(PG8_SA(0, 1), a2 + hstep, voffA);
;             PG8_WAIT_V(8); PG8_WAIT_L(0); PG8_BAR; PG8_MMA(0, 0, At, B0); PG8_MMA(0, 1, At, B1); PG8_BAR; PG8_SCHED;
	s_setprio 1
	s_waitcnt lgkmcnt(0)
	v_mfma_f32_16x16x32_bf16 v[78:81], v[148:151], v[182:185], v[78:81]
	v_mfma_f32_16x16x32_bf16 v[74:77], v[158:161], v[182:185], v[74:77]
	v_mfma_f32_16x16x32_bf16 v[62:65], v[148:151], v[204:207], v[62:65]
	v_mfma_f32_16x16x32_bf16 v[56:59], v[158:161], v[204:207], v[58:61]
	v_mfma_f32_16x16x32_bf16 v[30:33], v[148:151], v[212:215], v[30:33]
	v_mfma_f32_16x16x32_bf16 v[26:29], v[158:161], v[212:215], v[26:29]
	v_mfma_f32_16x16x32_bf16 v[14:17], v[148:151], v[220:223], v[14:17]
	v_mfma_f32_16x16x32_bf16 v[10:13], v[158:161], v[220:223], v[10:13]
	s_setprio 0
	s_setprio 1
	v_mfma_f32_16x16x32_bf16 v[78:81], v[154:157], v[200:203], v[78:81]
	v_mfma_f32_16x16x32_bf16 v[74:77], v[162:165], v[200:203], v[74:77]
	v_mfma_f32_16x16x32_bf16 v[62:65], v[154:157], v[208:211], v[62:65]
	v_mfma_f32_16x16x32_bf16 v[56:59], v[162:165], v[208:211], v[56:59]
	v_mfma_f32_16x16x32_bf16 v[30:33], v[154:157], v[216:219], v[30:33]
	v_mfma_f32_16x16x32_bf16 v[26:29], v[162:165], v[216:219], v[26:29]
	v_mfma_f32_16x16x32_bf16 v[14:17], v[154:157], v[232:235], v[14:17]
	v_mfma_f32_16x16x32_bf16 v[10:13], v[162:165], v[232:235], v[10:13]
	s_setprio 0
	s_setprio 1
	v_mfma_f32_16x16x32_bf16 v[70:73], v[166:169], v[182:185], v[70:73]
	v_mfma_f32_16x16x32_bf16 v[66:69], v[174:177], v[182:185], v[66:69]
	v_mfma_f32_16x16x32_bf16 v[42:45], v[166:169], v[204:207], v[42:45]
	v_mfma_f32_16x16x32_bf16 v[34:37], v[174:177], v[204:207], v[34:37]
	v_mfma_f32_16x16x32_bf16 v[22:25], v[166:169], v[212:215], v[22:25]
	v_mfma_f32_16x16x32_bf16 v[18:21], v[174:177], v[212:215], v[18:21]
	v_mfma_f32_16x16x32_bf16 v[6:9], v[166:169], v[220:223], v[6:9]
	v_mfma_f32_16x16x32_bf16 v[2:5], v[174:177], v[220:223], v[2:5]
	s_setprio 0
	s_setprio 1
	v_mfma_f32_16x16x32_bf16 v[70:73], v[170:173], v[200:203], v[70:73]
	v_mfma_f32_16x16x32_bf16 v[66:69], v[178:181], v[200:203], v[66:69]
	v_mfma_f32_16x16x32_bf16 v[42:45], v[170:173], v[208:211], v[42:45]
	v_mfma_f32_16x16x32_bf16 v[34:37], v[178:181], v[208:211], v[34:37]
	v_mfma_f32_16x16x32_bf16 v[22:25], v[170:173], v[216:219], v[22:25]
	v_mfma_f32_16x16x32_bf16 v[18:21], v[178:181], v[216:219], v[18:21]
	v_mfma_f32_16x16x32_bf16 v[6:9], v[170:173], v[232:235], v[6:9]
	v_mfma_f32_16x16x32_bf16 v[2:5], v[178:181], v[232:235], v[2:5]
	s_setprio 0
	s_barrier
	s_add_i32 s14, 0, 0x18000
	v_add_u32_e32 v55, s14, v53
	s_add_i32 s15, 0, 0x1c000
	ds_read_b128 v[148:151], v55
	ds_read_b128 v[154:157], v55 offset:1024
	ds_read_b128 v[158:161], v55 offset:2048
	ds_read_b128 v[162:165], v55 offset:3072
	v_add_u32_e32 v55, s15, v53
	ds_read_b128 v[166:169], v55
	ds_read_b128 v[170:173], v55 offset:1024
	ds_read_b128 v[174:177], v55 offset:2048
	ds_read_b128 v[178:181], v55 offset:3072
	s_add_u32 s8, s8, 0x80000
	s_addc_u32 s9, s9, 0
	s_mov_b32 m0, s16
	v_lshl_add_u64 v[60:61], s[8:9], 0, v[46:47]
	ds_read_b128 v[182:185], v54 offset:32768
	ds_read_b128 v[200:203], v54 offset:33792
	ds_read_b128 v[204:207], v54 offset:34816
	ds_read_b128 v[208:211], v54 offset:35840
	ds_read_b128 v[212:215], v54 offset:36864
	ds_read_b128 v[216:219], v54 offset:37888
	ds_read_b128 v[220:223], v54 offset:38912
	ds_read_b128 v[232:235], v54 offset:39936
	global_load_lds_dwordx4 v[60:61], off
	v_lshl_add_u64 v[60:61], s[8:9], 0, v[40:41]
	s_mov_b32 m0, s17
	s_nop 0
	global_load_lds_dwordx4 v[60:61], off
	s_waitcnt vmcnt(8)
	s_waitcnt lgkmcnt(0)
	s_barrier
	s_setprio 1
	s_waitcnt lgkmcnt(0)
	v_mfma_f32_16x16x32_bf16 v[142:145], v[148:151], v[182:185], v[142:145]
	v_mfma_f32_16x16x32_bf16 v[138:141], v[158:161], v[182:185], v[138:141]
	v_mfma_f32_16x16x32_bf16 v[126:129], v[148:151], v[204:207], v[126:129]
	v_mfma_f32_16x16x32_bf16 v[122:125], v[158:161], v[204:207], v[122:125]
	v_mfma_f32_16x16x32_bf16 v[110:113], v[148:151], v[212:215], v[110:113]
	v_mfma_f32_16x16x32_bf16 v[106:109], v[158:161], v[212:215], v[106:109]
	v_mfma_f32_16x16x32_bf16 v[94:97], v[148:151], v[220:223], v[94:97]
	v_mfma_f32_16x16x32_bf16 v[90:93], v[158:161], v[220:223], v[90:93]
	s_setprio 0
	s_setprio 1
	v_mfma_f32_16x16x32_bf16 v[142:145], v[154:157], v[200:203], v[142:145]
	v_mfma_f32_16x16x32_bf16 v[138:141], v[162:165], v[200:203], v[138:141]
	v_mfma_f32_16x16x32_bf16 v[126:129], v[154:157], v[208:211], v[126:129]
	v_mfma_f32_16x16x32_bf16 v[122:125], v[162:165], v[208:211], v[122:125]
	v_mfma_f32_16x16x32_bf16 v[110:113], v[154:157], v[216:219], v[110:113]
	v_mfma_f32_16x16x32_bf16 v[106:109], v[162:165], v[216:219], v[106:109]
	v_mfma_f32_16x16x32_bf16 v[94:97], v[154:157], v[232:235], v[94:97]
	v_mfma_f32_16x16x32_bf16 v[90:93], v[162:165], v[232:235], v[90:93]
	s_setprio 0
	s_setprio 1
	v_mfma_f32_16x16x32_bf16 v[134:137], v[166:169], v[182:185], v[134:137]
	v_mfma_f32_16x16x32_bf16 v[130:133], v[174:177], v[182:185], v[130:133]
	v_mfma_f32_16x16x32_bf16 v[118:121], v[166:169], v[204:207], v[118:121]
	v_mfma_f32_16x16x32_bf16 v[114:117], v[174:177], v[204:207], v[114:117]
	v_mfma_f32_16x16x32_bf16 v[102:105], v[166:169], v[212:215], v[102:105]
	v_mfma_f32_16x16x32_bf16 v[98:101], v[174:177], v[212:215], v[98:101]
	v_mfma_f32_16x16x32_bf16 v[86:89], v[166:169], v[220:223], v[86:89]
	v_mfma_f32_16x16x32_bf16 v[82:85], v[174:177], v[220:223], v[82:85]
	s_setprio 0
	s_setprio 1
	v_mfma_f32_16x16x32_bf16 v[134:137], v[170:173], v[200:203], v[134:137]
	v_mfma_f32_16x16x32_bf16 v[130:133], v[178:181], v[200:203], v[130:133]
	v_mfma_f32_16x16x32_bf16 v[118:121], v[170:173], v[208:211], v[118:121]
	v_mfma_f32_16x16x32_bf16 v[114:117], v[178:181], v[208:211], v[114:117]
	v_mfma_f32_16x16x32_bf16 v[102:105], v[170:173], v[216:219], v[102:105]
	v_mfma_f32_16x16x32_bf16 v[98:101], v[178:181], v[216:219], v[98:101]
	v_mfma_f32_16x16x32_bf16 v[86:89], v[170:173], v[232:235], v[86:89]
	v_mfma_f32_16x16x32_bf16 v[82:85], v[178:181], v[232:235], v[82:85]
	s_setprio 0
	s_barrier
; #define PG8_STAGE(bufoff, gbase, voff) do { _Pragma("unroll") for (int _i = 0; _i < 2; ++_i) \
;         __builtin_amdgcn_global_load_lds((const unsigned*)((const char*)(gbase) + (voff)[_i]), (LAS unsigned*)(lds + (bufoff) + ldsw + _i * 8192), 16, 0, 0); } while (0)
; #define PG8_LDA(dst, b, h) do { _Pragma("unroll") for (int m = 0; m < 4; ++m) _Pragma("unroll") for (int k = 0; k < 2; ++k) dst[m][k] = *(const LAS bf16x8*)(lds + PG8_SA(b, h) + aoff + m * 2048 + k * 1024); } while (0)
; #define PG8_MMA(ai, bj, At, Bt) do { __builtin_amdgcn_s_setprio(1); _Pragma("unroll") for (int m = 0; m < 4; ++m) _Pragma("unroll") for (int n = 0; n < 2; ++n) _Pragma("unroll") for (int k = 0; k < 2; ++k) \
;         acc[ai][bj][m][n] = __builtin_amdgcn_mfma_f32_16x16x32_bf16(Bt[n][k], At[m][k], acc[ai][bj][m][n], 0, 0, 0); __builtin_amdgcn_s_setprio(0); } while (0)
; #define PG8_WAIT_V(n) asm volatile("s_waitcnt vmcnt(" #n ")" ::: "memory")
; #define PG8_WAIT_L(n) asm volatile("s_waitcnt lgkmcnt(" #n ")" ::: "memory")
; #define PG8_BAR __builtin_amdgcn_s_barrier()
; #define PG8_SCHED __builtin_amdgcn_sched_barrier(0)
; template <class Epi, class Sched>
; __device__ __forceinline__ void gemm_phase(LAS unsigned char* lds, const Gemm g, const Sched& S, const Epi& E, const int tid, unsigned* last_sig = nullptr) {
;     ...
;             PG8_LDA(At, 1, 1); PG8_STAGE(PG8_SB(1, 0), b3, voffB); PG8_STAGE(PG8_SB(1, 1), b3 + hstep, voffB); PG8_STAGE(PG8_SA(1, 0), a3, voffA);
;             PG8_WAIT_V(8); PG8_WAIT_L(0); PG8_BAR; PG8_MMA(1, 0, At, B0); PG8_MMA(1, 1, At, B1); PG8_BAR; PG8_SCHED;
;         }
;         if (wr == 0) PG8_BAR;
	s_add_i32 s8, s14, s11
	v_lshl_add_u64 v[60:61], v[236:237], 0, s[34:35]
	s_mov_b32 m0, s8
	ds_read_b128 v[182:185], v54 offset:49152
	ds_read_b128 v[200:203], v54 offset:50176
	ds_read_b128 v[204:207], v54 offset:51200
	ds_read_b128 v[208:211], v54 offset:52224
	ds_read_b128 v[212:215], v54 offset:53248
	ds_read_b128 v[216:219], v54 offset:54272
	ds_read_b128 v[220:223], v54 offset:55296
	ds_read_b128 v[232:235], v54 offset:56320
	global_load_lds_dwordx4 v[60:61], off
	s_add_i32 m0, s8, 0x2000
	s_add_u32 s6, s6, 0x80080
	v_lshl_add_u64 v[60:61], v[238:239], 0, s[34:35]
	s_addc_u32 s7, s7, 0
	s_add_i32 s8, s15, s11
	global_load_lds_dwordx4 v[60:61], off
	v_lshl_add_u64 v[60:61], s[6:7], 0, v[186:187]
	s_mov_b32 m0, s8
	s_nop 0
	global_load_lds_dwordx4 v[60:61], off
	v_lshl_add_u64 v[60:61], s[6:7], 0, v[38:39]
	s_add_i32 m0, s8, 0x2000
	s_nop 0
	global_load_lds_dwordx4 v[60:61], off
	v_lshl_add_u64 v[60:61], v[240:241], 0, s[34:35]
	s_mov_b32 m0, s20
	s_nop 0
	global_load_lds_dwordx4 v[60:61], off
	v_lshl_add_u64 v[60:61], v[242:243], 0, s[34:35]
	s_mov_b32 m0, s21
	s_nop 0
	global_load_lds_dwordx4 v[60:61], off
	s_waitcnt vmcnt(8)
	s_waitcnt lgkmcnt(0)
	s_barrier
	s_setprio 1
	s_waitcnt lgkmcnt(0)
	v_mfma_f32_16x16x32_bf16 v[78:81], v[148:151], v[182:185], v[78:81]
	v_mfma_f32_16x16x32_bf16 v[74:77], v[158:161], v[182:185], v[74:77]
	v_mfma_f32_16x16x32_bf16 v[60:63], v[148:151], v[204:207], v[62:65]
	v_mfma_f32_16x16x32_bf16 v[56:59], v[158:161], v[204:207], v[56:59]
	v_mfma_f32_16x16x32_bf16 v[30:33], v[148:151], v[212:215], v[30:33]
	v_mfma_f32_16x16x32_bf16 v[26:29], v[158:161], v[212:215], v[26:29]
	v_mfma_f32_16x16x32_bf16 v[14:17], v[148:151], v[220:223], v[14:17]
	v_mfma_f32_16x16x32_bf16 v[10:13], v[158:161], v[220:223], v[10:13]
	s_setprio 0
	s_setprio 1
	v_mfma_f32_16x16x32_bf16 v[78:81], v[154:157], v[200:203], v[78:81]
	v_mfma_f32_16x16x32_bf16 v[74:77], v[162:165], v[200:203], v[74:77]
	v_mfma_f32_16x16x32_bf16 v[62:65], v[154:157], v[208:211], v[60:63]
	v_mfma_f32_16x16x32_bf16 v[58:61], v[162:165], v[208:211], v[56:59]
	v_mfma_f32_16x16x32_bf16 v[30:33], v[154:157], v[216:219], v[30:33]
	v_mfma_f32_16x16x32_bf16 v[26:29], v[162:165], v[216:219], v[26:29]
	v_mfma_f32_16x16x32_bf16 v[14:17], v[154:157], v[232:235], v[14:17]
	v_mfma_f32_16x16x32_bf16 v[10:13], v[162:165], v[232:235], v[10:13]
	s_setprio 0
	s_setprio 1
	v_mfma_f32_16x16x32_bf16 v[70:73], v[166:169], v[182:185], v[70:73]
	v_mfma_f32_16x16x32_bf16 v[66:69], v[174:177], v[182:185], v[66:69]
	v_mfma_f32_16x16x32_bf16 v[42:45], v[166:169], v[204:207], v[42:45]
	v_mfma_f32_16x16x32_bf16 v[34:37], v[174:177], v[204:207], v[34:37]
	v_mfma_f32_16x16x32_bf16 v[22:25], v[166:169], v[212:215], v[22:25]
	v_mfma_f32_16x16x32_bf16 v[18:21], v[174:177], v[212:215], v[18:21]
	v_mfma_f32_16x16x32_bf16 v[6:9], v[166:169], v[220:223], v[6:9]
	v_mfma_f32_16x16x32_bf16 v[2:5], v[174:177], v[220:223], v[2:5]
	s_setprio 0
	s_setprio 1
	v_mfma_f32_16x16x32_bf16 v[70:73], v[170:173], v[200:203], v[70:73]
	v_mfma_f32_16x16x32_bf16 v[66:69], v[178:181], v[200:203], v[66:69]
	v_mfma_f32_16x16x32_bf16 v[42:45], v[170:173], v[208:211], v[42:45]
	v_mfma_f32_16x16x32_bf16 v[34:37], v[178:181], v[208:211], v[34:37]
	v_mfma_f32_16x16x32_bf16 v[22:25], v[170:173], v[216:219], v[22:25]
	v_mfma_f32_16x16x32_bf16 v[18:21], v[178:181], v[216:219], v[18:21]
	v_mfma_f32_16x16x32_bf16 v[6:9], v[170:173], v[232:235], v[6:9]
	v_mfma_f32_16x16x32_bf16 v[2:5], v[178:181], v[232:235], v[2:5]
	s_setprio 0
	s_barrier
	s_add_i32 s28, s28, 2
	s_add_u32 s4, s4, 0x100
	s_addc_u32 s5, s5, 0
	s_cmp_gt_u32 s28, 29
	s_cbranch_scc0 .LBB0_334
	s_cmpk_lt_u32 s10, 0x100
	v_readlane_b32 s23, v255, 15
	s_cbranch_scc0 .LBB0_337
	s_barrier

; #define PG8_STAGE(bufoff, gbase, voff) do { _Pragma("unroll") for (int _i = 0; _i < 2; ++_i) \
;         __builtin_amdgcn_global_load_lds((const unsigned*)((const char*)(gbase) + (voff)[_i]), (LAS unsigned*)(lds + (bufoff) + ldsw + _i * 8192), 16, 0, 0); } while (0)
; #define PG8_LDA(dst, b, h) do { _Pragma("unroll") for (int m = 0; m < 4; ++m) _Pragma("unroll") for (int k = 0; k < 2; ++k) dst[m][k] = *(const LAS bf16x8*)(lds + PG8_SA(b, h) + aoff + m * 2048 + k * 1024); } while (0)
; #define PG8_LDB(dst, b, h) do { _Pragma("unroll") for (int n = 0; n < 2; ++n) _Pragma("unroll") for (int k = 0; k < 2; ++k) dst[n][k] = *(const LAS bf16x8*)(lds + PG8_SB(b, h) + boff + n * 2048 + k * 1024); } while (0)
; #define PG8_MMA(ai, bj, At, Bt) do { __builtin_amdgcn_s_setprio(1); _Pragma("unroll") for (int m = 0; m < 4; ++m) _Pragma("unroll") for (int n = 0; n < 2; ++n) _Pragma("unroll") for (int k = 0; k < 2; ++k) \
;         acc[ai][bj][m][n] = __builtin_amdgcn_mfma_f32_16x16x32_bf16(Bt[n][k], At[m][k], acc[ai][bj][m][n], 0, 0, 0); __builtin_amdgcn_s_setprio(0); } while (0)
; #define PG8_WAIT_V(n) asm volatile("s_waitcnt vmcnt(" #n ")" ::: "memory")
; #define PG8_WAIT_L(n) asm volatile("s_waitcnt lgkmcnt(" #n ")" ::: "memory")
; #define PG8_BAR __builtin_amdgcn_s_barrier()
; template <class Epi, class Sched>
; __device__ __forceinline__ void gemm_phase(LAS unsigned char* lds, const Gemm g, const Sched& S, const Epi& E, const int tid, unsigned* last_sig = nullptr) {
;     ...
;         for (int t = 0; t < nt; t += 2) {
;             const bool last = (t == nt - 2);
;             const char* a1 = cA + (size_t)(t + 1) * kstep;
;             const char* a2 = last ? nA : cA + (size_t)(t + 2) * kstep; const char* b2 = last ? nB : cB + (size_t)(t + 2) * kstep;
;             const char* a3 = a2 + kstep; const char* b3 = b2 + kstep;
;             PG8_LDB(B0, 0, 0); PG8_LDB(B1, 0, 1); PG8_SCHED; PG8_LDA(At, 0, 0); PG8_STAGE(PG8_SA(1, 1), a1 + hstep, voffA);
;             PG8_WAIT_V(8); PG8_WAIT_L(0); PG8_BAR; PG8_MMA(0, 0, At, B0); PG8_MMA(0, 1, At, B1); PG8_BAR; PG8_SCHED;
;             PG8_LDA(At, 0, 1); PG8_STAGE(PG8_SB(0, 0), b2, voffB); PG8_STAGE(PG8_SB(0, 1), b2 + hstep, voffB); PG8_STAGE(PG8_SA(0, 0), a2, voffA);
;             PG8_WAIT_V(8); PG8_WAIT_L(0); PG8_BAR; PG8_MMA(1, 0, At, B0); PG8_MMA(1, 1, At, B1); PG8_BAR; PG8_SCHED;
.LBB0_598:
	s_add_u32 s14, s20, 0xfffc0080
	s_addc_u32 s15, s21, -1
	s_add_i32 s56, 0, 0x10000
	s_cmp_eq_u32 s55, 12
	s_cselect_b32 s39, s13, s15
	s_cselect_b32 s38, s51, s14
	s_cselect_b32 s23, s11, s54
	s_cselect_b32 s22, s52, s53
	s_add_i32 s57, 0, 0x14000
	v_add_u32_e32 v142, s56, v185
	v_add_u32_e32 v162, s57, v185
	ds_read_b128 v[130:133], v142
	ds_read_b128 v[134:137], v142 offset:1024
	ds_read_b128 v[138:141], v142 offset:2048
	ds_read_b128 v[142:145], v142 offset:3072
	ds_read_b128 v[146:149], v162
	ds_read_b128 v[150:153], v162 offset:1024
	ds_read_b128 v[154:157], v162 offset:2048
	ds_read_b128 v[162:165], v162 offset:3072
	v_lshl_add_u64 v[240:241], s[20:21], 0, v[158:159]
	s_add_i32 m0, s42, 0xc000
	ds_read_b128 v[166:169], v207
	ds_read_b128 v[170:173], v207 offset:1024
	ds_read_b128 v[208:211], v207 offset:2048
	ds_read_b128 v[212:215], v207 offset:3072
	ds_read_b128 v[216:219], v207 offset:4096
	ds_read_b128 v[220:223], v207 offset:5120
	ds_read_b128 v[232:235], v207 offset:6144
	ds_read_b128 v[236:239], v207 offset:7168
	global_load_lds_dwordx4 v[240:241], off
	v_lshl_add_u64 v[240:241], s[20:21], 0, v[160:161]
	s_add_i32 m0, s42, 0xe000
	s_nop 0
	global_load_lds_dwordx4 v[240:241], off
	s_waitcnt vmcnt(8)
	s_waitcnt lgkmcnt(0)
	s_barrier
	s_setprio 1
	s_waitcnt lgkmcnt(0)
	v_mfma_f32_16x16x32_bf16 v[122:125], v[130:133], v[166:169], v[122:125]
	v_mfma_f32_16x16x32_bf16 v[126:129], v[138:141], v[166:169], v[126:129]
	v_mfma_f32_16x16x32_bf16 v[106:109], v[130:133], v[208:211], v[106:109]
	v_mfma_f32_16x16x32_bf16 v[110:113], v[138:141], v[208:211], v[110:113]
	v_mfma_f32_16x16x32_bf16 v[90:93], v[130:133], v[216:219], v[90:93]
	v_mfma_f32_16x16x32_bf16 v[94:97], v[138:141], v[216:219], v[94:97]
	v_mfma_f32_16x16x32_bf16 v[74:77], v[130:133], v[232:235], v[74:77]
	v_mfma_f32_16x16x32_bf16 v[78:81], v[138:141], v[232:235], v[78:81]
	s_setprio 0
	s_setprio 1
	v_mfma_f32_16x16x32_bf16 v[122:125], v[134:137], v[170:173], v[122:125]
	v_mfma_f32_16x16x32_bf16 v[126:129], v[142:145], v[170:173], v[126:129]
	v_mfma_f32_16x16x32_bf16 v[106:109], v[134:137], v[212:215], v[106:109]
	v_mfma_f32_16x16x32_bf16 v[110:113], v[142:145], v[212:215], v[110:113]
	v_mfma_f32_16x16x32_bf16 v[90:93], v[134:137], v[220:223], v[90:93]
	v_mfma_f32_16x16x32_bf16 v[94:97], v[142:145], v[220:223], v[94:97]
	v_mfma_f32_16x16x32_bf16 v[74:77], v[134:137], v[236:239], v[74:77]
	v_mfma_f32_16x16x32_bf16 v[78:81], v[142:145], v[236:239], v[78:81]
	s_setprio 0
	s_setprio 1
	v_mfma_f32_16x16x32_bf16 v[114:117], v[146:149], v[166:169], v[114:117]
	v_mfma_f32_16x16x32_bf16 v[118:121], v[154:157], v[166:169], v[118:121]
	v_mfma_f32_16x16x32_bf16 v[98:101], v[146:149], v[208:211], v[98:101]
	v_mfma_f32_16x16x32_bf16 v[102:105], v[154:157], v[208:211], v[102:105]
	v_mfma_f32_16x16x32_bf16 v[82:85], v[146:149], v[216:219], v[82:85]
	v_mfma_f32_16x16x32_bf16 v[86:89], v[154:157], v[216:219], v[86:89]
	v_mfma_f32_16x16x32_bf16 v[66:69], v[146:149], v[232:235], v[66:69]
	v_mfma_f32_16x16x32_bf16 v[70:73], v[154:157], v[232:235], v[70:73]
	s_setprio 0
	s_setprio 1
	v_mfma_f32_16x16x32_bf16 v[114:117], v[150:153], v[170:173], v[114:117]
	v_mfma_f32_16x16x32_bf16 v[118:121], v[162:165], v[170:173], v[118:121]
	v_mfma_f32_16x16x32_bf16 v[98:101], v[150:153], v[212:215], v[98:101]
	v_mfma_f32_16x16x32_bf16 v[102:105], v[162:165], v[212:215], v[102:105]
	v_mfma_f32_16x16x32_bf16 v[82:85], v[150:153], v[220:223], v[82:85]
	v_mfma_f32_16x16x32_bf16 v[86:89], v[162:165], v[220:223], v[86:89]
	v_mfma_f32_16x16x32_bf16 v[66:69], v[150:153], v[236:239], v[66:69]
	v_mfma_f32_16x16x32_bf16 v[70:73], v[162:165], v[236:239], v[70:73]
	s_setprio 0
	s_barrier
	s_add_i32 s14, s56, s41
	v_lshl_add_u64 v[240:241], s[22:23], 0, v[186:187]
	s_mov_b32 m0, s14
	ds_read_b128 v[166:169], v207 offset:16384
	ds_read_b128 v[170:173], v207 offset:17408
	ds_read_b128 v[208:211], v207 offset:18432
	ds_read_b128 v[212:215], v207 offset:19456
	ds_read_b128 v[216:219], v207 offset:20480
	ds_read_b128 v[220:223], v207 offset:21504
	ds_read_b128 v[232:235], v207 offset:22528
	ds_read_b128 v[236:239], v207 offset:23552
	global_load_lds_dwordx4 v[240:241], off
	s_add_i32 m0, s14, 0x2000
	s_add_u32 s14, s22, 0x40000
	v_lshl_add_u64 v[242:243], s[22:23], 0, v[204:205]
	s_addc_u32 s15, s23, 0
	s_add_i32 s56, s57, s41
	global_load_lds_dwordx4 v[242:243], off
	v_lshl_add_u64 v[244:245], s[14:15], 0, v[186:187]
	s_mov_b32 m0, s56
	v_lshl_add_u64 v[246:247], s[38:39], 0, v[202:203]
	global_load_lds_dwordx4 v[244:245], off
	v_lshl_add_u64 v[244:245], s[14:15], 0, v[204:205]
	s_add_i32 m0, s56, 0x2000
	s_nop 0
	global_load_lds_dwordx4 v[244:245], off
	v_lshl_add_u64 v[244:245], s[38:39], 0, v[200:201]
	s_mov_b32 m0, s42
	s_nop 0
	global_load_lds_dwordx4 v[244:245], off
	s_mov_b32 m0, s43
	s_nop 0
	global_load_lds_dwordx4 v[246:247], off
	s_waitcnt vmcnt(8)
	s_waitcnt lgkmcnt(0)
	s_barrier
; #define PG8_STAGE(bufoff, gbase, voff) do { _Pragma("unroll") for (int _i = 0; _i < 2; ++_i) \
;         __builtin_amdgcn_global_load_lds((const unsigned*)((const char*)(gbase) + (voff)[_i]), (LAS unsigned*)(lds + (bufoff) + ldsw + _i * 8192), 16, 0, 0); } while (0)
; #define PG8_LDA(dst, b, h) do { _Pragma("unroll") for (int m = 0; m < 4; ++m) _Pragma("unroll") for (int k = 0; k < 2; ++k) dst[m][k] = *(const LAS bf16x8*)(lds + PG8_SA(b, h) + aoff + m * 2048 + k * 1024); } while (0)
; #define PG8_LDB(dst, b, h) do { _Pragma("unroll") for (int n = 0; n < 2; ++n) _Pragma("unroll") for (int k = 0; k < 2; ++k) dst[n][k] = *(const LAS bf16x8*)(lds + PG8_SB(b, h) + boff + n * 2048 + k * 1024); } while (0)
; #define PG8_MMA(ai, bj, At, Bt) do { __builtin_amdgcn_s_setprio(1); _Pragma("unroll") for (int m = 0; m < 4; ++m) _Pragma("unroll") for (int n = 0; n < 2; ++n) _Pragma("unroll") for (int k = 0; k < 2; ++k) \
;         acc[ai][bj][m][n] = __builtin_amdgcn_mfma_f32_16x16x32_bf16(Bt[n][k], At[m][k], acc[ai][bj][m][n], 0, 0, 0); __builtin_amdgcn_s_setprio(0); } while (0)
; #define PG8_WAIT_V(n) asm volatile("s_waitcnt vmcnt(" #n ")" ::: "memory")
; #define PG8_WAIT_L(n) asm volatile("s_waitcnt lgkmcnt(" #n ")" ::: "memory")
; #define PG8_BAR __builtin_amdgcn_s_barrier()
; #define PG8_SCHED __builtin_amdgcn_sched_barrier(0)
; template <class Epi, class Sched>
; __device__ __forceinline__ void gemm_phase(LAS unsigned char* lds, const Gemm g, const Sched& S, const Epi& E, const int tid, unsigned* last_sig = nullptr) {
;     ...
;             PG8_WAIT_V(8); PG8_WAIT_L(0); PG8_BAR; PG8_MMA(1, 0, At, B0); PG8_MMA(1, 1, At, B1); PG8_BAR; PG8_SCHED;
;             PG8_LDB(B0, 1, 0); PG8_LDB(B1, 1, 1); PG8_SCHED; PG8_LDA(At, 1, 0); PG8_STAGE(PG8_SA(0, 1), a2 + hstep, voffA);
;             PG8_WAIT_V(8); PG8_WAIT_L(0); PG8_BAR; PG8_MMA(0, 0, At, B0); PG8_MMA(0, 1, At, B1); PG8_BAR; PG8_SCHED;
	s_setprio 1
	s_waitcnt lgkmcnt(0)
	v_mfma_f32_16x16x32_bf16 v[58:61], v[130:133], v[166:169], v[58:61]
	v_mfma_f32_16x16x32_bf16 v[62:65], v[138:141], v[166:169], v[62:65]
	v_mfma_f32_16x16x32_bf16 v[42:45], v[130:133], v[208:211], v[42:45]
	v_mfma_f32_16x16x32_bf16 v[46:49], v[138:141], v[208:211], v[46:49]
	v_mfma_f32_16x16x32_bf16 v[26:29], v[130:133], v[216:219], v[26:29]
	v_mfma_f32_16x16x32_bf16 v[30:33], v[138:141], v[216:219], v[30:33]
	v_mfma_f32_16x16x32_bf16 v[10:13], v[130:133], v[232:235], v[10:13]
	v_mfma_f32_16x16x32_bf16 v[14:17], v[138:141], v[232:235], v[14:17]
	s_setprio 0
	s_setprio 1
	v_mfma_f32_16x16x32_bf16 v[58:61], v[134:137], v[170:173], v[58:61]
	v_mfma_f32_16x16x32_bf16 v[62:65], v[142:145], v[170:173], v[62:65]
	v_mfma_f32_16x16x32_bf16 v[42:45], v[134:137], v[212:215], v[42:45]
	v_mfma_f32_16x16x32_bf16 v[46:49], v[142:145], v[212:215], v[46:49]
	v_mfma_f32_16x16x32_bf16 v[26:29], v[134:137], v[220:223], v[26:29]
	v_mfma_f32_16x16x32_bf16 v[30:33], v[142:145], v[220:223], v[30:33]
	v_mfma_f32_16x16x32_bf16 v[10:13], v[134:137], v[236:239], v[10:13]
	v_mfma_f32_16x16x32_bf16 v[14:17], v[142:145], v[236:239], v[14:17]
	s_setprio 0
	s_setprio 1
	v_mfma_f32_16x16x32_bf16 v[50:53], v[146:149], v[166:169], v[50:53]
	v_mfma_f32_16x16x32_bf16 v[54:57], v[154:157], v[166:169], v[54:57]
	v_mfma_f32_16x16x32_bf16 v[34:37], v[146:149], v[208:211], v[34:37]
	v_mfma_f32_16x16x32_bf16 v[38:41], v[154:157], v[208:211], v[38:41]
	v_mfma_f32_16x16x32_bf16 v[18:21], v[146:149], v[216:219], v[18:21]
	v_mfma_f32_16x16x32_bf16 v[22:25], v[154:157], v[216:219], v[22:25]
	v_mfma_f32_16x16x32_bf16 v[2:5], v[146:149], v[232:235], v[2:5]
	v_mfma_f32_16x16x32_bf16 v[6:9], v[154:157], v[232:235], v[6:9]
	s_setprio 0
	s_setprio 1
	v_mfma_f32_16x16x32_bf16 v[50:53], v[150:153], v[170:173], v[50:53]
	v_mfma_f32_16x16x32_bf16 v[54:57], v[162:165], v[170:173], v[54:57]
	v_mfma_f32_16x16x32_bf16 v[34:37], v[150:153], v[212:215], v[34:37]
	v_mfma_f32_16x16x32_bf16 v[38:41], v[162:165], v[212:215], v[38:41]
	v_mfma_f32_16x16x32_bf16 v[18:21], v[150:153], v[220:223], v[18:21]
	v_mfma_f32_16x16x32_bf16 v[22:25], v[162:165], v[220:223], v[22:25]
	v_mfma_f32_16x16x32_bf16 v[2:5], v[150:153], v[236:239], v[2:5]
	v_mfma_f32_16x16x32_bf16 v[6:9], v[162:165], v[236:239], v[6:9]
	s_setprio 0
	s_barrier
	s_add_i32 s56, 0, 0x18000
	s_add_i32 s57, 0, 0x1c000
	v_add_u32_e32 v142, s56, v185
	v_add_u32_e32 v162, s57, v185
	ds_read_b128 v[130:133], v142
	ds_read_b128 v[134:137], v142 offset:1024
	ds_read_b128 v[138:141], v142 offset:2048
	ds_read_b128 v[142:145], v142 offset:3072
	ds_read_b128 v[146:149], v162
	ds_read_b128 v[150:153], v162 offset:1024
	ds_read_b128 v[154:157], v162 offset:2048
	ds_read_b128 v[162:165], v162 offset:3072
	s_add_u32 s14, s38, 0x40000
	s_addc_u32 s15, s39, 0
	s_mov_b32 m0, s44
	v_lshl_add_u64 v[248:249], s[14:15], 0, v[200:201]
	ds_read_b128 v[166:169], v207 offset:32768
	ds_read_b128 v[170:173], v207 offset:33792
	ds_read_b128 v[208:211], v207 offset:34816
	ds_read_b128 v[212:215], v207 offset:35840
	ds_read_b128 v[216:219], v207 offset:36864
	ds_read_b128 v[220:223], v207 offset:37888
	ds_read_b128 v[232:235], v207 offset:38912
	ds_read_b128 v[236:239], v207 offset:39936
	global_load_lds_dwordx4 v[248:249], off
	v_lshl_add_u64 v[248:249], s[14:15], 0, v[202:203]
	s_mov_b32 m0, s45
	s_nop 0
	global_load_lds_dwordx4 v[248:249], off
	s_waitcnt vmcnt(8)
	s_waitcnt lgkmcnt(0)
	s_barrier
	s_setprio 1
	s_waitcnt lgkmcnt(0)
	v_mfma_f32_16x16x32_bf16 v[122:125], v[130:133], v[166:169], v[122:125]
	v_mfma_f32_16x16x32_bf16 v[126:129], v[138:141], v[166:169], v[126:129]
	v_mfma_f32_16x16x32_bf16 v[106:109], v[130:133], v[208:211], v[106:109]
	v_mfma_f32_16x16x32_bf16 v[110:113], v[138:141], v[208:211], v[110:113]
	v_mfma_f32_16x16x32_bf16 v[90:93], v[130:133], v[216:219], v[90:93]
	v_mfma_f32_16x16x32_bf16 v[94:97], v[138:141], v[216:219], v[94:97]
	v_mfma_f32_16x16x32_bf16 v[74:77], v[130:133], v[232:235], v[74:77]
	v_mfma_f32_16x16x32_bf16 v[78:81], v[138:141], v[232:235], v[78:81]
	s_setprio 0
	s_setprio 1
	v_mfma_f32_16x16x32_bf16 v[122:125], v[134:137], v[170:173], v[122:125]
	v_mfma_f32_16x16x32_bf16 v[126:129], v[142:145], v[170:173], v[126:129]
	v_mfma_f32_16x16x32_bf16 v[106:109], v[134:137], v[212:215], v[106:109]
	v_mfma_f32_16x16x32_bf16 v[110:113], v[142:145], v[212:215], v[110:113]
	v_mfma_f32_16x16x32_bf16 v[90:93], v[134:137], v[220:223], v[90:93]
	v_mfma_f32_16x16x32_bf16 v[94:97], v[142:145], v[220:223], v[94:97]
	v_mfma_f32_16x16x32_bf16 v[74:77], v[134:137], v[236:239], v[74:77]
	v_mfma_f32_16x16x32_bf16 v[78:81], v[142:145], v[236:239], v[78:81]
	s_setprio 0
	s_setprio 1
	v_mfma_f32_16x16x32_bf16 v[114:117], v[146:149], v[166:169], v[114:117]
	v_mfma_f32_16x16x32_bf16 v[118:121], v[154:157], v[166:169], v[118:121]
	v_mfma_f32_16x16x32_bf16 v[98:101], v[146:149], v[208:211], v[98:101]
	v_mfma_f32_16x16x32_bf16 v[102:105], v[154:157], v[208:211], v[102:105]
	v_mfma_f32_16x16x32_bf16 v[82:85], v[146:149], v[216:219], v[82:85]
	v_mfma_f32_16x16x32_bf16 v[86:89], v[154:157], v[216:219], v[86:89]
	v_mfma_f32_16x16x32_bf16 v[66:69], v[146:149], v[232:235], v[66:69]
	v_mfma_f32_16x16x32_bf16 v[70:73], v[154:157], v[232:235], v[70:73]
	s_setprio 0
	s_setprio 1
	v_mfma_f32_16x16x32_bf16 v[114:117], v[150:153], v[170:173], v[114:117]
	v_mfma_f32_16x16x32_bf16 v[118:121], v[162:165], v[170:173], v[118:121]
	v_mfma_f32_16x16x32_bf16 v[98:101], v[150:153], v[212:215], v[98:101]
	v_mfma_f32_16x16x32_bf16 v[102:105], v[162:165], v[212:215], v[102:105]
	v_mfma_f32_16x16x32_bf16 v[82:85], v[150:153], v[220:223], v[82:85]
	v_mfma_f32_16x16x32_bf16 v[86:89], v[162:165], v[220:223], v[86:89]
	v_mfma_f32_16x16x32_bf16 v[66:69], v[150:153], v[236:239], v[66:69]
	v_mfma_f32_16x16x32_bf16 v[70:73], v[162:165], v[236:239], v[70:73]
	s_setprio 0
	s_barrier
; #define PG8_STAGE(bufoff, gbase, voff) do { _Pragma("unroll") for (int _i = 0; _i < 2; ++_i) \
;         __builtin_amdgcn_global_load_lds((const unsigned*)((const char*)(gbase) + (voff)[_i]), (LAS unsigned*)(lds + (bufoff) + ldsw + _i * 8192), 16, 0, 0); } while (0)
; #define PG8_LDA(dst, b, h) do { _Pragma("unroll") for (int m = 0; m < 4; ++m) _Pragma("unroll") for (int k = 0; k < 2; ++k) dst[m][k] = *(const LAS bf16x8*)(lds + PG8_SA(b, h) + aoff + m * 2048 + k * 1024); } while (0)
; #define PG8_MMA(ai, bj, At, Bt) do { __builtin_amdgcn_s_setprio(1); _Pragma("unroll") for (int m = 0; m < 4; ++m) _Pragma("unroll") for (int n = 0; n < 2; ++n) _Pragma("unroll") for (int k = 0; k < 2; ++k) \
;         acc[ai][bj][m][n] = __builtin_amdgcn_mfma_f32_16x16x32_bf16(Bt[n][k], At[m][k], acc[ai][bj][m][n], 0, 0, 0); __builtin_amdgcn_s_setprio(0); } while (0)
; #define PG8_WAIT_V(n) asm volatile("s_waitcnt vmcnt(" #n ")" ::: "memory")
; #define PG8_WAIT_L(n) asm volatile("s_waitcnt lgkmcnt(" #n ")" ::: "memory")
; #define PG8_BAR __builtin_amdgcn_s_barrier()
; #define PG8_SCHED __builtin_amdgcn_sched_barrier(0)
; template <class Epi, class Sched>
; __device__ __forceinline__ void gemm_phase(LAS unsigned char* lds, const Gemm g, const Sched& S, const Epi& E, const int tid, unsigned* last_sig = nullptr) {
;     ...
;             PG8_LDA(At, 1, 1); PG8_STAGE(PG8_SB(1, 0), b3, voffB); PG8_STAGE(PG8_SB(1, 1), b3 + hstep, voffB); PG8_STAGE(PG8_SA(1, 0), a3, voffA);
;             PG8_WAIT_V(8); PG8_WAIT_L(0); PG8_BAR; PG8_MMA(1, 0, At, B0); PG8_MMA(1, 1, At, B1); PG8_BAR; PG8_SCHED;
;         }
;         if (wr == 0) PG8_BAR;
	s_add_i32 s14, s56, s41
	v_lshl_add_u64 v[240:241], v[240:241], 0, s[34:35]
	s_mov_b32 m0, s14
	ds_read_b128 v[166:169], v207 offset:49152
	ds_read_b128 v[170:173], v207 offset:50176
	ds_read_b128 v[208:211], v207 offset:51200
	ds_read_b128 v[212:215], v207 offset:52224
	ds_read_b128 v[216:219], v207 offset:53248
	ds_read_b128 v[220:223], v207 offset:54272
	ds_read_b128 v[232:235], v207 offset:55296
	ds_read_b128 v[236:239], v207 offset:56320
	global_load_lds_dwordx4 v[240:241], off
	s_add_i32 m0, s14, 0x2000
	s_add_u32 s14, s22, 0x40080
	v_lshl_add_u64 v[240:241], v[242:243], 0, s[34:35]
	s_addc_u32 s15, s23, 0
	s_add_i32 s22, s57, s41
	global_load_lds_dwordx4 v[240:241], off
	v_lshl_add_u64 v[240:241], s[14:15], 0, v[186:187]
	s_mov_b32 m0, s22
	s_nop 0
	global_load_lds_dwordx4 v[240:241], off
	v_lshl_add_u64 v[240:241], s[14:15], 0, v[204:205]
	s_add_i32 m0, s22, 0x2000
	s_nop 0
	global_load_lds_dwordx4 v[240:241], off
	v_lshl_add_u64 v[240:241], v[244:245], 0, s[34:35]
	s_mov_b32 m0, s46
	s_nop 0
	global_load_lds_dwordx4 v[240:241], off
	v_lshl_add_u64 v[240:241], v[246:247], 0, s[34:35]
	s_mov_b32 m0, s47
	s_nop 0
	global_load_lds_dwordx4 v[240:241], off
	s_waitcnt vmcnt(8)
	s_waitcnt lgkmcnt(0)
	s_barrier
	s_setprio 1
	s_waitcnt lgkmcnt(0)
	v_mfma_f32_16x16x32_bf16 v[58:61], v[130:133], v[166:169], v[58:61]
	v_mfma_f32_16x16x32_bf16 v[62:65], v[138:141], v[166:169], v[62:65]
	v_mfma_f32_16x16x32_bf16 v[42:45], v[130:133], v[208:211], v[42:45]
	v_mfma_f32_16x16x32_bf16 v[46:49], v[138:141], v[208:211], v[46:49]
	v_mfma_f32_16x16x32_bf16 v[26:29], v[130:133], v[216:219], v[26:29]
	v_mfma_f32_16x16x32_bf16 v[30:33], v[138:141], v[216:219], v[30:33]
	v_mfma_f32_16x16x32_bf16 v[10:13], v[130:133], v[232:235], v[10:13]
	v_mfma_f32_16x16x32_bf16 v[14:17], v[138:141], v[232:235], v[14:17]
	s_setprio 0
	s_setprio 1
	v_mfma_f32_16x16x32_bf16 v[58:61], v[134:137], v[170:173], v[58:61]
	v_mfma_f32_16x16x32_bf16 v[62:65], v[142:145], v[170:173], v[62:65]
	v_mfma_f32_16x16x32_bf16 v[42:45], v[134:137], v[212:215], v[42:45]
	v_mfma_f32_16x16x32_bf16 v[46:49], v[142:145], v[212:215], v[46:49]
	v_mfma_f32_16x16x32_bf16 v[26:29], v[134:137], v[220:223], v[26:29]
	v_mfma_f32_16x16x32_bf16 v[30:33], v[142:145], v[220:223], v[30:33]
	v_mfma_f32_16x16x32_bf16 v[10:13], v[134:137], v[236:239], v[10:13]
	v_mfma_f32_16x16x32_bf16 v[14:17], v[142:145], v[236:239], v[14:17]
	s_setprio 0
	s_setprio 1
	v_mfma_f32_16x16x32_bf16 v[50:53], v[146:149], v[166:169], v[50:53]
	v_mfma_f32_16x16x32_bf16 v[54:57], v[154:157], v[166:169], v[54:57]
	v_mfma_f32_16x16x32_bf16 v[34:37], v[146:149], v[208:211], v[34:37]
	v_mfma_f32_16x16x32_bf16 v[38:41], v[154:157], v[208:211], v[38:41]
	v_mfma_f32_16x16x32_bf16 v[18:21], v[146:149], v[216:219], v[18:21]
	v_mfma_f32_16x16x32_bf16 v[22:25], v[154:157], v[216:219], v[22:25]
	v_mfma_f32_16x16x32_bf16 v[2:5], v[146:149], v[232:235], v[2:5]
	v_mfma_f32_16x16x32_bf16 v[6:9], v[154:157], v[232:235], v[6:9]
	s_setprio 0
	s_setprio 1
	v_mfma_f32_16x16x32_bf16 v[50:53], v[150:153], v[170:173], v[50:53]
	v_mfma_f32_16x16x32_bf16 v[54:57], v[162:165], v[170:173], v[54:57]
	v_mfma_f32_16x16x32_bf16 v[34:37], v[150:153], v[212:215], v[34:37]
	v_mfma_f32_16x16x32_bf16 v[38:41], v[162:165], v[212:215], v[38:41]
	v_mfma_f32_16x16x32_bf16 v[18:21], v[150:153], v[220:223], v[18:21]
	v_mfma_f32_16x16x32_bf16 v[22:25], v[162:165], v[220:223], v[22:25]
	v_mfma_f32_16x16x32_bf16 v[2:5], v[150:153], v[236:239], v[2:5]
	v_mfma_f32_16x16x32_bf16 v[6:9], v[162:165], v[236:239], v[6:9]
	s_setprio 0
	s_barrier
	s_add_i32 s55, s55, 2
	s_add_u32 s20, s20, 0x100
	s_addc_u32 s21, s21, 0
	s_add_u32 s53, s53, 0x100
	s_addc_u32 s54, s54, 0
	s_cmp_gt_u32 s55, 13
	s_cbranch_scc0 .LBB0_598
	s_and_b64 vcc, exec, s[8:9]
	s_cbranch_vccz .LBB0_601
	s_barrier

; #define PG8_STAGE(bufoff, gbase, voff) do { _Pragma("unroll") for (int _i = 0; _i < 2; ++_i) \
;         __builtin_amdgcn_global_load_lds((const unsigned*)((const char*)(gbase) + (voff)[_i]), (LAS unsigned*)(lds + (bufoff) + ldsw + _i * 8192), 16, 0, 0); } while (0)
; #define PG8_LDA(dst, b, h) do { _Pragma("unroll") for (int m = 0; m < 4; ++m) _Pragma("unroll") for (int k = 0; k < 2; ++k) dst[m][k] = *(const LAS bf16x8*)(lds + PG8_SA(b, h) + aoff + m * 2048 + k * 1024); } while (0)
; #define PG8_LDB(dst, b, h) do { _Pragma("unroll") for (int n = 0; n < 2; ++n) _Pragma("unroll") for (int k = 0; k < 2; ++k) dst[n][k] = *(const LAS bf16x8*)(lds + PG8_SB(b, h) + boff + n * 2048 + k * 1024); } while (0)
; #define PG8_MMA(ai, bj, At, Bt) do { __builtin_amdgcn_s_setprio(1); _Pragma("unroll") for (int m = 0; m < 4; ++m) _Pragma("unroll") for (int n = 0; n < 2; ++n) _Pragma("unroll") for (int k = 0; k < 2; ++k) \
;         acc[ai][bj][m][n] = __builtin_amdgcn_mfma_f32_16x16x32_bf16(Bt[n][k], At[m][k], acc[ai][bj][m][n], 0, 0, 0); __builtin_amdgcn_s_setprio(0); } while (0)
; #define PG8_WAIT_V(n) asm volatile("s_waitcnt vmcnt(" #n ")" ::: "memory")
; #define PG8_WAIT_L(n) asm volatile("s_waitcnt lgkmcnt(" #n ")" ::: "memory")
; #define PG8_BAR __builtin_amdgcn_s_barrier()
; template <class Epi, class Sched>
; __device__ __forceinline__ void gemm_phase(LAS unsigned char* lds, const Gemm g, const Sched& S, const Epi& E, const int tid, unsigned* last_sig = nullptr) {
;     ...
;         for (int t = 0; t < nt; t += 2) {
;             const bool last = (t == nt - 2);
;             const char* a1 = cA + (size_t)(t + 1) * kstep;
;             const char* a2 = last ? nA : cA + (size_t)(t + 2) * kstep; const char* b2 = last ? nB : cB + (size_t)(t + 2) * kstep;
;             const char* a3 = a2 + kstep; const char* b3 = b2 + kstep;
;             PG8_LDB(B0, 0, 0); PG8_LDB(B1, 0, 1); PG8_SCHED; PG8_LDA(At, 0, 0); PG8_STAGE(PG8_SA(1, 1), a1 + hstep, voffA);
;             PG8_WAIT_V(8); PG8_WAIT_L(0); PG8_BAR; PG8_MMA(0, 0, At, B0); PG8_MMA(0, 1, At, B1); PG8_BAR; PG8_SCHED;
;             PG8_LDA(At, 0, 1); PG8_STAGE(PG8_SB(0, 0), b2, voffB); PG8_STAGE(PG8_SB(0, 1), b2 + hstep, voffB); PG8_STAGE(PG8_SA(0, 0), a2, voffA);
;             PG8_WAIT_V(8); PG8_WAIT_L(0); PG8_BAR; PG8_MMA(1, 0, At, B0); PG8_MMA(1, 1, At, B1); PG8_BAR; PG8_SCHED;
.LBB0_618:
	s_add_u32 s14, s22, 0xfffc0080
	s_addc_u32 s15, s23, -1
	s_add_i32 s53, 0, 0x10000
	s_cmp_eq_u32 s52, 12
	s_cselect_b32 s41, s11, s15
	s_cselect_b32 s40, s19, s14
	s_cselect_b32 s39, s9, s51
	s_cselect_b32 s38, s49, s50
	s_add_i32 s54, 0, 0x14000
	v_add_u32_e32 v142, s53, v232
	v_add_u32_e32 v158, s54, v232
	ds_read_b128 v[130:133], v142
	ds_read_b128 v[134:137], v142 offset:1024
	ds_read_b128 v[138:141], v142 offset:2048
	ds_read_b128 v[142:145], v142 offset:3072
	ds_read_b128 v[146:149], v158
	ds_read_b128 v[150:153], v158 offset:1024
	ds_read_b128 v[154:157], v158 offset:2048
	ds_read_b128 v[158:161], v158 offset:3072
	v_lshl_add_u64 v[218:219], s[22:23], 0, v[206:207]
	s_add_i32 m0, s21, 0xc000
	ds_read_b128 v[162:165], v234
	ds_read_b128 v[166:169], v234 offset:1024
	ds_read_b128 v[170:173], v234 offset:2048
	ds_read_b128 v[174:177], v234 offset:3072
	ds_read_b128 v[178:181], v234 offset:4096
	ds_read_b128 v[182:185], v234 offset:5120
	ds_read_b128 v[210:213], v234 offset:6144
	ds_read_b128 v[214:217], v234 offset:7168
	global_load_lds_dwordx4 v[218:219], off
	v_lshl_add_u64 v[218:219], s[22:23], 0, v[208:209]
	s_add_i32 m0, s21, 0xe000
	s_nop 0
	global_load_lds_dwordx4 v[218:219], off
	s_waitcnt vmcnt(8)
	s_waitcnt lgkmcnt(0)
	s_barrier
	s_setprio 1
	s_waitcnt lgkmcnt(0)
	v_mfma_f32_16x16x32_bf16 v[122:125], v[130:133], v[162:165], v[122:125]
	v_mfma_f32_16x16x32_bf16 v[126:129], v[138:141], v[162:165], v[126:129]
	v_mfma_f32_16x16x32_bf16 v[106:109], v[130:133], v[170:173], v[106:109]
	v_mfma_f32_16x16x32_bf16 v[110:113], v[138:141], v[170:173], v[110:113]
	v_mfma_f32_16x16x32_bf16 v[90:93], v[130:133], v[178:181], v[90:93]
	v_mfma_f32_16x16x32_bf16 v[94:97], v[138:141], v[178:181], v[94:97]
	v_mfma_f32_16x16x32_bf16 v[74:77], v[130:133], v[210:213], v[74:77]
	v_mfma_f32_16x16x32_bf16 v[78:81], v[138:141], v[210:213], v[78:81]
	s_setprio 0
	s_setprio 1
	v_mfma_f32_16x16x32_bf16 v[122:125], v[134:137], v[166:169], v[122:125]
	v_mfma_f32_16x16x32_bf16 v[126:129], v[142:145], v[166:169], v[126:129]
	v_mfma_f32_16x16x32_bf16 v[106:109], v[134:137], v[174:177], v[106:109]
	v_mfma_f32_16x16x32_bf16 v[110:113], v[142:145], v[174:177], v[110:113]
	v_mfma_f32_16x16x32_bf16 v[90:93], v[134:137], v[182:185], v[90:93]
	v_mfma_f32_16x16x32_bf16 v[94:97], v[142:145], v[182:185], v[94:97]
	v_mfma_f32_16x16x32_bf16 v[74:77], v[134:137], v[214:217], v[74:77]
	v_mfma_f32_16x16x32_bf16 v[78:81], v[142:145], v[214:217], v[78:81]
	s_setprio 0
	s_setprio 1
	v_mfma_f32_16x16x32_bf16 v[114:117], v[146:149], v[162:165], v[114:117]
	v_mfma_f32_16x16x32_bf16 v[118:121], v[154:157], v[162:165], v[118:121]
	v_mfma_f32_16x16x32_bf16 v[98:101], v[146:149], v[170:173], v[98:101]
	v_mfma_f32_16x16x32_bf16 v[102:105], v[154:157], v[170:173], v[102:105]
	v_mfma_f32_16x16x32_bf16 v[82:85], v[146:149], v[178:181], v[82:85]
	v_mfma_f32_16x16x32_bf16 v[86:89], v[154:157], v[178:181], v[86:89]
	v_mfma_f32_16x16x32_bf16 v[66:69], v[146:149], v[210:213], v[66:69]
	v_mfma_f32_16x16x32_bf16 v[70:73], v[154:157], v[210:213], v[70:73]
	s_setprio 0
	s_setprio 1
	v_mfma_f32_16x16x32_bf16 v[114:117], v[150:153], v[166:169], v[114:117]
	v_mfma_f32_16x16x32_bf16 v[118:121], v[158:161], v[166:169], v[118:121]
	v_mfma_f32_16x16x32_bf16 v[98:101], v[150:153], v[174:177], v[98:101]
	v_mfma_f32_16x16x32_bf16 v[102:105], v[158:161], v[174:177], v[102:105]
	v_mfma_f32_16x16x32_bf16 v[82:85], v[150:153], v[182:185], v[82:85]
	v_mfma_f32_16x16x32_bf16 v[86:89], v[158:161], v[182:185], v[86:89]
	v_mfma_f32_16x16x32_bf16 v[66:69], v[150:153], v[214:217], v[66:69]
	v_mfma_f32_16x16x32_bf16 v[70:73], v[158:161], v[214:217], v[70:73]
	s_setprio 0
	s_barrier
	s_add_i32 s14, s53, s42
	v_lshl_add_u64 v[218:219], s[38:39], 0, v[186:187]
	s_mov_b32 m0, s14
	ds_read_b128 v[162:165], v234 offset:16384
	ds_read_b128 v[166:169], v234 offset:17408
	ds_read_b128 v[170:173], v234 offset:18432
	ds_read_b128 v[174:177], v234 offset:19456
	ds_read_b128 v[178:181], v234 offset:20480
	ds_read_b128 v[182:185], v234 offset:21504
	ds_read_b128 v[210:213], v234 offset:22528
	ds_read_b128 v[214:217], v234 offset:23552
	global_load_lds_dwordx4 v[218:219], off
	s_add_i32 m0, s14, 0x2000
	s_add_u32 s14, s38, 0x40000
	v_lshl_add_u64 v[220:221], s[38:39], 0, v[204:205]
	s_addc_u32 s15, s39, 0
	s_add_i32 s53, s54, s42
	global_load_lds_dwordx4 v[220:221], off
	v_lshl_add_u64 v[222:223], s[14:15], 0, v[186:187]
	s_mov_b32 m0, s53
	v_lshl_add_u64 v[236:237], s[40:41], 0, v[202:203]
	global_load_lds_dwordx4 v[222:223], off
	v_lshl_add_u64 v[222:223], s[14:15], 0, v[204:205]
	s_add_i32 m0, s53, 0x2000
	s_nop 0
	global_load_lds_dwordx4 v[222:223], off
	v_lshl_add_u64 v[222:223], s[40:41], 0, v[200:201]
	s_mov_b32 m0, s21
	s_nop 0
	global_load_lds_dwordx4 v[222:223], off
	s_mov_b32 m0, s43
	s_nop 0
	global_load_lds_dwordx4 v[236:237], off
	s_waitcnt vmcnt(8)
	s_waitcnt lgkmcnt(0)
	s_barrier
; #define PG8_STAGE(bufoff, gbase, voff) do { _Pragma("unroll") for (int _i = 0; _i < 2; ++_i) \
;         __builtin_amdgcn_global_load_lds((const unsigned*)((const char*)(gbase) + (voff)[_i]), (LAS unsigned*)(lds + (bufoff) + ldsw + _i * 8192), 16, 0, 0); } while (0)
; #define PG8_LDA(dst, b, h) do { _Pragma("unroll") for (int m = 0; m < 4; ++m) _Pragma("unroll") for (int k = 0; k < 2; ++k) dst[m][k] = *(const LAS bf16x8*)(lds + PG8_SA(b, h) + aoff + m * 2048 + k * 1024); } while (0)
; #define PG8_LDB(dst, b, h) do { _Pragma("unroll") for (int n = 0; n < 2; ++n) _Pragma("unroll") for (int k = 0; k < 2; ++k) dst[n][k] = *(const LAS bf16x8*)(lds + PG8_SB(b, h) + boff + n * 2048 + k * 1024); } while (0)
; #define PG8_MMA(ai, bj, At, Bt) do { __builtin_amdgcn_s_setprio(1); _Pragma("unroll") for (int m = 0; m < 4; ++m) _Pragma("unroll") for (int n = 0; n < 2; ++n) _Pragma("unroll") for (int k = 0; k < 2; ++k) \
;         acc[ai][bj][m][n] = __builtin_amdgcn_mfma_f32_16x16x32_bf16(Bt[n][k], At[m][k], acc[ai][bj][m][n], 0, 0, 0); __builtin_amdgcn_s_setprio(0); } while (0)
; #define PG8_WAIT_V(n) asm volatile("s_waitcnt vmcnt(" #n ")" ::: "memory")
; #define PG8_WAIT_L(n) asm volatile("s_waitcnt lgkmcnt(" #n ")" ::: "memory")
; #define PG8_BAR __builtin_amdgcn_s_barrier()
; #define PG8_SCHED __builtin_amdgcn_sched_barrier(0)
; template <class Epi, class Sched>
; __device__ __forceinline__ void gemm_phase(LAS unsigned char* lds, const Gemm g, const Sched& S, const Epi& E, const int tid, unsigned* last_sig = nullptr) {
;     ...
;             PG8_WAIT_V(8); PG8_WAIT_L(0); PG8_BAR; PG8_MMA(1, 0, At, B0); PG8_MMA(1, 1, At, B1); PG8_BAR; PG8_SCHED;
;             PG8_LDB(B0, 1, 0); PG8_LDB(B1, 1, 1); PG8_SCHED; PG8_LDA(At, 1, 0); PG8_STAGE(PG8_SA(0, 1), a2 + hstep, voffA);
;             PG8_WAIT_V(8); PG8_WAIT_L(0); PG8_BAR; PG8_MMA(0, 0, At, B0); PG8_MMA(0, 1, At, B1); PG8_BAR; PG8_SCHED;
	s_setprio 1
	s_waitcnt lgkmcnt(0)
	v_mfma_f32_16x16x32_bf16 v[58:61], v[130:133], v[162:165], v[58:61]
	v_mfma_f32_16x16x32_bf16 v[62:65], v[138:141], v[162:165], v[62:65]
	v_mfma_f32_16x16x32_bf16 v[42:45], v[130:133], v[170:173], v[42:45]
	v_mfma_f32_16x16x32_bf16 v[46:49], v[138:141], v[170:173], v[46:49]
	v_mfma_f32_16x16x32_bf16 v[26:29], v[130:133], v[178:181], v[26:29]
	v_mfma_f32_16x16x32_bf16 v[30:33], v[138:141], v[178:181], v[30:33]
	v_mfma_f32_16x16x32_bf16 v[10:13], v[130:133], v[210:213], v[10:13]
	v_mfma_f32_16x16x32_bf16 v[14:17], v[138:141], v[210:213], v[14:17]
	s_setprio 0
	s_setprio 1
	v_mfma_f32_16x16x32_bf16 v[58:61], v[134:137], v[166:169], v[58:61]
	v_mfma_f32_16x16x32_bf16 v[62:65], v[142:145], v[166:169], v[62:65]
	v_mfma_f32_16x16x32_bf16 v[42:45], v[134:137], v[174:177], v[42:45]
	v_mfma_f32_16x16x32_bf16 v[46:49], v[142:145], v[174:177], v[46:49]
	v_mfma_f32_16x16x32_bf16 v[26:29], v[134:137], v[182:185], v[26:29]
	v_mfma_f32_16x16x32_bf16 v[30:33], v[142:145], v[182:185], v[30:33]
	v_mfma_f32_16x16x32_bf16 v[10:13], v[134:137], v[214:217], v[10:13]
	v_mfma_f32_16x16x32_bf16 v[14:17], v[142:145], v[214:217], v[14:17]
	s_setprio 0
	s_setprio 1
	v_mfma_f32_16x16x32_bf16 v[50:53], v[146:149], v[162:165], v[50:53]
	v_mfma_f32_16x16x32_bf16 v[54:57], v[154:157], v[162:165], v[54:57]
	v_mfma_f32_16x16x32_bf16 v[34:37], v[146:149], v[170:173], v[34:37]
	v_mfma_f32_16x16x32_bf16 v[38:41], v[154:157], v[170:173], v[38:41]
	v_mfma_f32_16x16x32_bf16 v[18:21], v[146:149], v[178:181], v[18:21]
	v_mfma_f32_16x16x32_bf16 v[22:25], v[154:157], v[178:181], v[22:25]
	v_mfma_f32_16x16x32_bf16 v[2:5], v[146:149], v[210:213], v[2:5]
	v_mfma_f32_16x16x32_bf16 v[6:9], v[154:157], v[210:213], v[6:9]
	s_setprio 0
	s_setprio 1
	v_mfma_f32_16x16x32_bf16 v[50:53], v[150:153], v[166:169], v[50:53]
	v_mfma_f32_16x16x32_bf16 v[54:57], v[158:161], v[166:169], v[54:57]
	v_mfma_f32_16x16x32_bf16 v[34:37], v[150:153], v[174:177], v[34:37]
	v_mfma_f32_16x16x32_bf16 v[38:41], v[158:161], v[174:177], v[38:41]
	v_mfma_f32_16x16x32_bf16 v[18:21], v[150:153], v[182:185], v[18:21]
	v_mfma_f32_16x16x32_bf16 v[22:25], v[158:161], v[182:185], v[22:25]
	v_mfma_f32_16x16x32_bf16 v[2:5], v[150:153], v[214:217], v[2:5]
	v_mfma_f32_16x16x32_bf16 v[6:9], v[158:161], v[214:217], v[6:9]
	s_setprio 0
	s_barrier
	s_add_i32 s53, 0, 0x18000
	s_add_i32 s54, 0, 0x1c000
	v_add_u32_e32 v142, s53, v232
	v_add_u32_e32 v158, s54, v232
	ds_read_b128 v[130:133], v142
	ds_read_b128 v[134:137], v142 offset:1024
	ds_read_b128 v[138:141], v142 offset:2048
	ds_read_b128 v[142:145], v142 offset:3072
	ds_read_b128 v[146:149], v158
	ds_read_b128 v[150:153], v158 offset:1024
	ds_read_b128 v[154:157], v158 offset:2048
	ds_read_b128 v[158:161], v158 offset:3072
	s_add_u32 s14, s40, 0x40000
	s_addc_u32 s15, s41, 0
	s_mov_b32 m0, s44
	v_lshl_add_u64 v[238:239], s[14:15], 0, v[200:201]
	ds_read_b128 v[162:165], v234 offset:32768
	ds_read_b128 v[166:169], v234 offset:33792
	ds_read_b128 v[170:173], v234 offset:34816
	ds_read_b128 v[174:177], v234 offset:35840
	ds_read_b128 v[178:181], v234 offset:36864
	ds_read_b128 v[182:185], v234 offset:37888
	ds_read_b128 v[210:213], v234 offset:38912
	ds_read_b128 v[214:217], v234 offset:39936
	global_load_lds_dwordx4 v[238:239], off
	v_lshl_add_u64 v[238:239], s[14:15], 0, v[202:203]
	s_mov_b32 m0, s45
	s_nop 0
	global_load_lds_dwordx4 v[238:239], off
	s_waitcnt vmcnt(8)
	s_waitcnt lgkmcnt(0)
	s_barrier
	s_setprio 1
	s_waitcnt lgkmcnt(0)
	v_mfma_f32_16x16x32_bf16 v[122:125], v[130:133], v[162:165], v[122:125]
	v_mfma_f32_16x16x32_bf16 v[126:129], v[138:141], v[162:165], v[126:129]
	v_mfma_f32_16x16x32_bf16 v[106:109], v[130:133], v[170:173], v[106:109]
	v_mfma_f32_16x16x32_bf16 v[110:113], v[138:141], v[170:173], v[110:113]
	v_mfma_f32_16x16x32_bf16 v[90:93], v[130:133], v[178:181], v[90:93]
	v_mfma_f32_16x16x32_bf16 v[94:97], v[138:141], v[178:181], v[94:97]
	v_mfma_f32_16x16x32_bf16 v[74:77], v[130:133], v[210:213], v[74:77]
	v_mfma_f32_16x16x32_bf16 v[78:81], v[138:141], v[210:213], v[78:81]
	s_setprio 0
	s_setprio 1
	v_mfma_f32_16x16x32_bf16 v[122:125], v[134:137], v[166:169], v[122:125]
	v_mfma_f32_16x16x32_bf16 v[126:129], v[142:145], v[166:169], v[126:129]
	v_mfma_f32_16x16x32_bf16 v[106:109], v[134:137], v[174:177], v[106:109]
	v_mfma_f32_16x16x32_bf16 v[110:113], v[142:145], v[174:177], v[110:113]
	v_mfma_f32_16x16x32_bf16 v[90:93], v[134:137], v[182:185], v[90:93]
	v_mfma_f32_16x16x32_bf16 v[94:97], v[142:145], v[182:185], v[94:97]
	v_mfma_f32_16x16x32_bf16 v[74:77], v[134:137], v[214:217], v[74:77]
	v_mfma_f32_16x16x32_bf16 v[78:81], v[142:145], v[214:217], v[78:81]
	s_setprio 0
	s_setprio 1
	v_mfma_f32_16x16x32_bf16 v[114:117], v[146:149], v[162:165], v[114:117]
	v_mfma_f32_16x16x32_bf16 v[118:121], v[154:157], v[162:165], v[118:121]
	v_mfma_f32_16x16x32_bf16 v[98:101], v[146:149], v[170:173], v[98:101]
	v_mfma_f32_16x16x32_bf16 v[102:105], v[154:157], v[170:173], v[102:105]
	v_mfma_f32_16x16x32_bf16 v[82:85], v[146:149], v[178:181], v[82:85]
	v_mfma_f32_16x16x32_bf16 v[86:89], v[154:157], v[178:181], v[86:89]
	v_mfma_f32_16x16x32_bf16 v[66:69], v[146:149], v[210:213], v[66:69]
	v_mfma_f32_16x16x32_bf16 v[70:73], v[154:157], v[210:213], v[70:73]
	s_setprio 0
	s_setprio 1
	v_mfma_f32_16x16x32_bf16 v[114:117], v[150:153], v[166:169], v[114:117]
	v_mfma_f32_16x16x32_bf16 v[118:121], v[158:161], v[166:169], v[118:121]
	v_mfma_f32_16x16x32_bf16 v[98:101], v[150:153], v[174:177], v[98:101]
	v_mfma_f32_16x16x32_bf16 v[102:105], v[158:161], v[174:177], v[102:105]
	v_mfma_f32_16x16x32_bf16 v[82:85], v[150:153], v[182:185], v[82:85]
	v_mfma_f32_16x16x32_bf16 v[86:89], v[158:161], v[182:185], v[86:89]
	v_mfma_f32_16x16x32_bf16 v[66:69], v[150:153], v[214:217], v[66:69]
	v_mfma_f32_16x16x32_bf16 v[70:73], v[158:161], v[214:217], v[70:73]
	s_setprio 0
	s_barrier
; #define PG8_STAGE(bufoff, gbase, voff) do { _Pragma("unroll") for (int _i = 0; _i < 2; ++_i) \
;         __builtin_amdgcn_global_load_lds((const unsigned*)((const char*)(gbase) + (voff)[_i]), (LAS unsigned*)(lds + (bufoff) + ldsw + _i * 8192), 16, 0, 0); } while (0)
; #define PG8_LDA(dst, b, h) do { _Pragma("unroll") for (int m = 0; m < 4; ++m) _Pragma("unroll") for (int k = 0; k < 2; ++k) dst[m][k] = *(const LAS bf16x8*)(lds + PG8_SA(b, h) + aoff + m * 2048 + k * 1024); } while (0)
; #define PG8_MMA(ai, bj, At, Bt) do { __builtin_amdgcn_s_setprio(1); _Pragma("unroll") for (int m = 0; m < 4; ++m) _Pragma("unroll") for (int n = 0; n < 2; ++n) _Pragma("unroll") for (int k = 0; k < 2; ++k) \
;         acc[ai][bj][m][n] = __builtin_amdgcn_mfma_f32_16x16x32_bf16(Bt[n][k], At[m][k], acc[ai][bj][m][n], 0, 0, 0); __builtin_amdgcn_s_setprio(0); } while (0)
; #define PG8_WAIT_V(n) asm volatile("s_waitcnt vmcnt(" #n ")" ::: "memory")
; #define PG8_WAIT_L(n) asm volatile("s_waitcnt lgkmcnt(" #n ")" ::: "memory")
; #define PG8_BAR __builtin_amdgcn_s_barrier()
; #define PG8_SCHED __builtin_amdgcn_sched_barrier(0)
; template <class Epi, class Sched>
; __device__ __forceinline__ void gemm_phase(LAS unsigned char* lds, const Gemm g, const Sched& S, const Epi& E, const int tid, unsigned* last_sig = nullptr) {
;     ...
;             PG8_LDA(At, 1, 1); PG8_STAGE(PG8_SB(1, 0), b3, voffB); PG8_STAGE(PG8_SB(1, 1), b3 + hstep, voffB); PG8_STAGE(PG8_SA(1, 0), a3, voffA);
;             PG8_WAIT_V(8); PG8_WAIT_L(0); PG8_BAR; PG8_MMA(1, 0, At, B0); PG8_MMA(1, 1, At, B1); PG8_BAR; PG8_SCHED;
;         }
;         if (wr == 0) PG8_BAR;
	s_add_i32 s14, s53, s42
	v_lshl_add_u64 v[218:219], v[218:219], 0, s[34:35]
	s_mov_b32 m0, s14
	ds_read_b128 v[162:165], v234 offset:49152
	ds_read_b128 v[166:169], v234 offset:50176
	ds_read_b128 v[170:173], v234 offset:51200
	ds_read_b128 v[174:177], v234 offset:52224
	ds_read_b128 v[178:181], v234 offset:53248
	ds_read_b128 v[182:185], v234 offset:54272
	ds_read_b128 v[210:213], v234 offset:55296
	ds_read_b128 v[214:217], v234 offset:56320
	global_load_lds_dwordx4 v[218:219], off
	s_add_i32 m0, s14, 0x2000
	s_add_u32 s14, s38, 0x40080
	v_lshl_add_u64 v[218:219], v[220:221], 0, s[34:35]
	s_addc_u32 s15, s39, 0
	s_add_i32 s38, s54, s42
	global_load_lds_dwordx4 v[218:219], off
	v_lshl_add_u64 v[218:219], s[14:15], 0, v[186:187]
	s_mov_b32 m0, s38
	s_nop 0
	global_load_lds_dwordx4 v[218:219], off
	v_lshl_add_u64 v[218:219], s[14:15], 0, v[204:205]
	s_add_i32 m0, s38, 0x2000
	s_nop 0
	global_load_lds_dwordx4 v[218:219], off
	v_lshl_add_u64 v[218:219], v[222:223], 0, s[34:35]
	s_mov_b32 m0, s46
	s_nop 0
	global_load_lds_dwordx4 v[218:219], off
	v_lshl_add_u64 v[218:219], v[236:237], 0, s[34:35]
	s_mov_b32 m0, s47
	s_nop 0
	global_load_lds_dwordx4 v[218:219], off
	s_waitcnt vmcnt(8)
	s_waitcnt lgkmcnt(0)
	s_barrier
	s_setprio 1
	s_waitcnt lgkmcnt(0)
	v_mfma_f32_16x16x32_bf16 v[58:61], v[130:133], v[162:165], v[58:61]
	v_mfma_f32_16x16x32_bf16 v[62:65], v[138:141], v[162:165], v[62:65]
	v_mfma_f32_16x16x32_bf16 v[42:45], v[130:133], v[170:173], v[42:45]
	v_mfma_f32_16x16x32_bf16 v[46:49], v[138:141], v[170:173], v[46:49]
	v_mfma_f32_16x16x32_bf16 v[26:29], v[130:133], v[178:181], v[26:29]
	v_mfma_f32_16x16x32_bf16 v[30:33], v[138:141], v[178:181], v[30:33]
	v_mfma_f32_16x16x32_bf16 v[10:13], v[130:133], v[210:213], v[10:13]
	v_mfma_f32_16x16x32_bf16 v[14:17], v[138:141], v[210:213], v[14:17]
	s_setprio 0
	s_setprio 1
	v_mfma_f32_16x16x32_bf16 v[58:61], v[134:137], v[166:169], v[58:61]
	v_mfma_f32_16x16x32_bf16 v[62:65], v[142:145], v[166:169], v[62:65]
	v_mfma_f32_16x16x32_bf16 v[42:45], v[134:137], v[174:177], v[42:45]
	v_mfma_f32_16x16x32_bf16 v[46:49], v[142:145], v[174:177], v[46:49]
	v_mfma_f32_16x16x32_bf16 v[26:29], v[134:137], v[182:185], v[26:29]
	v_mfma_f32_16x16x32_bf16 v[30:33], v[142:145], v[182:185], v[30:33]
	v_mfma_f32_16x16x32_bf16 v[10:13], v[134:137], v[214:217], v[10:13]
	v_mfma_f32_16x16x32_bf16 v[14:17], v[142:145], v[214:217], v[14:17]
	s_setprio 0
	s_setprio 1
	v_mfma_f32_16x16x32_bf16 v[50:53], v[146:149], v[162:165], v[50:53]
	v_mfma_f32_16x16x32_bf16 v[54:57], v[154:157], v[162:165], v[54:57]
	v_mfma_f32_16x16x32_bf16 v[34:37], v[146:149], v[170:173], v[34:37]
	v_mfma_f32_16x16x32_bf16 v[38:41], v[154:157], v[170:173], v[38:41]
	v_mfma_f32_16x16x32_bf16 v[18:21], v[146:149], v[178:181], v[18:21]
	v_mfma_f32_16x16x32_bf16 v[22:25], v[154:157], v[178:181], v[22:25]
	v_mfma_f32_16x16x32_bf16 v[2:5], v[146:149], v[210:213], v[2:5]
	v_mfma_f32_16x16x32_bf16 v[6:9], v[154:157], v[210:213], v[6:9]
	s_setprio 0
	s_setprio 1
	v_mfma_f32_16x16x32_bf16 v[50:53], v[150:153], v[166:169], v[50:53]
	v_mfma_f32_16x16x32_bf16 v[54:57], v[158:161], v[166:169], v[54:57]
	v_mfma_f32_16x16x32_bf16 v[34:37], v[150:153], v[174:177], v[34:37]
	v_mfma_f32_16x16x32_bf16 v[38:41], v[158:161], v[174:177], v[38:41]
	v_mfma_f32_16x16x32_bf16 v[18:21], v[150:153], v[182:185], v[18:21]
	v_mfma_f32_16x16x32_bf16 v[22:25], v[158:161], v[182:185], v[22:25]
	v_mfma_f32_16x16x32_bf16 v[2:5], v[150:153], v[214:217], v[2:5]
	v_mfma_f32_16x16x32_bf16 v[6:9], v[158:161], v[214:217], v[6:9]
	s_setprio 0
	s_barrier
	s_add_i32 s52, s52, 2
	s_add_u32 s22, s22, 0x100
	s_addc_u32 s23, s23, 0
	s_add_u32 s50, s50, 0x100
	s_addc_u32 s51, s51, 0
	s_cmp_gt_u32 s52, 13
	s_cbranch_scc0 .LBB0_618
	s_and_b64 vcc, exec, s[6:7]
	s_cbranch_vccz .LBB0_621
	s_barrier

; #define PG8_STAGE(bufoff, gbase, voff) do { _Pragma("unroll") for (int _i = 0; _i < 2; ++_i) \
;         __builtin_amdgcn_global_load_lds((const unsigned*)((const char*)(gbase) + (voff)[_i]), (LAS unsigned*)(lds + (bufoff) + ldsw + _i * 8192), 16, 0, 0); } while (0)
; #define PG8_LDA(dst, b, h) do { _Pragma("unroll") for (int m = 0; m < 4; ++m) _Pragma("unroll") for (int k = 0; k < 2; ++k) dst[m][k] = *(const LAS bf16x8*)(lds + PG8_SA(b, h) + aoff + m * 2048 + k * 1024); } while (0)
; #define PG8_LDB(dst, b, h) do { _Pragma("unroll") for (int n = 0; n < 2; ++n) _Pragma("unroll") for (int k = 0; k < 2; ++k) dst[n][k] = *(const LAS bf16x8*)(lds + PG8_SB(b, h) + boff + n * 2048 + k * 1024); } while (0)
; #define PG8_MMA(ai, bj, At, Bt) do { __builtin_amdgcn_s_setprio(1); _Pragma("unroll") for (int m = 0; m < 4; ++m) _Pragma("unroll") for (int n = 0; n < 2; ++n) _Pragma("unroll") for (int k = 0; k < 2; ++k) \
;         acc[ai][bj][m][n] = __builtin_amdgcn_mfma_f32_16x16x32_bf16(Bt[n][k], At[m][k], acc[ai][bj][m][n], 0, 0, 0); __builtin_amdgcn_s_setprio(0); } while (0)
; #define PG8_WAIT_V(n) asm volatile("s_waitcnt vmcnt(" #n ")" ::: "memory")
; #define PG8_WAIT_L(n) asm volatile("s_waitcnt lgkmcnt(" #n ")" ::: "memory")
; #define PG8_BAR __builtin_amdgcn_s_barrier()
; template <class Epi, class Sched>
; __device__ __forceinline__ void gemm_phase(LAS unsigned char* lds, const Gemm g, const Sched& S, const Epi& E, const int tid, unsigned* last_sig = nullptr) {
;     ...
;         for (int t = 0; t < nt; t += 2) {
;             const bool last = (t == nt - 2);
;             const char* a1 = cA + (size_t)(t + 1) * kstep;
;             const char* a2 = last ? nA : cA + (size_t)(t + 2) * kstep; const char* b2 = last ? nB : cB + (size_t)(t + 2) * kstep;
;             const char* a3 = a2 + kstep; const char* b3 = b2 + kstep;
;             PG8_LDB(B0, 0, 0); PG8_LDB(B1, 0, 1); PG8_SCHED; PG8_LDA(At, 0, 0); PG8_STAGE(PG8_SA(1, 1), a1 + hstep, voffA);
;             PG8_WAIT_V(8); PG8_WAIT_L(0); PG8_BAR; PG8_MMA(0, 0, At, B0); PG8_MMA(0, 1, At, B1); PG8_BAR; PG8_SCHED;
;             PG8_LDA(At, 0, 1); PG8_STAGE(PG8_SB(0, 0), b2, voffB); PG8_STAGE(PG8_SB(0, 1), b2 + hstep, voffB); PG8_STAGE(PG8_SA(0, 0), a2, voffA);
;             PG8_WAIT_V(8); PG8_WAIT_L(0); PG8_BAR; PG8_MMA(1, 0, At, B0); PG8_MMA(1, 1, At, B1); PG8_BAR; PG8_SCHED;
.LBB0_691:
	s_add_u32 s22, s20, 0x100
	s_addc_u32 s23, s21, 0
	s_add_i32 s14, 0, 0x10000
	s_cmp_eq_u32 s56, 28
	s_cselect_b32 s41, s13, s23
	s_cselect_b32 s40, s52, s22
	s_cselect_b32 s39, s11, s55
	s_cselect_b32 s38, s53, s54
	s_add_i32 s57, 0, 0x14000
	v_add_u32_e32 v148, s14, v156
	v_add_u32_e32 v159, s57, v156
	ds_read_b128 v[130:133], v148
	ds_read_b128 v[134:137], v148 offset:1024
	ds_read_b128 v[138:141], v148 offset:2048
	ds_read_b128 v[148:151], v148 offset:3072
	ds_read_b128 v[152:155], v159
	ds_read_b128 v[160:163], v159 offset:1024
	ds_read_b128 v[164:167], v159 offset:2048
	ds_read_b128 v[168:171], v159 offset:3072
	v_lshl_add_u64 v[184:185], s[20:21], 0, v[144:145]
	s_add_i32 m0, s43, 0xc000
	ds_read_b128 v[172:175], v158
	ds_read_b128 v[176:179], v158 offset:1024
	ds_read_b128 v[180:183], v158 offset:2048
	ds_read_b128 v[200:203], v158 offset:3072
	ds_read_b128 v[204:207], v158 offset:4096
	ds_read_b128 v[208:211], v158 offset:5120
	ds_read_b128 v[212:215], v158 offset:6144
	ds_read_b128 v[216:219], v158 offset:7168
	global_load_lds_dwordx4 v[184:185], off
	v_lshl_add_u64 v[184:185], s[20:21], 0, v[146:147]
	s_add_i32 m0, s43, 0xe000
	s_nop 0
	global_load_lds_dwordx4 v[184:185], off
	s_waitcnt vmcnt(8)
	s_waitcnt lgkmcnt(0)
	s_barrier
	s_setprio 1
	s_waitcnt lgkmcnt(0)
	v_mfma_f32_16x16x32_bf16 v[126:129], v[130:133], v[172:175], v[126:129]
	v_mfma_f32_16x16x32_bf16 v[122:125], v[138:141], v[172:175], v[122:125]
	v_mfma_f32_16x16x32_bf16 v[118:121], v[130:133], v[180:183], v[118:121]
	v_mfma_f32_16x16x32_bf16 v[106:109], v[138:141], v[180:183], v[106:109]
	v_mfma_f32_16x16x32_bf16 v[102:105], v[130:133], v[204:207], v[102:105]
	v_mfma_f32_16x16x32_bf16 v[90:93], v[138:141], v[204:207], v[90:93]
	v_mfma_f32_16x16x32_bf16 v[86:89], v[130:133], v[212:215], v[86:89]
	v_mfma_f32_16x16x32_bf16 v[74:77], v[138:141], v[212:215], v[74:77]
	s_setprio 0
	s_setprio 1
	v_mfma_f32_16x16x32_bf16 v[126:129], v[134:137], v[176:179], v[126:129]
	v_mfma_f32_16x16x32_bf16 v[122:125], v[148:151], v[176:179], v[122:125]
	v_mfma_f32_16x16x32_bf16 v[118:121], v[134:137], v[200:203], v[118:121]
	v_mfma_f32_16x16x32_bf16 v[106:109], v[148:151], v[200:203], v[106:109]
	v_mfma_f32_16x16x32_bf16 v[102:105], v[134:137], v[208:211], v[102:105]
	v_mfma_f32_16x16x32_bf16 v[90:93], v[148:151], v[208:211], v[90:93]
	v_mfma_f32_16x16x32_bf16 v[86:89], v[134:137], v[216:219], v[86:89]
	v_mfma_f32_16x16x32_bf16 v[74:77], v[148:151], v[216:219], v[74:77]
	s_setprio 0
	s_setprio 1
	v_mfma_f32_16x16x32_bf16 v[114:117], v[152:155], v[172:175], v[114:117]
	v_mfma_f32_16x16x32_bf16 v[110:113], v[164:167], v[172:175], v[110:113]
	v_mfma_f32_16x16x32_bf16 v[98:101], v[152:155], v[180:183], v[98:101]
	v_mfma_f32_16x16x32_bf16 v[94:97], v[164:167], v[180:183], v[94:97]
	v_mfma_f32_16x16x32_bf16 v[82:85], v[152:155], v[204:207], v[82:85]
	v_mfma_f32_16x16x32_bf16 v[78:81], v[164:167], v[204:207], v[78:81]
	v_mfma_f32_16x16x32_bf16 v[70:73], v[152:155], v[212:215], v[70:73]
	v_mfma_f32_16x16x32_bf16 v[66:69], v[164:167], v[212:215], v[66:69]
	s_setprio 0
	s_setprio 1
	v_mfma_f32_16x16x32_bf16 v[114:117], v[160:163], v[176:179], v[114:117]
	v_mfma_f32_16x16x32_bf16 v[110:113], v[168:171], v[176:179], v[110:113]
	v_mfma_f32_16x16x32_bf16 v[98:101], v[160:163], v[200:203], v[98:101]
	v_mfma_f32_16x16x32_bf16 v[94:97], v[168:171], v[200:203], v[94:97]
	v_mfma_f32_16x16x32_bf16 v[82:85], v[160:163], v[208:211], v[82:85]
	v_mfma_f32_16x16x32_bf16 v[78:81], v[168:171], v[208:211], v[78:81]
	v_mfma_f32_16x16x32_bf16 v[70:73], v[160:163], v[216:219], v[70:73]
	v_mfma_f32_16x16x32_bf16 v[66:69], v[168:171], v[216:219], v[66:69]
	s_setprio 0
	s_barrier
	s_add_i32 s14, s14, s42
	v_lshl_add_u64 v[184:185], s[38:39], 0, v[186:187]
	s_mov_b32 m0, s14
	ds_read_b128 v[172:175], v158 offset:16384
	ds_read_b128 v[176:179], v158 offset:17408
	ds_read_b128 v[180:183], v158 offset:18432
	ds_read_b128 v[200:203], v158 offset:19456
	ds_read_b128 v[204:207], v158 offset:20480
	ds_read_b128 v[208:211], v158 offset:21504
	ds_read_b128 v[212:215], v158 offset:22528
	ds_read_b128 v[216:219], v158 offset:23552
	global_load_lds_dwordx4 v[184:185], off
	s_add_i32 m0, s14, 0x2000
	s_add_u32 s14, s38, 0x80000
	v_lshl_add_u64 v[220:221], s[38:39], 0, v[142:143]
	s_addc_u32 s15, s39, 0
	s_add_i32 s20, s57, s42
	global_load_lds_dwordx4 v[220:221], off
	v_lshl_add_u64 v[222:223], s[14:15], 0, v[186:187]
	s_mov_b32 m0, s20
	v_lshl_add_u64 v[232:233], s[40:41], 0, v[142:143]
	global_load_lds_dwordx4 v[222:223], off
	v_lshl_add_u64 v[222:223], s[14:15], 0, v[142:143]
	s_add_i32 m0, s20, 0x2000
	s_nop 0
	global_load_lds_dwordx4 v[222:223], off
	v_lshl_add_u64 v[222:223], s[40:41], 0, v[186:187]
	s_mov_b32 m0, s43
	s_nop 0
	global_load_lds_dwordx4 v[222:223], off
	s_mov_b32 m0, s44
	s_nop 0
	global_load_lds_dwordx4 v[232:233], off
	s_waitcnt vmcnt(8)
	s_waitcnt lgkmcnt(0)
	s_barrier
; #define PG8_STAGE(bufoff, gbase, voff) do { _Pragma("unroll") for (int _i = 0; _i < 2; ++_i) \
;         __builtin_amdgcn_global_load_lds((const unsigned*)((const char*)(gbase) + (voff)[_i]), (LAS unsigned*)(lds + (bufoff) + ldsw + _i * 8192), 16, 0, 0); } while (0)
; #define PG8_LDA(dst, b, h) do { _Pragma("unroll") for (int m = 0; m < 4; ++m) _Pragma("unroll") for (int k = 0; k < 2; ++k) dst[m][k] = *(const LAS bf16x8*)(lds + PG8_SA(b, h) + aoff + m * 2048 + k * 1024); } while (0)
; #define PG8_LDB(dst, b, h) do { _Pragma("unroll") for (int n = 0; n < 2; ++n) _Pragma("unroll") for (int k = 0; k < 2; ++k) dst[n][k] = *(const LAS bf16x8*)(lds + PG8_SB(b, h) + boff + n * 2048 + k * 1024); } while (0)
; #define PG8_MMA(ai, bj, At, Bt) do { __builtin_amdgcn_s_setprio(1); _Pragma("unroll") for (int m = 0; m < 4; ++m) _Pragma("unroll") for (int n = 0; n < 2; ++n) _Pragma("unroll") for (int k = 0; k < 2; ++k) \
;         acc[ai][bj][m][n] = __builtin_amdgcn_mfma_f32_16x16x32_bf16(Bt[n][k], At[m][k], acc[ai][bj][m][n], 0, 0, 0); __builtin_amdgcn_s_setprio(0); } while (0)
; #define PG8_WAIT_V(n) asm volatile("s_waitcnt vmcnt(" #n ")" ::: "memory")
; #define PG8_WAIT_L(n) asm volatile("s_waitcnt lgkmcnt(" #n ")" ::: "memory")
; #define PG8_BAR __builtin_amdgcn_s_barrier()
; #define PG8_SCHED __builtin_amdgcn_sched_barrier(0)
; template <class Epi, class Sched>
; __device__ __forceinline__ void gemm_phase(LAS unsigned char* lds, const Gemm g, const Sched& S, const Epi& E, const int tid, unsigned* last_sig = nullptr) {
;     ...
;             PG8_WAIT_V(8); PG8_WAIT_L(0); PG8_BAR; PG8_MMA(1, 0, At, B0); PG8_MMA(1, 1, At, B1); PG8_BAR; PG8_SCHED;
;             PG8_LDB(B0, 1, 0); PG8_LDB(B1, 1, 1); PG8_SCHED; PG8_LDA(At, 1, 0); PG8_STAGE(PG8_SA(0, 1), a2 + hstep, voffA);
;             PG8_WAIT_V(8); PG8_WAIT_L(0); PG8_BAR; PG8_MMA(0, 0, At, B0); PG8_MMA(0, 1, At, B1); PG8_BAR; PG8_SCHED;
	s_setprio 1
	s_waitcnt lgkmcnt(0)
	v_mfma_f32_16x16x32_bf16 v[62:65], v[130:133], v[172:175], v[62:65]
	v_mfma_f32_16x16x32_bf16 v[58:61], v[138:141], v[172:175], v[58:61]
	v_mfma_f32_16x16x32_bf16 v[54:57], v[130:133], v[180:183], v[54:57]
	v_mfma_f32_16x16x32_bf16 v[42:45], v[138:141], v[180:183], v[42:45]
	v_mfma_f32_16x16x32_bf16 v[38:41], v[130:133], v[204:207], v[38:41]
	v_mfma_f32_16x16x32_bf16 v[26:29], v[138:141], v[204:207], v[26:29]
	v_mfma_f32_16x16x32_bf16 v[22:25], v[130:133], v[212:215], v[22:25]
	v_mfma_f32_16x16x32_bf16 v[10:13], v[138:141], v[212:215], v[10:13]
	s_setprio 0
	s_setprio 1
	v_mfma_f32_16x16x32_bf16 v[62:65], v[134:137], v[176:179], v[62:65]
	v_mfma_f32_16x16x32_bf16 v[58:61], v[148:151], v[176:179], v[58:61]
	v_mfma_f32_16x16x32_bf16 v[54:57], v[134:137], v[200:203], v[54:57]
	v_mfma_f32_16x16x32_bf16 v[42:45], v[148:151], v[200:203], v[42:45]
	v_mfma_f32_16x16x32_bf16 v[38:41], v[134:137], v[208:211], v[38:41]
	v_mfma_f32_16x16x32_bf16 v[26:29], v[148:151], v[208:211], v[26:29]
	v_mfma_f32_16x16x32_bf16 v[22:25], v[134:137], v[216:219], v[22:25]
	v_mfma_f32_16x16x32_bf16 v[10:13], v[148:151], v[216:219], v[10:13]
	s_setprio 0
	s_setprio 1
	v_mfma_f32_16x16x32_bf16 v[50:53], v[152:155], v[172:175], v[50:53]
	v_mfma_f32_16x16x32_bf16 v[46:49], v[164:167], v[172:175], v[46:49]
	v_mfma_f32_16x16x32_bf16 v[34:37], v[152:155], v[180:183], v[34:37]
	v_mfma_f32_16x16x32_bf16 v[30:33], v[164:167], v[180:183], v[30:33]
	v_mfma_f32_16x16x32_bf16 v[18:21], v[152:155], v[204:207], v[18:21]
	v_mfma_f32_16x16x32_bf16 v[14:17], v[164:167], v[204:207], v[14:17]
	v_mfma_f32_16x16x32_bf16 v[6:9], v[152:155], v[212:215], v[6:9]
	v_mfma_f32_16x16x32_bf16 v[2:5], v[164:167], v[212:215], v[2:5]
	s_setprio 0
	s_setprio 1
	v_mfma_f32_16x16x32_bf16 v[50:53], v[160:163], v[176:179], v[50:53]
	v_mfma_f32_16x16x32_bf16 v[46:49], v[168:171], v[176:179], v[46:49]
	v_mfma_f32_16x16x32_bf16 v[34:37], v[160:163], v[200:203], v[34:37]
	v_mfma_f32_16x16x32_bf16 v[30:33], v[168:171], v[200:203], v[30:33]
	v_mfma_f32_16x16x32_bf16 v[18:21], v[160:163], v[208:211], v[18:21]
	v_mfma_f32_16x16x32_bf16 v[14:17], v[168:171], v[208:211], v[14:17]
	v_mfma_f32_16x16x32_bf16 v[6:9], v[160:163], v[216:219], v[6:9]
	v_mfma_f32_16x16x32_bf16 v[2:5], v[168:171], v[216:219], v[2:5]
	s_setprio 0
	s_barrier
	s_add_i32 s20, 0, 0x18000
	s_add_i32 s21, 0, 0x1c000
	v_add_u32_e32 v148, s20, v156
	v_add_u32_e32 v159, s21, v156
	ds_read_b128 v[130:133], v148
	ds_read_b128 v[134:137], v148 offset:1024
	ds_read_b128 v[138:141], v148 offset:2048
	ds_read_b128 v[148:151], v148 offset:3072
	ds_read_b128 v[152:155], v159
	ds_read_b128 v[160:163], v159 offset:1024
	ds_read_b128 v[164:167], v159 offset:2048
	ds_read_b128 v[168:171], v159 offset:3072
	s_add_u32 s14, s40, 0x80000
	s_addc_u32 s15, s41, 0
	s_mov_b32 m0, s45
	v_lshl_add_u64 v[234:235], s[14:15], 0, v[186:187]
	ds_read_b128 v[172:175], v158 offset:32768
	ds_read_b128 v[176:179], v158 offset:33792
	ds_read_b128 v[180:183], v158 offset:34816
	ds_read_b128 v[200:203], v158 offset:35840
	ds_read_b128 v[204:207], v158 offset:36864
	ds_read_b128 v[208:211], v158 offset:37888
	ds_read_b128 v[212:215], v158 offset:38912
	ds_read_b128 v[216:219], v158 offset:39936
	global_load_lds_dwordx4 v[234:235], off
	v_lshl_add_u64 v[234:235], s[14:15], 0, v[142:143]
	s_mov_b32 m0, s46
	s_nop 0
	global_load_lds_dwordx4 v[234:235], off
	s_waitcnt vmcnt(8)
	s_waitcnt lgkmcnt(0)
	s_barrier
	s_setprio 1
	s_waitcnt lgkmcnt(0)
	v_mfma_f32_16x16x32_bf16 v[126:129], v[130:133], v[172:175], v[126:129]
	v_mfma_f32_16x16x32_bf16 v[122:125], v[138:141], v[172:175], v[122:125]
	v_mfma_f32_16x16x32_bf16 v[118:121], v[130:133], v[180:183], v[118:121]
	v_mfma_f32_16x16x32_bf16 v[106:109], v[138:141], v[180:183], v[106:109]
	v_mfma_f32_16x16x32_bf16 v[102:105], v[130:133], v[204:207], v[102:105]
	v_mfma_f32_16x16x32_bf16 v[90:93], v[138:141], v[204:207], v[90:93]
	v_mfma_f32_16x16x32_bf16 v[86:89], v[130:133], v[212:215], v[86:89]
	v_mfma_f32_16x16x32_bf16 v[74:77], v[138:141], v[212:215], v[74:77]
	s_setprio 0
	s_setprio 1
	v_mfma_f32_16x16x32_bf16 v[126:129], v[134:137], v[176:179], v[126:129]
	v_mfma_f32_16x16x32_bf16 v[122:125], v[148:151], v[176:179], v[122:125]
	v_mfma_f32_16x16x32_bf16 v[118:121], v[134:137], v[200:203], v[118:121]
	v_mfma_f32_16x16x32_bf16 v[106:109], v[148:151], v[200:203], v[106:109]
	v_mfma_f32_16x16x32_bf16 v[102:105], v[134:137], v[208:211], v[102:105]
	v_mfma_f32_16x16x32_bf16 v[90:93], v[148:151], v[208:211], v[90:93]
	v_mfma_f32_16x16x32_bf16 v[86:89], v[134:137], v[216:219], v[86:89]
	v_mfma_f32_16x16x32_bf16 v[74:77], v[148:151], v[216:219], v[74:77]
	s_setprio 0
	s_setprio 1
	v_mfma_f32_16x16x32_bf16 v[114:117], v[152:155], v[172:175], v[114:117]
	v_mfma_f32_16x16x32_bf16 v[110:113], v[164:167], v[172:175], v[110:113]
	v_mfma_f32_16x16x32_bf16 v[98:101], v[152:155], v[180:183], v[98:101]
	v_mfma_f32_16x16x32_bf16 v[94:97], v[164:167], v[180:183], v[94:97]
	v_mfma_f32_16x16x32_bf16 v[82:85], v[152:155], v[204:207], v[82:85]
	v_mfma_f32_16x16x32_bf16 v[78:81], v[164:167], v[204:207], v[78:81]
	v_mfma_f32_16x16x32_bf16 v[70:73], v[152:155], v[212:215], v[70:73]
	v_mfma_f32_16x16x32_bf16 v[66:69], v[164:167], v[212:215], v[66:69]
	s_setprio 0
	s_setprio 1
	v_mfma_f32_16x16x32_bf16 v[114:117], v[160:163], v[176:179], v[114:117]
	v_mfma_f32_16x16x32_bf16 v[110:113], v[168:171], v[176:179], v[110:113]
	v_mfma_f32_16x16x32_bf16 v[98:101], v[160:163], v[200:203], v[98:101]
	v_mfma_f32_16x16x32_bf16 v[94:97], v[168:171], v[200:203], v[94:97]
	v_mfma_f32_16x16x32_bf16 v[82:85], v[160:163], v[208:211], v[82:85]
	v_mfma_f32_16x16x32_bf16 v[78:81], v[168:171], v[208:211], v[78:81]
	v_mfma_f32_16x16x32_bf16 v[70:73], v[160:163], v[216:219], v[70:73]
	v_mfma_f32_16x16x32_bf16 v[66:69], v[168:171], v[216:219], v[66:69]
	s_setprio 0
	s_barrier
; #define PG8_STAGE(bufoff, gbase, voff) do { _Pragma("unroll") for (int _i = 0; _i < 2; ++_i) \
;         __builtin_amdgcn_global_load_lds((const unsigned*)((const char*)(gbase) + (voff)[_i]), (LAS unsigned*)(lds + (bufoff) + ldsw + _i * 8192), 16, 0, 0); } while (0)
; #define PG8_LDA(dst, b, h) do { _Pragma("unroll") for (int m = 0; m < 4; ++m) _Pragma("unroll") for (int k = 0; k < 2; ++k) dst[m][k] = *(const LAS bf16x8*)(lds + PG8_SA(b, h) + aoff + m * 2048 + k * 1024); } while (0)
; #define PG8_MMA(ai, bj, At, Bt) do { __builtin_amdgcn_s_setprio(1); _Pragma("unroll") for (int m = 0; m < 4; ++m) _Pragma("unroll") for (int n = 0; n < 2; ++n) _Pragma("unroll") for (int k = 0; k < 2; ++k) \
;         acc[ai][bj][m][n] = __builtin_amdgcn_mfma_f32_16x16x32_bf16(Bt[n][k], At[m][k], acc[ai][bj][m][n], 0, 0, 0); __builtin_amdgcn_s_setprio(0); } while (0)
; #define PG8_WAIT_V(n) asm volatile("s_waitcnt vmcnt(" #n ")" ::: "memory")
; #define PG8_WAIT_L(n) asm volatile("s_waitcnt lgkmcnt(" #n ")" ::: "memory")
; #define PG8_BAR __builtin_amdgcn_s_barrier()
; #define PG8_SCHED __builtin_amdgcn_sched_barrier(0)
; template <class Epi, class Sched>
; __device__ __forceinline__ void gemm_phase(LAS unsigned char* lds, const Gemm g, const Sched& S, const Epi& E, const int tid, unsigned* last_sig = nullptr) {
;     ...
;             PG8_LDA(At, 1, 1); PG8_STAGE(PG8_SB(1, 0), b3, voffB); PG8_STAGE(PG8_SB(1, 1), b3 + hstep, voffB); PG8_STAGE(PG8_SA(1, 0), a3, voffA);
;             PG8_WAIT_V(8); PG8_WAIT_L(0); PG8_BAR; PG8_MMA(1, 0, At, B0); PG8_MMA(1, 1, At, B1); PG8_BAR; PG8_SCHED;
;         }
;         if (wr == 0) PG8_BAR;
	s_add_i32 s14, s20, s42
	v_lshl_add_u64 v[184:185], v[184:185], 0, s[34:35]
	s_mov_b32 m0, s14
	ds_read_b128 v[172:175], v158 offset:49152
	ds_read_b128 v[176:179], v158 offset:50176
	ds_read_b128 v[180:183], v158 offset:51200
	ds_read_b128 v[200:203], v158 offset:52224
	ds_read_b128 v[204:207], v158 offset:53248
	ds_read_b128 v[208:211], v158 offset:54272
	ds_read_b128 v[212:215], v158 offset:55296
	ds_read_b128 v[216:219], v158 offset:56320
	global_load_lds_dwordx4 v[184:185], off
	s_add_i32 m0, s14, 0x2000
	s_add_u32 s14, s38, 0x80080
	v_lshl_add_u64 v[184:185], v[220:221], 0, s[34:35]
	s_addc_u32 s15, s39, 0
	s_add_i32 s20, s21, s42
	global_load_lds_dwordx4 v[184:185], off
	v_lshl_add_u64 v[184:185], s[14:15], 0, v[186:187]
	s_mov_b32 m0, s20
	s_nop 0
	global_load_lds_dwordx4 v[184:185], off
	v_lshl_add_u64 v[184:185], s[14:15], 0, v[142:143]
	s_add_i32 m0, s20, 0x2000
	s_nop 0
	global_load_lds_dwordx4 v[184:185], off
	v_lshl_add_u64 v[184:185], v[222:223], 0, s[34:35]
	s_mov_b32 m0, s47
	s_nop 0
	global_load_lds_dwordx4 v[184:185], off
	v_lshl_add_u64 v[184:185], v[232:233], 0, s[34:35]
	s_mov_b32 m0, s48
	s_nop 0
	global_load_lds_dwordx4 v[184:185], off
	s_waitcnt vmcnt(8)
	s_waitcnt lgkmcnt(0)
	s_barrier
	s_setprio 1
	s_waitcnt lgkmcnt(0)
	v_mfma_f32_16x16x32_bf16 v[62:65], v[130:133], v[172:175], v[62:65]
	v_mfma_f32_16x16x32_bf16 v[58:61], v[138:141], v[172:175], v[58:61]
	v_mfma_f32_16x16x32_bf16 v[54:57], v[130:133], v[180:183], v[54:57]
	v_mfma_f32_16x16x32_bf16 v[42:45], v[138:141], v[180:183], v[42:45]
	v_mfma_f32_16x16x32_bf16 v[38:41], v[130:133], v[204:207], v[38:41]
	v_mfma_f32_16x16x32_bf16 v[26:29], v[138:141], v[204:207], v[26:29]
	v_mfma_f32_16x16x32_bf16 v[22:25], v[130:133], v[212:215], v[22:25]
	v_mfma_f32_16x16x32_bf16 v[10:13], v[138:141], v[212:215], v[10:13]
	s_setprio 0
	s_setprio 1
	v_mfma_f32_16x16x32_bf16 v[62:65], v[134:137], v[176:179], v[62:65]
	v_mfma_f32_16x16x32_bf16 v[58:61], v[148:151], v[176:179], v[58:61]
	v_mfma_f32_16x16x32_bf16 v[54:57], v[134:137], v[200:203], v[54:57]
	v_mfma_f32_16x16x32_bf16 v[42:45], v[148:151], v[200:203], v[42:45]
	v_mfma_f32_16x16x32_bf16 v[38:41], v[134:137], v[208:211], v[38:41]
	v_mfma_f32_16x16x32_bf16 v[26:29], v[148:151], v[208:211], v[26:29]
	v_mfma_f32_16x16x32_bf16 v[22:25], v[134:137], v[216:219], v[22:25]
	v_mfma_f32_16x16x32_bf16 v[10:13], v[148:151], v[216:219], v[10:13]
	s_setprio 0
	s_setprio 1
	v_mfma_f32_16x16x32_bf16 v[50:53], v[152:155], v[172:175], v[50:53]
	v_mfma_f32_16x16x32_bf16 v[46:49], v[164:167], v[172:175], v[46:49]
	v_mfma_f32_16x16x32_bf16 v[34:37], v[152:155], v[180:183], v[34:37]
	v_mfma_f32_16x16x32_bf16 v[30:33], v[164:167], v[180:183], v[30:33]
	v_mfma_f32_16x16x32_bf16 v[18:21], v[152:155], v[204:207], v[18:21]
	v_mfma_f32_16x16x32_bf16 v[14:17], v[164:167], v[204:207], v[14:17]
	v_mfma_f32_16x16x32_bf16 v[6:9], v[152:155], v[212:215], v[6:9]
	v_mfma_f32_16x16x32_bf16 v[2:5], v[164:167], v[212:215], v[2:5]
	s_setprio 0
	s_setprio 1
	v_mfma_f32_16x16x32_bf16 v[50:53], v[160:163], v[176:179], v[50:53]
	v_mfma_f32_16x16x32_bf16 v[46:49], v[168:171], v[176:179], v[46:49]
	v_mfma_f32_16x16x32_bf16 v[34:37], v[160:163], v[200:203], v[34:37]
	v_mfma_f32_16x16x32_bf16 v[30:33], v[168:171], v[200:203], v[30:33]
	v_mfma_f32_16x16x32_bf16 v[18:21], v[160:163], v[208:211], v[18:21]
	v_mfma_f32_16x16x32_bf16 v[14:17], v[168:171], v[208:211], v[14:17]
	v_mfma_f32_16x16x32_bf16 v[6:9], v[160:163], v[216:219], v[6:9]
	v_mfma_f32_16x16x32_bf16 v[2:5], v[168:171], v[216:219], v[2:5]
	s_setprio 0
	s_barrier
	s_add_i32 s56, s56, 2
	s_add_u32 s54, s54, 0x100
	s_addc_u32 s55, s55, 0
	s_cmp_gt_u32 s56, 29
	s_mov_b64 s[20:21], s[22:23]
	s_cbranch_scc0 .LBB0_691
	s_and_b64 vcc, exec, s[8:9]
	s_cbranch_vccz .LBB0_694
	s_barrier

; #define PG8_STAGE(bufoff, gbase, voff) do { _Pragma("unroll") for (int _i = 0; _i < 2; ++_i) \
;         __builtin_amdgcn_global_load_lds((const unsigned*)((const char*)(gbase) + (voff)[_i]), (LAS unsigned*)(lds + (bufoff) + ldsw + _i * 8192), 16, 0, 0); } while (0)
; #define PG8_LDA(dst, b, h) do { _Pragma("unroll") for (int m = 0; m < 4; ++m) _Pragma("unroll") for (int k = 0; k < 2; ++k) dst[m][k] = *(const LAS bf16x8*)(lds + PG8_SA(b, h) + aoff + m * 2048 + k * 1024); } while (0)
; #define PG8_LDB(dst, b, h) do { _Pragma("unroll") for (int n = 0; n < 2; ++n) _Pragma("unroll") for (int k = 0; k < 2; ++k) dst[n][k] = *(const LAS bf16x8*)(lds + PG8_SB(b, h) + boff + n * 2048 + k * 1024); } while (0)
; #define PG8_MMA(ai, bj, At, Bt) do { __builtin_amdgcn_s_setprio(1); _Pragma("unroll") for (int m = 0; m < 4; ++m) _Pragma("unroll") for (int n = 0; n < 2; ++n) _Pragma("unroll") for (int k = 0; k < 2; ++k) \
;         acc[ai][bj][m][n] = __builtin_amdgcn_mfma_f32_16x16x32_bf16(Bt[n][k], At[m][k], acc[ai][bj][m][n], 0, 0, 0); __builtin_amdgcn_s_setprio(0); } while (0)
; #define PG8_WAIT_V(n) asm volatile("s_waitcnt vmcnt(" #n ")" ::: "memory")
; #define PG8_WAIT_L(n) asm volatile("s_waitcnt lgkmcnt(" #n ")" ::: "memory")
; #define PG8_BAR __builtin_amdgcn_s_barrier()
; template <class Epi, class Sched>
; __device__ __forceinline__ void gemm_phase(LAS unsigned char* lds, const Gemm g, const Sched& S, const Epi& E, const int tid, unsigned* last_sig = nullptr) {
;     ...
;         for (int t = 0; t < nt; t += 2) {
;             const bool last = (t == nt - 2);
;             const char* a1 = cA + (size_t)(t + 1) * kstep;
;             const char* a2 = last ? nA : cA + (size_t)(t + 2) * kstep; const char* b2 = last ? nB : cB + (size_t)(t + 2) * kstep;
;             const char* a3 = a2 + kstep; const char* b3 = b2 + kstep;
;             PG8_LDB(B0, 0, 0); PG8_LDB(B1, 0, 1); PG8_SCHED; PG8_LDA(At, 0, 0); PG8_STAGE(PG8_SA(1, 1), a1 + hstep, voffA);
;             PG8_WAIT_V(8); PG8_WAIT_L(0); PG8_BAR; PG8_MMA(0, 0, At, B0); PG8_MMA(0, 1, At, B1); PG8_BAR; PG8_SCHED;
;             PG8_LDA(At, 0, 1); PG8_STAGE(PG8_SB(0, 0), b2, voffB); PG8_STAGE(PG8_SB(0, 1), b2 + hstep, voffB); PG8_STAGE(PG8_SA(0, 0), a2, voffA);
;             PG8_WAIT_V(8); PG8_WAIT_L(0); PG8_BAR; PG8_MMA(1, 0, At, B0); PG8_MMA(1, 1, At, B1); PG8_BAR; PG8_SCHED;
.LBB0_1104:
	s_add_u32 s14, s4, 0xfff80080
	s_addc_u32 s15, s5, -1
	s_add_i32 s59, 0, 0x10000
	s_cmp_eq_u32 s58, 28
	s_cselect_b32 s47, s17, s15
	s_cselect_b32 s46, s19, s14
	v_add_u32_e32 v140, s59, v143
	s_cselect_b32 s45, s21, s57
	s_cselect_b32 s44, s20, s56
	s_add_i32 s60, 0, 0x14000
	ds_read_b128 v[146:149], v140
	ds_read_b128 v[150:153], v140 offset:1024
	ds_read_b128 v[154:157], v140 offset:2048
	ds_read_b128 v[158:161], v140 offset:3072
	v_add_u32_e32 v140, s60, v143
	ds_read_b128 v[162:165], v140
	ds_read_b128 v[166:169], v140 offset:1024
	ds_read_b128 v[170:173], v140 offset:2048
	ds_read_b128 v[174:177], v140 offset:3072
	v_lshl_add_u64 v[140:141], s[4:5], 0, v[136:137]
	s_add_i32 m0, s41, 0xc000
	ds_read_b128 v[178:181], v145
	ds_read_b128 v[182:185], v145 offset:1024
	ds_read_b128 v[200:203], v145 offset:2048
	ds_read_b128 v[204:207], v145 offset:3072
	ds_read_b128 v[208:211], v145 offset:4096
	ds_read_b128 v[212:215], v145 offset:5120
	ds_read_b128 v[216:219], v145 offset:6144
	ds_read_b128 v[220:223], v145 offset:7168
	global_load_lds_dwordx4 v[140:141], off
	v_lshl_add_u64 v[140:141], s[4:5], 0, v[138:139]
	s_add_i32 m0, s41, 0xe000
	s_nop 0
	global_load_lds_dwordx4 v[140:141], off
	s_waitcnt vmcnt(8)
	s_waitcnt lgkmcnt(0)
	s_barrier
	s_setprio 1
	s_waitcnt lgkmcnt(0)
	v_mfma_f32_16x16x32_bf16 v[126:129], v[146:149], v[178:181], v[126:129]
	v_mfma_f32_16x16x32_bf16 v[118:121], v[154:157], v[178:181], v[118:121]
	v_mfma_f32_16x16x32_bf16 v[110:113], v[146:149], v[200:203], v[110:113]
	v_mfma_f32_16x16x32_bf16 v[102:105], v[154:157], v[200:203], v[102:105]
	v_mfma_f32_16x16x32_bf16 v[94:97], v[146:149], v[208:211], v[94:97]
	v_mfma_f32_16x16x32_bf16 v[86:89], v[154:157], v[208:211], v[86:89]
	v_mfma_f32_16x16x32_bf16 v[78:81], v[146:149], v[216:219], v[78:81]
	v_mfma_f32_16x16x32_bf16 v[70:73], v[154:157], v[216:219], v[70:73]
	s_setprio 0
	s_setprio 1
	v_mfma_f32_16x16x32_bf16 v[126:129], v[150:153], v[182:185], v[126:129]
	v_mfma_f32_16x16x32_bf16 v[118:121], v[158:161], v[182:185], v[118:121]
	v_mfma_f32_16x16x32_bf16 v[110:113], v[150:153], v[204:207], v[110:113]
	v_mfma_f32_16x16x32_bf16 v[102:105], v[158:161], v[204:207], v[102:105]
	v_mfma_f32_16x16x32_bf16 v[94:97], v[150:153], v[212:215], v[94:97]
	v_mfma_f32_16x16x32_bf16 v[86:89], v[158:161], v[212:215], v[86:89]
	v_mfma_f32_16x16x32_bf16 v[78:81], v[150:153], v[220:223], v[78:81]
	v_mfma_f32_16x16x32_bf16 v[70:73], v[158:161], v[220:223], v[70:73]
	s_setprio 0
	s_setprio 1
	v_mfma_f32_16x16x32_bf16 v[122:125], v[162:165], v[178:181], v[122:125]
	v_mfma_f32_16x16x32_bf16 v[114:117], v[170:173], v[178:181], v[114:117]
	v_mfma_f32_16x16x32_bf16 v[106:109], v[162:165], v[200:203], v[106:109]
	v_mfma_f32_16x16x32_bf16 v[98:101], v[170:173], v[200:203], v[98:101]
	v_mfma_f32_16x16x32_bf16 v[90:93], v[162:165], v[208:211], v[90:93]
	v_mfma_f32_16x16x32_bf16 v[82:85], v[170:173], v[208:211], v[82:85]
	v_mfma_f32_16x16x32_bf16 v[74:77], v[162:165], v[216:219], v[74:77]
	v_mfma_f32_16x16x32_bf16 v[66:69], v[170:173], v[216:219], v[66:69]
	s_setprio 0
	s_setprio 1
	v_mfma_f32_16x16x32_bf16 v[122:125], v[166:169], v[182:185], v[122:125]
	v_mfma_f32_16x16x32_bf16 v[114:117], v[174:177], v[182:185], v[114:117]
	v_mfma_f32_16x16x32_bf16 v[106:109], v[166:169], v[204:207], v[106:109]
	v_mfma_f32_16x16x32_bf16 v[98:101], v[174:177], v[204:207], v[98:101]
	v_mfma_f32_16x16x32_bf16 v[90:93], v[166:169], v[212:215], v[90:93]
	v_mfma_f32_16x16x32_bf16 v[82:85], v[174:177], v[212:215], v[82:85]
	v_mfma_f32_16x16x32_bf16 v[74:77], v[166:169], v[220:223], v[74:77]
	v_mfma_f32_16x16x32_bf16 v[66:69], v[174:177], v[220:223], v[66:69]
	s_setprio 0
	s_barrier
	s_add_i32 s14, s59, s31
	v_lshl_add_u64 v[140:141], s[44:45], 0, v[186:187]
	s_mov_b32 m0, s14
	ds_read_b128 v[178:181], v145 offset:16384
	ds_read_b128 v[182:185], v145 offset:17408
	ds_read_b128 v[200:203], v145 offset:18432
	ds_read_b128 v[204:207], v145 offset:19456
	ds_read_b128 v[208:211], v145 offset:20480
	ds_read_b128 v[212:215], v145 offset:21504
	ds_read_b128 v[216:219], v145 offset:22528
	ds_read_b128 v[220:223], v145 offset:23552
	global_load_lds_dwordx4 v[140:141], off
	s_add_i32 m0, s14, 0x2000
	s_add_u32 s14, s44, 0x80000
	v_lshl_add_u64 v[232:233], s[44:45], 0, v[132:133]
	s_addc_u32 s15, s45, 0
	s_add_i32 s59, s60, s31
	global_load_lds_dwordx4 v[232:233], off
	v_lshl_add_u64 v[234:235], s[14:15], 0, v[186:187]
	s_mov_b32 m0, s59
	v_lshl_add_u64 v[236:237], s[46:47], 0, v[134:135]
	global_load_lds_dwordx4 v[234:235], off
	v_lshl_add_u64 v[234:235], s[14:15], 0, v[132:133]
	s_add_i32 m0, s59, 0x2000
	s_nop 0
	global_load_lds_dwordx4 v[234:235], off
	v_lshl_add_u64 v[234:235], s[46:47], 0, v[130:131]
	s_mov_b32 m0, s41
	s_nop 0
	global_load_lds_dwordx4 v[234:235], off
	s_mov_b32 m0, s43
	s_nop 0
	global_load_lds_dwordx4 v[236:237], off
	s_waitcnt vmcnt(8)
	s_waitcnt lgkmcnt(0)
	s_barrier
; #define PG8_STAGE(bufoff, gbase, voff) do { _Pragma("unroll") for (int _i = 0; _i < 2; ++_i) \
;         __builtin_amdgcn_global_load_lds((const unsigned*)((const char*)(gbase) + (voff)[_i]), (LAS unsigned*)(lds + (bufoff) + ldsw + _i * 8192), 16, 0, 0); } while (0)
; #define PG8_LDA(dst, b, h) do { _Pragma("unroll") for (int m = 0; m < 4; ++m) _Pragma("unroll") for (int k = 0; k < 2; ++k) dst[m][k] = *(const LAS bf16x8*)(lds + PG8_SA(b, h) + aoff + m * 2048 + k * 1024); } while (0)
; #define PG8_LDB(dst, b, h) do { _Pragma("unroll") for (int n = 0; n < 2; ++n) _Pragma("unroll") for (int k = 0; k < 2; ++k) dst[n][k] = *(const LAS bf16x8*)(lds + PG8_SB(b, h) + boff + n * 2048 + k * 1024); } while (0)
; #define PG8_MMA(ai, bj, At, Bt) do { __builtin_amdgcn_s_setprio(1); _Pragma("unroll") for (int m = 0; m < 4; ++m) _Pragma("unroll") for (int n = 0; n < 2; ++n) _Pragma("unroll") for (int k = 0; k < 2; ++k) \
;         acc[ai][bj][m][n] = __builtin_amdgcn_mfma_f32_16x16x32_bf16(Bt[n][k], At[m][k], acc[ai][bj][m][n], 0, 0, 0); __builtin_amdgcn_s_setprio(0); } while (0)
; #define PG8_WAIT_V(n) asm volatile("s_waitcnt vmcnt(" #n ")" ::: "memory")
; #define PG8_WAIT_L(n) asm volatile("s_waitcnt lgkmcnt(" #n ")" ::: "memory")
; #define PG8_BAR __builtin_amdgcn_s_barrier()
; #define PG8_SCHED __builtin_amdgcn_sched_barrier(0)
; template <class Epi, class Sched>
; __device__ __forceinline__ void gemm_phase(LAS unsigned char* lds, const Gemm g, const Sched& S, const Epi& E, const int tid, unsigned* last_sig = nullptr) {
;     ...
;             PG8_WAIT_V(8); PG8_WAIT_L(0); PG8_BAR; PG8_MMA(1, 0, At, B0); PG8_MMA(1, 1, At, B1); PG8_BAR; PG8_SCHED;
;             PG8_LDB(B0, 1, 0); PG8_LDB(B1, 1, 1); PG8_SCHED; PG8_LDA(At, 1, 0); PG8_STAGE(PG8_SA(0, 1), a2 + hstep, voffA);
;             PG8_WAIT_V(8); PG8_WAIT_L(0); PG8_BAR; PG8_MMA(0, 0, At, B0); PG8_MMA(0, 1, At, B1); PG8_BAR; PG8_SCHED;
	s_setprio 1
	s_waitcnt lgkmcnt(0)
	v_mfma_f32_16x16x32_bf16 v[62:65], v[146:149], v[178:181], v[62:65]
	v_mfma_f32_16x16x32_bf16 v[54:57], v[154:157], v[178:181], v[54:57]
	v_mfma_f32_16x16x32_bf16 v[46:49], v[146:149], v[200:203], v[46:49]
	v_mfma_f32_16x16x32_bf16 v[38:41], v[154:157], v[200:203], v[38:41]
	v_mfma_f32_16x16x32_bf16 v[30:33], v[146:149], v[208:211], v[30:33]
	v_mfma_f32_16x16x32_bf16 v[22:25], v[154:157], v[208:211], v[22:25]
	v_mfma_f32_16x16x32_bf16 v[14:17], v[146:149], v[216:219], v[14:17]
	v_mfma_f32_16x16x32_bf16 v[6:9], v[154:157], v[216:219], v[6:9]
	s_setprio 0
	s_setprio 1
	v_mfma_f32_16x16x32_bf16 v[62:65], v[150:153], v[182:185], v[62:65]
	v_mfma_f32_16x16x32_bf16 v[54:57], v[158:161], v[182:185], v[54:57]
	v_mfma_f32_16x16x32_bf16 v[46:49], v[150:153], v[204:207], v[46:49]
	v_mfma_f32_16x16x32_bf16 v[38:41], v[158:161], v[204:207], v[38:41]
	v_mfma_f32_16x16x32_bf16 v[30:33], v[150:153], v[212:215], v[30:33]
	v_mfma_f32_16x16x32_bf16 v[22:25], v[158:161], v[212:215], v[22:25]
	v_mfma_f32_16x16x32_bf16 v[14:17], v[150:153], v[220:223], v[14:17]
	v_mfma_f32_16x16x32_bf16 v[6:9], v[158:161], v[220:223], v[6:9]
	s_setprio 0
	s_setprio 1
	v_mfma_f32_16x16x32_bf16 v[58:61], v[162:165], v[178:181], v[58:61]
	v_mfma_f32_16x16x32_bf16 v[50:53], v[170:173], v[178:181], v[50:53]
	v_mfma_f32_16x16x32_bf16 v[42:45], v[162:165], v[200:203], v[42:45]
	v_mfma_f32_16x16x32_bf16 v[34:37], v[170:173], v[200:203], v[34:37]
	v_mfma_f32_16x16x32_bf16 v[26:29], v[162:165], v[208:211], v[26:29]
	v_mfma_f32_16x16x32_bf16 v[18:21], v[170:173], v[208:211], v[18:21]
	v_mfma_f32_16x16x32_bf16 v[10:13], v[162:165], v[216:219], v[10:13]
	v_mfma_f32_16x16x32_bf16 v[2:5], v[170:173], v[216:219], v[2:5]
	s_setprio 0
	s_setprio 1
	v_mfma_f32_16x16x32_bf16 v[58:61], v[166:169], v[182:185], v[58:61]
	v_mfma_f32_16x16x32_bf16 v[50:53], v[174:177], v[182:185], v[50:53]
	v_mfma_f32_16x16x32_bf16 v[42:45], v[166:169], v[204:207], v[42:45]
	v_mfma_f32_16x16x32_bf16 v[34:37], v[174:177], v[204:207], v[34:37]
	v_mfma_f32_16x16x32_bf16 v[26:29], v[166:169], v[212:215], v[26:29]
	v_mfma_f32_16x16x32_bf16 v[18:21], v[174:177], v[212:215], v[18:21]
	v_mfma_f32_16x16x32_bf16 v[10:13], v[166:169], v[220:223], v[10:13]
	v_mfma_f32_16x16x32_bf16 v[2:5], v[174:177], v[220:223], v[2:5]
	s_setprio 0
	s_barrier
	s_add_i32 s59, 0, 0x18000
	s_add_i32 s60, 0, 0x1c000
	v_add_u32_e32 v158, s59, v143
	v_add_u32_e32 v174, s60, v143
	ds_read_b128 v[146:149], v158
	ds_read_b128 v[150:153], v158 offset:1024
	ds_read_b128 v[154:157], v158 offset:2048
	ds_read_b128 v[158:161], v158 offset:3072
	ds_read_b128 v[162:165], v174
	ds_read_b128 v[166:169], v174 offset:1024
	ds_read_b128 v[170:173], v174 offset:2048
	ds_read_b128 v[174:177], v174 offset:3072
	s_add_u32 s14, s46, 0x80000
	s_addc_u32 s15, s47, 0
	s_mov_b32 m0, s50
	v_lshl_add_u64 v[238:239], s[14:15], 0, v[130:131]
	ds_read_b128 v[178:181], v145 offset:32768
	ds_read_b128 v[182:185], v145 offset:33792
	ds_read_b128 v[200:203], v145 offset:34816
	ds_read_b128 v[204:207], v145 offset:35840
	ds_read_b128 v[208:211], v145 offset:36864
	ds_read_b128 v[212:215], v145 offset:37888
	ds_read_b128 v[216:219], v145 offset:38912
	ds_read_b128 v[220:223], v145 offset:39936
	global_load_lds_dwordx4 v[238:239], off
	v_lshl_add_u64 v[238:239], s[14:15], 0, v[134:135]
	s_mov_b32 m0, s51
	s_nop 0
	global_load_lds_dwordx4 v[238:239], off
	s_waitcnt vmcnt(8)
	s_waitcnt lgkmcnt(0)
	s_barrier
	s_setprio 1
	s_waitcnt lgkmcnt(0)
	v_mfma_f32_16x16x32_bf16 v[126:129], v[146:149], v[178:181], v[126:129]
	v_mfma_f32_16x16x32_bf16 v[118:121], v[154:157], v[178:181], v[118:121]
	v_mfma_f32_16x16x32_bf16 v[110:113], v[146:149], v[200:203], v[110:113]
	v_mfma_f32_16x16x32_bf16 v[102:105], v[154:157], v[200:203], v[102:105]
	v_mfma_f32_16x16x32_bf16 v[94:97], v[146:149], v[208:211], v[94:97]
	v_mfma_f32_16x16x32_bf16 v[86:89], v[154:157], v[208:211], v[86:89]
	v_mfma_f32_16x16x32_bf16 v[78:81], v[146:149], v[216:219], v[78:81]
	v_mfma_f32_16x16x32_bf16 v[70:73], v[154:157], v[216:219], v[70:73]
	s_setprio 0
	s_setprio 1
	v_mfma_f32_16x16x32_bf16 v[126:129], v[150:153], v[182:185], v[126:129]
	v_mfma_f32_16x16x32_bf16 v[118:121], v[158:161], v[182:185], v[118:121]
	v_mfma_f32_16x16x32_bf16 v[110:113], v[150:153], v[204:207], v[110:113]
	v_mfma_f32_16x16x32_bf16 v[102:105], v[158:161], v[204:207], v[102:105]
	v_mfma_f32_16x16x32_bf16 v[94:97], v[150:153], v[212:215], v[94:97]
	v_mfma_f32_16x16x32_bf16 v[86:89], v[158:161], v[212:215], v[86:89]
	v_mfma_f32_16x16x32_bf16 v[78:81], v[150:153], v[220:223], v[78:81]
	v_mfma_f32_16x16x32_bf16 v[70:73], v[158:161], v[220:223], v[70:73]
	s_setprio 0
	s_setprio 1
	v_mfma_f32_16x16x32_bf16 v[122:125], v[162:165], v[178:181], v[122:125]
	v_mfma_f32_16x16x32_bf16 v[114:117], v[170:173], v[178:181], v[114:117]
	v_mfma_f32_16x16x32_bf16 v[106:109], v[162:165], v[200:203], v[106:109]
	v_mfma_f32_16x16x32_bf16 v[98:101], v[170:173], v[200:203], v[98:101]
	v_mfma_f32_16x16x32_bf16 v[90:93], v[162:165], v[208:211], v[90:93]
	v_mfma_f32_16x16x32_bf16 v[82:85], v[170:173], v[208:211], v[82:85]
	v_mfma_f32_16x16x32_bf16 v[74:77], v[162:165], v[216:219], v[74:77]
	v_mfma_f32_16x16x32_bf16 v[66:69], v[170:173], v[216:219], v[66:69]
	s_setprio 0
	s_setprio 1
	v_mfma_f32_16x16x32_bf16 v[122:125], v[166:169], v[182:185], v[122:125]
	v_mfma_f32_16x16x32_bf16 v[114:117], v[174:177], v[182:185], v[114:117]
	v_mfma_f32_16x16x32_bf16 v[106:109], v[166:169], v[204:207], v[106:109]
	v_mfma_f32_16x16x32_bf16 v[98:101], v[174:177], v[204:207], v[98:101]
	v_mfma_f32_16x16x32_bf16 v[90:93], v[166:169], v[212:215], v[90:93]
	v_mfma_f32_16x16x32_bf16 v[82:85], v[174:177], v[212:215], v[82:85]
	v_mfma_f32_16x16x32_bf16 v[74:77], v[166:169], v[220:223], v[74:77]
	v_mfma_f32_16x16x32_bf16 v[66:69], v[174:177], v[220:223], v[66:69]
	s_setprio 0
	s_barrier
; #define PG8_STAGE(bufoff, gbase, voff) do { _Pragma("unroll") for (int _i = 0; _i < 2; ++_i) \
;         __builtin_amdgcn_global_load_lds((const unsigned*)((const char*)(gbase) + (voff)[_i]), (LAS unsigned*)(lds + (bufoff) + ldsw + _i * 8192), 16, 0, 0); } while (0)
; #define PG8_LDA(dst, b, h) do { _Pragma("unroll") for (int m = 0; m < 4; ++m) _Pragma("unroll") for (int k = 0; k < 2; ++k) dst[m][k] = *(const LAS bf16x8*)(lds + PG8_SA(b, h) + aoff + m * 2048 + k * 1024); } while (0)
; #define PG8_MMA(ai, bj, At, Bt) do { __builtin_amdgcn_s_setprio(1); _Pragma("unroll") for (int m = 0; m < 4; ++m) _Pragma("unroll") for (int n = 0; n < 2; ++n) _Pragma("unroll") for (int k = 0; k < 2; ++k) \
;         acc[ai][bj][m][n] = __builtin_amdgcn_mfma_f32_16x16x32_bf16(Bt[n][k], At[m][k], acc[ai][bj][m][n], 0, 0, 0); __builtin_amdgcn_s_setprio(0); } while (0)
; #define PG8_WAIT_V(n) asm volatile("s_waitcnt vmcnt(" #n ")" ::: "memory")
; #define PG8_WAIT_L(n) asm volatile("s_waitcnt lgkmcnt(" #n ")" ::: "memory")
; #define PG8_BAR __builtin_amdgcn_s_barrier()
; #define PG8_SCHED __builtin_amdgcn_sched_barrier(0)
; template <class Epi, class Sched>
; __device__ __forceinline__ void gemm_phase(LAS unsigned char* lds, const Gemm g, const Sched& S, const Epi& E, const int tid, unsigned* last_sig = nullptr) {
;     ...
;             PG8_LDA(At, 1, 1); PG8_STAGE(PG8_SB(1, 0), b3, voffB); PG8_STAGE(PG8_SB(1, 1), b3 + hstep, voffB); PG8_STAGE(PG8_SA(1, 0), a3, voffA);
;             PG8_WAIT_V(8); PG8_WAIT_L(0); PG8_BAR; PG8_MMA(1, 0, At, B0); PG8_MMA(1, 1, At, B1); PG8_BAR; PG8_SCHED;
;         }
;         if (wr == 0) PG8_BAR;
	s_add_i32 s14, s59, s31
	v_lshl_add_u64 v[140:141], v[140:141], 0, s[34:35]
	s_mov_b32 m0, s14
	ds_read_b128 v[178:181], v145 offset:49152
	ds_read_b128 v[182:185], v145 offset:50176
	ds_read_b128 v[200:203], v145 offset:51200
	ds_read_b128 v[204:207], v145 offset:52224
	ds_read_b128 v[208:211], v145 offset:53248
	ds_read_b128 v[212:215], v145 offset:54272
	ds_read_b128 v[216:219], v145 offset:55296
	ds_read_b128 v[220:223], v145 offset:56320
	global_load_lds_dwordx4 v[140:141], off
	s_add_i32 m0, s14, 0x2000
	s_add_u32 s14, s44, 0x80080
	v_lshl_add_u64 v[140:141], v[232:233], 0, s[34:35]
	s_addc_u32 s15, s45, 0
	s_add_i32 s44, s60, s31
	global_load_lds_dwordx4 v[140:141], off
	v_lshl_add_u64 v[140:141], s[14:15], 0, v[186:187]
	s_mov_b32 m0, s44
	s_nop 0
	global_load_lds_dwordx4 v[140:141], off
	v_lshl_add_u64 v[140:141], s[14:15], 0, v[132:133]
	s_add_i32 m0, s44, 0x2000
	s_nop 0
	global_load_lds_dwordx4 v[140:141], off
	v_lshl_add_u64 v[140:141], v[234:235], 0, s[34:35]
	s_mov_b32 m0, s52
	s_nop 0
	global_load_lds_dwordx4 v[140:141], off
	v_lshl_add_u64 v[140:141], v[236:237], 0, s[34:35]
	s_mov_b32 m0, s53
	s_nop 0
	global_load_lds_dwordx4 v[140:141], off
	s_waitcnt vmcnt(8)
	s_waitcnt lgkmcnt(0)
	s_barrier
	s_setprio 1
	s_waitcnt lgkmcnt(0)
	v_mfma_f32_16x16x32_bf16 v[62:65], v[146:149], v[178:181], v[62:65]
	v_mfma_f32_16x16x32_bf16 v[54:57], v[154:157], v[178:181], v[54:57]
	v_mfma_f32_16x16x32_bf16 v[46:49], v[146:149], v[200:203], v[46:49]
	v_mfma_f32_16x16x32_bf16 v[38:41], v[154:157], v[200:203], v[38:41]
	v_mfma_f32_16x16x32_bf16 v[30:33], v[146:149], v[208:211], v[30:33]
	v_mfma_f32_16x16x32_bf16 v[22:25], v[154:157], v[208:211], v[22:25]
	v_mfma_f32_16x16x32_bf16 v[14:17], v[146:149], v[216:219], v[14:17]
	v_mfma_f32_16x16x32_bf16 v[6:9], v[154:157], v[216:219], v[6:9]
	s_setprio 0
	s_setprio 1
	v_mfma_f32_16x16x32_bf16 v[62:65], v[150:153], v[182:185], v[62:65]
	v_mfma_f32_16x16x32_bf16 v[54:57], v[158:161], v[182:185], v[54:57]
	v_mfma_f32_16x16x32_bf16 v[46:49], v[150:153], v[204:207], v[46:49]
	v_mfma_f32_16x16x32_bf16 v[38:41], v[158:161], v[204:207], v[38:41]
	v_mfma_f32_16x16x32_bf16 v[30:33], v[150:153], v[212:215], v[30:33]
	v_mfma_f32_16x16x32_bf16 v[22:25], v[158:161], v[212:215], v[22:25]
	v_mfma_f32_16x16x32_bf16 v[14:17], v[150:153], v[220:223], v[14:17]
	v_mfma_f32_16x16x32_bf16 v[6:9], v[158:161], v[220:223], v[6:9]
	s_setprio 0
	s_setprio 1
	v_mfma_f32_16x16x32_bf16 v[58:61], v[162:165], v[178:181], v[58:61]
	v_mfma_f32_16x16x32_bf16 v[50:53], v[170:173], v[178:181], v[50:53]
	v_mfma_f32_16x16x32_bf16 v[42:45], v[162:165], v[200:203], v[42:45]
	v_mfma_f32_16x16x32_bf16 v[34:37], v[170:173], v[200:203], v[34:37]
	v_mfma_f32_16x16x32_bf16 v[26:29], v[162:165], v[208:211], v[26:29]
	v_mfma_f32_16x16x32_bf16 v[18:21], v[170:173], v[208:211], v[18:21]
	v_mfma_f32_16x16x32_bf16 v[10:13], v[162:165], v[216:219], v[10:13]
	v_mfma_f32_16x16x32_bf16 v[2:5], v[170:173], v[216:219], v[2:5]
	s_setprio 0
	s_setprio 1
	v_mfma_f32_16x16x32_bf16 v[58:61], v[166:169], v[182:185], v[58:61]
	v_mfma_f32_16x16x32_bf16 v[50:53], v[174:177], v[182:185], v[50:53]
	v_mfma_f32_16x16x32_bf16 v[42:45], v[166:169], v[204:207], v[42:45]
	v_mfma_f32_16x16x32_bf16 v[34:37], v[174:177], v[204:207], v[34:37]
	v_mfma_f32_16x16x32_bf16 v[26:29], v[166:169], v[212:215], v[26:29]
	v_mfma_f32_16x16x32_bf16 v[18:21], v[174:177], v[212:215], v[18:21]
	v_mfma_f32_16x16x32_bf16 v[10:13], v[166:169], v[220:223], v[10:13]
	v_mfma_f32_16x16x32_bf16 v[2:5], v[174:177], v[220:223], v[2:5]
	s_setprio 0
	s_barrier
	s_add_i32 s58, s58, 2
	s_add_u32 s4, s4, 0x100
	s_addc_u32 s5, s5, 0
	s_add_u32 s56, s56, 0x100
	s_addc_u32 s57, s57, 0
	s_cmp_gt_u32 s58, 29
	s_cbranch_scc0 .LBB0_1104
	s_and_b64 vcc, exec, s[12:13]
	s_cbranch_vccz .LBB0_1107
	s_barrier

; #define PG8_STAGE(bufoff, gbase, voff) do { _Pragma("unroll") for (int _i = 0; _i < 2; ++_i) \
;         __builtin_amdgcn_global_load_lds((const unsigned*)((const char*)(gbase) + (voff)[_i]), (LAS unsigned*)(lds + (bufoff) + ldsw + _i * 8192), 16, 0, 0); } while (0)
; #define PG8_LDA(dst, b, h) do { _Pragma("unroll") for (int m = 0; m < 4; ++m) _Pragma("unroll") for (int k = 0; k < 2; ++k) dst[m][k] = *(const LAS bf16x8*)(lds + PG8_SA(b, h) + aoff + m * 2048 + k * 1024); } while (0)
; #define PG8_LDB(dst, b, h) do { _Pragma("unroll") for (int n = 0; n < 2; ++n) _Pragma("unroll") for (int k = 0; k < 2; ++k) dst[n][k] = *(const LAS bf16x8*)(lds + PG8_SB(b, h) + boff + n * 2048 + k * 1024); } while (0)
; #define PG8_MMA(ai, bj, At, Bt) do { __builtin_amdgcn_s_setprio(1); _Pragma("unroll") for (int m = 0; m < 4; ++m) _Pragma("unroll") for (int n = 0; n < 2; ++n) _Pragma("unroll") for (int k = 0; k < 2; ++k) \
;         acc[ai][bj][m][n] = __builtin_amdgcn_mfma_f32_16x16x32_bf16(Bt[n][k], At[m][k], acc[ai][bj][m][n], 0, 0, 0); __builtin_amdgcn_s_setprio(0); } while (0)
; #define PG8_WAIT_V(n) asm volatile("s_waitcnt vmcnt(" #n ")" ::: "memory")
; #define PG8_WAIT_L(n) asm volatile("s_waitcnt lgkmcnt(" #n ")" ::: "memory")
; #define PG8_BAR __builtin_amdgcn_s_barrier()
; template <class Epi, class Sched>
; __device__ __forceinline__ void gemm_phase(LAS unsigned char* lds, const Gemm g, const Sched& S, const Epi& E, const int tid, unsigned* last_sig = nullptr) {
;     ...
;         for (int t = 0; t < nt; t += 2) {
;             const bool last = (t == nt - 2);
;             const char* a1 = cA + (size_t)(t + 1) * kstep;
;             const char* a2 = last ? nA : cA + (size_t)(t + 2) * kstep; const char* b2 = last ? nB : cB + (size_t)(t + 2) * kstep;
;             const char* a3 = a2 + kstep; const char* b3 = b2 + kstep;
;             PG8_LDB(B0, 0, 0); PG8_LDB(B1, 0, 1); PG8_SCHED; PG8_LDA(At, 0, 0); PG8_STAGE(PG8_SA(1, 1), a1 + hstep, voffA);
;             PG8_WAIT_V(8); PG8_WAIT_L(0); PG8_BAR; PG8_MMA(0, 0, At, B0); PG8_MMA(0, 1, At, B1); PG8_BAR; PG8_SCHED;
;             PG8_LDA(At, 0, 1); PG8_STAGE(PG8_SB(0, 0), b2, voffB); PG8_STAGE(PG8_SB(0, 1), b2 + hstep, voffB); PG8_STAGE(PG8_SA(0, 0), a2, voffA);
;             PG8_WAIT_V(8); PG8_WAIT_L(0); PG8_BAR; PG8_MMA(1, 0, At, B0); PG8_MMA(1, 1, At, B1); PG8_BAR; PG8_SCHED;
.LBB0_1188:
	s_add_u32 s14, s20, 0xfff80080
	s_addc_u32 s15, s21, -1
	s_add_i32 s55, 0, 0x10000
	s_cmp_eq_u32 s54, 28
	s_cselect_b32 s41, s13, s15
	s_cselect_b32 s40, s50, s14
	v_add_u32_e32 v140, s55, v1
	s_cselect_b32 s23, s11, s53
	s_cselect_b32 s22, s51, s52
	s_add_i32 s56, 0, 0x14000
	ds_read_b128 v[146:149], v140
	ds_read_b128 v[150:153], v140 offset:1024
	ds_read_b128 v[154:157], v140 offset:2048
	ds_read_b128 v[158:161], v140 offset:3072
	v_add_u32_e32 v140, s56, v1
	ds_read_b128 v[162:165], v140
	ds_read_b128 v[166:169], v140 offset:1024
	ds_read_b128 v[170:173], v140 offset:2048
	ds_read_b128 v[174:177], v140 offset:3072
	v_lshl_add_u64 v[140:141], s[20:21], 0, v[136:137]
	s_add_i32 m0, s31, 0xc000
	ds_read_b128 v[178:181], v144
	ds_read_b128 v[182:185], v144 offset:1024
	ds_read_b128 v[200:203], v144 offset:2048
	ds_read_b128 v[204:207], v144 offset:3072
	ds_read_b128 v[208:211], v144 offset:4096
	ds_read_b128 v[212:215], v144 offset:5120
	ds_read_b128 v[216:219], v144 offset:6144
	ds_read_b128 v[220:223], v144 offset:7168
	global_load_lds_dwordx4 v[140:141], off
	v_lshl_add_u64 v[140:141], s[20:21], 0, v[138:139]
	s_add_i32 m0, s31, 0xe000
	s_nop 0
	global_load_lds_dwordx4 v[140:141], off
	s_waitcnt vmcnt(8)
	s_waitcnt lgkmcnt(0)
	s_barrier
	s_setprio 1
	s_waitcnt lgkmcnt(0)
	v_mfma_f32_16x16x32_bf16 v[126:129], v[146:149], v[178:181], v[126:129]
	v_mfma_f32_16x16x32_bf16 v[118:121], v[154:157], v[178:181], v[118:121]
	v_mfma_f32_16x16x32_bf16 v[110:113], v[146:149], v[200:203], v[110:113]
	v_mfma_f32_16x16x32_bf16 v[102:105], v[154:157], v[200:203], v[102:105]
	v_mfma_f32_16x16x32_bf16 v[94:97], v[146:149], v[208:211], v[94:97]
	v_mfma_f32_16x16x32_bf16 v[86:89], v[154:157], v[208:211], v[86:89]
	v_mfma_f32_16x16x32_bf16 v[78:81], v[146:149], v[216:219], v[78:81]
	v_mfma_f32_16x16x32_bf16 v[70:73], v[154:157], v[216:219], v[70:73]
	s_setprio 0
	s_setprio 1
	v_mfma_f32_16x16x32_bf16 v[126:129], v[150:153], v[182:185], v[126:129]
	v_mfma_f32_16x16x32_bf16 v[118:121], v[158:161], v[182:185], v[118:121]
	v_mfma_f32_16x16x32_bf16 v[110:113], v[150:153], v[204:207], v[110:113]
	v_mfma_f32_16x16x32_bf16 v[102:105], v[158:161], v[204:207], v[102:105]
	v_mfma_f32_16x16x32_bf16 v[94:97], v[150:153], v[212:215], v[94:97]
	v_mfma_f32_16x16x32_bf16 v[86:89], v[158:161], v[212:215], v[86:89]
	v_mfma_f32_16x16x32_bf16 v[78:81], v[150:153], v[220:223], v[78:81]
	v_mfma_f32_16x16x32_bf16 v[70:73], v[158:161], v[220:223], v[70:73]
	s_setprio 0
	s_setprio 1
	v_mfma_f32_16x16x32_bf16 v[122:125], v[162:165], v[178:181], v[122:125]
	v_mfma_f32_16x16x32_bf16 v[114:117], v[170:173], v[178:181], v[114:117]
	v_mfma_f32_16x16x32_bf16 v[106:109], v[162:165], v[200:203], v[106:109]
	v_mfma_f32_16x16x32_bf16 v[98:101], v[170:173], v[200:203], v[98:101]
	v_mfma_f32_16x16x32_bf16 v[90:93], v[162:165], v[208:211], v[90:93]
	v_mfma_f32_16x16x32_bf16 v[82:85], v[170:173], v[208:211], v[82:85]
	v_mfma_f32_16x16x32_bf16 v[74:77], v[162:165], v[216:219], v[74:77]
	v_mfma_f32_16x16x32_bf16 v[66:69], v[170:173], v[216:219], v[66:69]
	s_setprio 0
	s_setprio 1
	v_mfma_f32_16x16x32_bf16 v[122:125], v[166:169], v[182:185], v[122:125]
	v_mfma_f32_16x16x32_bf16 v[114:117], v[174:177], v[182:185], v[114:117]
	v_mfma_f32_16x16x32_bf16 v[106:109], v[166:169], v[204:207], v[106:109]
	v_mfma_f32_16x16x32_bf16 v[98:101], v[174:177], v[204:207], v[98:101]
	v_mfma_f32_16x16x32_bf16 v[90:93], v[166:169], v[212:215], v[90:93]
	v_mfma_f32_16x16x32_bf16 v[82:85], v[174:177], v[212:215], v[82:85]
	v_mfma_f32_16x16x32_bf16 v[74:77], v[166:169], v[220:223], v[74:77]
	v_mfma_f32_16x16x32_bf16 v[66:69], v[174:177], v[220:223], v[66:69]
	s_setprio 0
	s_barrier
	s_add_i32 s14, s55, s28
	v_lshl_add_u64 v[140:141], s[22:23], 0, v[186:187]
	s_mov_b32 m0, s14
	ds_read_b128 v[178:181], v144 offset:16384
	ds_read_b128 v[182:185], v144 offset:17408
	ds_read_b128 v[200:203], v144 offset:18432
	ds_read_b128 v[204:207], v144 offset:19456
	ds_read_b128 v[208:211], v144 offset:20480
	ds_read_b128 v[212:215], v144 offset:21504
	ds_read_b128 v[216:219], v144 offset:22528
	ds_read_b128 v[220:223], v144 offset:23552
	global_load_lds_dwordx4 v[140:141], off
	s_add_i32 m0, s14, 0x2000
	s_add_u32 s14, s22, 0x80000
	v_lshl_add_u64 v[232:233], s[22:23], 0, v[130:131]
	s_addc_u32 s15, s23, 0
	s_add_i32 s55, s56, s28
	global_load_lds_dwordx4 v[232:233], off
	v_lshl_add_u64 v[234:235], s[14:15], 0, v[186:187]
	s_mov_b32 m0, s55
	v_lshl_add_u64 v[236:237], s[40:41], 0, v[132:133]
	global_load_lds_dwordx4 v[234:235], off
	v_lshl_add_u64 v[234:235], s[14:15], 0, v[130:131]
	s_add_i32 m0, s55, 0x2000
	s_nop 0
	global_load_lds_dwordx4 v[234:235], off
	v_lshl_add_u64 v[234:235], s[40:41], 0, v[134:135]
	s_mov_b32 m0, s31
	s_nop 0
	global_load_lds_dwordx4 v[234:235], off
	s_mov_b32 m0, s42
	s_nop 0
	global_load_lds_dwordx4 v[236:237], off
	s_waitcnt vmcnt(8)
	s_waitcnt lgkmcnt(0)
	s_barrier
; #define PG8_STAGE(bufoff, gbase, voff) do { _Pragma("unroll") for (int _i = 0; _i < 2; ++_i) \
;         __builtin_amdgcn_global_load_lds((const unsigned*)((const char*)(gbase) + (voff)[_i]), (LAS unsigned*)(lds + (bufoff) + ldsw + _i * 8192), 16, 0, 0); } while (0)
; #define PG8_LDA(dst, b, h) do { _Pragma("unroll") for (int m = 0; m < 4; ++m) _Pragma("unroll") for (int k = 0; k < 2; ++k) dst[m][k] = *(const LAS bf16x8*)(lds + PG8_SA(b, h) + aoff + m * 2048 + k * 1024); } while (0)
; #define PG8_LDB(dst, b, h) do { _Pragma("unroll") for (int n = 0; n < 2; ++n) _Pragma("unroll") for (int k = 0; k < 2; ++k) dst[n][k] = *(const LAS bf16x8*)(lds + PG8_SB(b, h) + boff + n * 2048 + k * 1024); } while (0)
; #define PG8_MMA(ai, bj, At, Bt) do { __builtin_amdgcn_s_setprio(1); _Pragma("unroll") for (int m = 0; m < 4; ++m) _Pragma("unroll") for (int n = 0; n < 2; ++n) _Pragma("unroll") for (int k = 0; k < 2; ++k) \
;         acc[ai][bj][m][n] = __builtin_amdgcn_mfma_f32_16x16x32_bf16(Bt[n][k], At[m][k], acc[ai][bj][m][n], 0, 0, 0); __builtin_amdgcn_s_setprio(0); } while (0)
; #define PG8_WAIT_V(n) asm volatile("s_waitcnt vmcnt(" #n ")" ::: "memory")
; #define PG8_WAIT_L(n) asm volatile("s_waitcnt lgkmcnt(" #n ")" ::: "memory")
; #define PG8_BAR __builtin_amdgcn_s_barrier()
; #define PG8_SCHED __builtin_amdgcn_sched_barrier(0)
; template <class Epi, class Sched>
; __device__ __forceinline__ void gemm_phase(LAS unsigned char* lds, const Gemm g, const Sched& S, const Epi& E, const int tid, unsigned* last_sig = nullptr) {
;     ...
;             PG8_WAIT_V(8); PG8_WAIT_L(0); PG8_BAR; PG8_MMA(1, 0, At, B0); PG8_MMA(1, 1, At, B1); PG8_BAR; PG8_SCHED;
;             PG8_LDB(B0, 1, 0); PG8_LDB(B1, 1, 1); PG8_SCHED; PG8_LDA(At, 1, 0); PG8_STAGE(PG8_SA(0, 1), a2 + hstep, voffA);
;             PG8_WAIT_V(8); PG8_WAIT_L(0); PG8_BAR; PG8_MMA(0, 0, At, B0); PG8_MMA(0, 1, At, B1); PG8_BAR; PG8_SCHED;
	s_setprio 1
	s_waitcnt lgkmcnt(0)
	v_mfma_f32_16x16x32_bf16 v[62:65], v[146:149], v[178:181], v[62:65]
	v_mfma_f32_16x16x32_bf16 v[54:57], v[154:157], v[178:181], v[54:57]
	v_mfma_f32_16x16x32_bf16 v[46:49], v[146:149], v[200:203], v[46:49]
	v_mfma_f32_16x16x32_bf16 v[38:41], v[154:157], v[200:203], v[38:41]
	v_mfma_f32_16x16x32_bf16 v[30:33], v[146:149], v[208:211], v[30:33]
	v_mfma_f32_16x16x32_bf16 v[22:25], v[154:157], v[208:211], v[22:25]
	v_mfma_f32_16x16x32_bf16 v[14:17], v[146:149], v[216:219], v[14:17]
	v_mfma_f32_16x16x32_bf16 v[6:9], v[154:157], v[216:219], v[6:9]
	s_setprio 0
	s_setprio 1
	v_mfma_f32_16x16x32_bf16 v[62:65], v[150:153], v[182:185], v[62:65]
	v_mfma_f32_16x16x32_bf16 v[54:57], v[158:161], v[182:185], v[54:57]
	v_mfma_f32_16x16x32_bf16 v[46:49], v[150:153], v[204:207], v[46:49]
	v_mfma_f32_16x16x32_bf16 v[38:41], v[158:161], v[204:207], v[38:41]
	v_mfma_f32_16x16x32_bf16 v[30:33], v[150:153], v[212:215], v[30:33]
	v_mfma_f32_16x16x32_bf16 v[22:25], v[158:161], v[212:215], v[22:25]
	v_mfma_f32_16x16x32_bf16 v[14:17], v[150:153], v[220:223], v[14:17]
	v_mfma_f32_16x16x32_bf16 v[6:9], v[158:161], v[220:223], v[6:9]
	s_setprio 0
	s_setprio 1
	v_mfma_f32_16x16x32_bf16 v[58:61], v[162:165], v[178:181], v[58:61]
	v_mfma_f32_16x16x32_bf16 v[50:53], v[170:173], v[178:181], v[50:53]
	v_mfma_f32_16x16x32_bf16 v[42:45], v[162:165], v[200:203], v[42:45]
	v_mfma_f32_16x16x32_bf16 v[34:37], v[170:173], v[200:203], v[34:37]
	v_mfma_f32_16x16x32_bf16 v[26:29], v[162:165], v[208:211], v[26:29]
	v_mfma_f32_16x16x32_bf16 v[18:21], v[170:173], v[208:211], v[18:21]
	v_mfma_f32_16x16x32_bf16 v[10:13], v[162:165], v[216:219], v[10:13]
	v_mfma_f32_16x16x32_bf16 v[2:5], v[170:173], v[216:219], v[2:5]
	s_setprio 0
	s_setprio 1
	v_mfma_f32_16x16x32_bf16 v[58:61], v[166:169], v[182:185], v[58:61]
	v_mfma_f32_16x16x32_bf16 v[50:53], v[174:177], v[182:185], v[50:53]
	v_mfma_f32_16x16x32_bf16 v[42:45], v[166:169], v[204:207], v[42:45]
	v_mfma_f32_16x16x32_bf16 v[34:37], v[174:177], v[204:207], v[34:37]
	v_mfma_f32_16x16x32_bf16 v[26:29], v[166:169], v[212:215], v[26:29]
	v_mfma_f32_16x16x32_bf16 v[18:21], v[174:177], v[212:215], v[18:21]
	v_mfma_f32_16x16x32_bf16 v[10:13], v[166:169], v[220:223], v[10:13]
	v_mfma_f32_16x16x32_bf16 v[2:5], v[174:177], v[220:223], v[2:5]
	s_setprio 0
	s_barrier
	s_add_i32 s55, 0, 0x18000
	v_add_u32_e32 v145, s55, v1
	s_add_i32 s56, 0, 0x1c000
	ds_read_b128 v[146:149], v145
	ds_read_b128 v[150:153], v145 offset:1024
	ds_read_b128 v[154:157], v145 offset:2048
	ds_read_b128 v[158:161], v145 offset:3072
	v_add_u32_e32 v145, s56, v1
	ds_read_b128 v[162:165], v145
	ds_read_b128 v[166:169], v145 offset:1024
	ds_read_b128 v[170:173], v145 offset:2048
	ds_read_b128 v[174:177], v145 offset:3072
	s_add_u32 s14, s40, 0x80000
	s_addc_u32 s15, s41, 0
	s_mov_b32 m0, s43
	v_lshl_add_u64 v[238:239], s[14:15], 0, v[134:135]
	ds_read_b128 v[178:181], v144 offset:32768
	ds_read_b128 v[182:185], v144 offset:33792
	ds_read_b128 v[200:203], v144 offset:34816
	ds_read_b128 v[204:207], v144 offset:35840
	ds_read_b128 v[208:211], v144 offset:36864
	ds_read_b128 v[212:215], v144 offset:37888
	ds_read_b128 v[216:219], v144 offset:38912
	ds_read_b128 v[220:223], v144 offset:39936
	global_load_lds_dwordx4 v[238:239], off
	v_lshl_add_u64 v[238:239], s[14:15], 0, v[132:133]
	s_mov_b32 m0, s44
	s_nop 0
	global_load_lds_dwordx4 v[238:239], off
	s_waitcnt vmcnt(8)
	s_waitcnt lgkmcnt(0)
	s_barrier
	s_setprio 1
	s_waitcnt lgkmcnt(0)
	v_mfma_f32_16x16x32_bf16 v[126:129], v[146:149], v[178:181], v[126:129]
	v_mfma_f32_16x16x32_bf16 v[118:121], v[154:157], v[178:181], v[118:121]
	v_mfma_f32_16x16x32_bf16 v[110:113], v[146:149], v[200:203], v[110:113]
	v_mfma_f32_16x16x32_bf16 v[102:105], v[154:157], v[200:203], v[102:105]
	v_mfma_f32_16x16x32_bf16 v[94:97], v[146:149], v[208:211], v[94:97]
	v_mfma_f32_16x16x32_bf16 v[86:89], v[154:157], v[208:211], v[86:89]
	v_mfma_f32_16x16x32_bf16 v[78:81], v[146:149], v[216:219], v[78:81]
	v_mfma_f32_16x16x32_bf16 v[70:73], v[154:157], v[216:219], v[70:73]
	s_setprio 0
	s_setprio 1
	v_mfma_f32_16x16x32_bf16 v[126:129], v[150:153], v[182:185], v[126:129]
	v_mfma_f32_16x16x32_bf16 v[118:121], v[158:161], v[182:185], v[118:121]
	v_mfma_f32_16x16x32_bf16 v[110:113], v[150:153], v[204:207], v[110:113]
	v_mfma_f32_16x16x32_bf16 v[102:105], v[158:161], v[204:207], v[102:105]
	v_mfma_f32_16x16x32_bf16 v[94:97], v[150:153], v[212:215], v[94:97]
	v_mfma_f32_16x16x32_bf16 v[86:89], v[158:161], v[212:215], v[86:89]
	v_mfma_f32_16x16x32_bf16 v[78:81], v[150:153], v[220:223], v[78:81]
	v_mfma_f32_16x16x32_bf16 v[70:73], v[158:161], v[220:223], v[70:73]
	s_setprio 0
	s_setprio 1
	v_mfma_f32_16x16x32_bf16 v[122:125], v[162:165], v[178:181], v[122:125]
	v_mfma_f32_16x16x32_bf16 v[114:117], v[170:173], v[178:181], v[114:117]
	v_mfma_f32_16x16x32_bf16 v[106:109], v[162:165], v[200:203], v[106:109]
	v_mfma_f32_16x16x32_bf16 v[98:101], v[170:173], v[200:203], v[98:101]
	v_mfma_f32_16x16x32_bf16 v[90:93], v[162:165], v[208:211], v[90:93]
	v_mfma_f32_16x16x32_bf16 v[82:85], v[170:173], v[208:211], v[82:85]
	v_mfma_f32_16x16x32_bf16 v[74:77], v[162:165], v[216:219], v[74:77]
	v_mfma_f32_16x16x32_bf16 v[66:69], v[170:173], v[216:219], v[66:69]
	s_setprio 0
	s_setprio 1
	v_mfma_f32_16x16x32_bf16 v[122:125], v[166:169], v[182:185], v[122:125]
	v_mfma_f32_16x16x32_bf16 v[114:117], v[174:177], v[182:185], v[114:117]
	v_mfma_f32_16x16x32_bf16 v[106:109], v[166:169], v[204:207], v[106:109]
	v_mfma_f32_16x16x32_bf16 v[98:101], v[174:177], v[204:207], v[98:101]
	v_mfma_f32_16x16x32_bf16 v[90:93], v[166:169], v[212:215], v[90:93]
	v_mfma_f32_16x16x32_bf16 v[82:85], v[174:177], v[212:215], v[82:85]
	v_mfma_f32_16x16x32_bf16 v[74:77], v[166:169], v[220:223], v[74:77]
	v_mfma_f32_16x16x32_bf16 v[66:69], v[174:177], v[220:223], v[66:69]
	s_setprio 0
	s_barrier
; #define PG8_STAGE(bufoff, gbase, voff) do { _Pragma("unroll") for (int _i = 0; _i < 2; ++_i) \
;         __builtin_amdgcn_global_load_lds((const unsigned*)((const char*)(gbase) + (voff)[_i]), (LAS unsigned*)(lds + (bufoff) + ldsw + _i * 8192), 16, 0, 0); } while (0)
; #define PG8_LDA(dst, b, h) do { _Pragma("unroll") for (int m = 0; m < 4; ++m) _Pragma("unroll") for (int k = 0; k < 2; ++k) dst[m][k] = *(const LAS bf16x8*)(lds + PG8_SA(b, h) + aoff + m * 2048 + k * 1024); } while (0)
; #define PG8_MMA(ai, bj, At, Bt) do { __builtin_amdgcn_s_setprio(1); _Pragma("unroll") for (int m = 0; m < 4; ++m) _Pragma("unroll") for (int n = 0; n < 2; ++n) _Pragma("unroll") for (int k = 0; k < 2; ++k) \
;         acc[ai][bj][m][n] = __builtin_amdgcn_mfma_f32_16x16x32_bf16(Bt[n][k], At[m][k], acc[ai][bj][m][n], 0, 0, 0); __builtin_amdgcn_s_setprio(0); } while (0)
; #define PG8_WAIT_V(n) asm volatile("s_waitcnt vmcnt(" #n ")" ::: "memory")
; #define PG8_WAIT_L(n) asm volatile("s_waitcnt lgkmcnt(" #n ")" ::: "memory")
; #define PG8_BAR __builtin_amdgcn_s_barrier()
; #define PG8_SCHED __builtin_amdgcn_sched_barrier(0)
; template <class Epi, class Sched>
; __device__ __forceinline__ void gemm_phase(LAS unsigned char* lds, const Gemm g, const Sched& S, const Epi& E, const int tid, unsigned* last_sig = nullptr) {
;     ...
;         for (int t = 0; t < nt; t += 2) {
;     ...
;             PG8_LDA(At, 1, 1); PG8_STAGE(PG8_SB(1, 0), b3, voffB); PG8_STAGE(PG8_SB(1, 1), b3 + hstep, voffB); PG8_STAGE(PG8_SA(1, 0), a3, voffA);
;             PG8_WAIT_V(8); PG8_WAIT_L(0); PG8_BAR; PG8_MMA(1, 0, At, B0); PG8_MMA(1, 1, At, B1); PG8_BAR; PG8_SCHED;
;         }
;         if (wr == 0) PG8_BAR;
	s_add_i32 s14, s55, s28
	v_lshl_add_u64 v[140:141], v[140:141], 0, s[34:35]
	s_mov_b32 m0, s14
	ds_read_b128 v[178:181], v144 offset:49152
	ds_read_b128 v[182:185], v144 offset:50176
	ds_read_b128 v[200:203], v144 offset:51200
	ds_read_b128 v[204:207], v144 offset:52224
	ds_read_b128 v[208:211], v144 offset:53248
	ds_read_b128 v[212:215], v144 offset:54272
	ds_read_b128 v[216:219], v144 offset:55296
	ds_read_b128 v[220:223], v144 offset:56320
	global_load_lds_dwordx4 v[140:141], off
	s_add_i32 m0, s14, 0x2000
	s_add_u32 s14, s22, 0x80080
	v_lshl_add_u64 v[140:141], v[232:233], 0, s[34:35]
	s_addc_u32 s15, s23, 0
	s_add_i32 s22, s56, s28
	global_load_lds_dwordx4 v[140:141], off
	v_lshl_add_u64 v[140:141], s[14:15], 0, v[186:187]
	s_mov_b32 m0, s22
	s_nop 0
	global_load_lds_dwordx4 v[140:141], off
	v_lshl_add_u64 v[140:141], s[14:15], 0, v[130:131]
	s_add_i32 m0, s22, 0x2000
	s_nop 0
	global_load_lds_dwordx4 v[140:141], off
	v_lshl_add_u64 v[140:141], v[234:235], 0, s[34:35]
	s_mov_b32 m0, s45
	s_nop 0
	global_load_lds_dwordx4 v[140:141], off
	v_lshl_add_u64 v[140:141], v[236:237], 0, s[34:35]
	s_mov_b32 m0, s46
	s_nop 0
	global_load_lds_dwordx4 v[140:141], off
	s_waitcnt vmcnt(8)
	s_waitcnt lgkmcnt(0)
	s_barrier
	s_setprio 1
	s_waitcnt lgkmcnt(0)
	v_mfma_f32_16x16x32_bf16 v[62:65], v[146:149], v[178:181], v[62:65]
	v_mfma_f32_16x16x32_bf16 v[54:57], v[154:157], v[178:181], v[54:57]
	v_mfma_f32_16x16x32_bf16 v[46:49], v[146:149], v[200:203], v[46:49]
	v_mfma_f32_16x16x32_bf16 v[38:41], v[154:157], v[200:203], v[38:41]
	v_mfma_f32_16x16x32_bf16 v[30:33], v[146:149], v[208:211], v[30:33]
	v_mfma_f32_16x16x32_bf16 v[22:25], v[154:157], v[208:211], v[22:25]
	v_mfma_f32_16x16x32_bf16 v[14:17], v[146:149], v[216:219], v[14:17]
	v_mfma_f32_16x16x32_bf16 v[6:9], v[154:157], v[216:219], v[6:9]
	s_setprio 0
	s_setprio 1
	v_mfma_f32_16x16x32_bf16 v[62:65], v[150:153], v[182:185], v[62:65]
	v_mfma_f32_16x16x32_bf16 v[54:57], v[158:161], v[182:185], v[54:57]
	v_mfma_f32_16x16x32_bf16 v[46:49], v[150:153], v[204:207], v[46:49]
	v_mfma_f32_16x16x32_bf16 v[38:41], v[158:161], v[204:207], v[38:41]
	v_mfma_f32_16x16x32_bf16 v[30:33], v[150:153], v[212:215], v[30:33]
	v_mfma_f32_16x16x32_bf16 v[22:25], v[158:161], v[212:215], v[22:25]
	v_mfma_f32_16x16x32_bf16 v[14:17], v[150:153], v[220:223], v[14:17]
	v_mfma_f32_16x16x32_bf16 v[6:9], v[158:161], v[220:223], v[6:9]
	s_setprio 0
	s_setprio 1
	v_mfma_f32_16x16x32_bf16 v[58:61], v[162:165], v[178:181], v[58:61]
	v_mfma_f32_16x16x32_bf16 v[50:53], v[170:173], v[178:181], v[50:53]
	v_mfma_f32_16x16x32_bf16 v[42:45], v[162:165], v[200:203], v[42:45]
	v_mfma_f32_16x16x32_bf16 v[34:37], v[170:173], v[200:203], v[34:37]
	v_mfma_f32_16x16x32_bf16 v[26:29], v[162:165], v[208:211], v[26:29]
	v_mfma_f32_16x16x32_bf16 v[18:21], v[170:173], v[208:211], v[18:21]
	v_mfma_f32_16x16x32_bf16 v[10:13], v[162:165], v[216:219], v[10:13]
	v_mfma_f32_16x16x32_bf16 v[2:5], v[170:173], v[216:219], v[2:5]
	s_setprio 0
	s_setprio 1
	v_mfma_f32_16x16x32_bf16 v[58:61], v[166:169], v[182:185], v[58:61]
	v_mfma_f32_16x16x32_bf16 v[50:53], v[174:177], v[182:185], v[50:53]
	v_mfma_f32_16x16x32_bf16 v[42:45], v[166:169], v[204:207], v[42:45]
	v_mfma_f32_16x16x32_bf16 v[34:37], v[174:177], v[204:207], v[34:37]
	v_mfma_f32_16x16x32_bf16 v[26:29], v[166:169], v[212:215], v[26:29]
	v_mfma_f32_16x16x32_bf16 v[18:21], v[174:177], v[212:215], v[18:21]
	v_mfma_f32_16x16x32_bf16 v[10:13], v[166:169], v[220:223], v[10:13]
	v_mfma_f32_16x16x32_bf16 v[2:5], v[174:177], v[220:223], v[2:5]
	s_setprio 0
	s_barrier
	s_add_i32 s54, s54, 2
	s_add_u32 s20, s20, 0x100
	s_addc_u32 s21, s21, 0
	s_add_u32 s52, s52, 0x100
	s_addc_u32 s53, s53, 0
	s_cmp_gt_u32 s54, 29
	s_cbranch_scc0 .LBB0_1188
	s_and_b64 vcc, exec, s[8:9]
	s_cbranch_vccz .LBB0_1191
	s_barrier

; #define PG8_STAGE(bufoff, gbase, voff) do { _Pragma("unroll") for (int _i = 0; _i < 2; ++_i) \
;         __builtin_amdgcn_global_load_lds((const unsigned*)((const char*)(gbase) + (voff)[_i]), (LAS unsigned*)(lds + (bufoff) + ldsw + _i * 8192), 16, 0, 0); } while (0)
; #define PG8_LDA(dst, b, h) do { _Pragma("unroll") for (int m = 0; m < 4; ++m) _Pragma("unroll") for (int k = 0; k < 2; ++k) dst[m][k] = *(const LAS bf16x8*)(lds + PG8_SA(b, h) + aoff + m * 2048 + k * 1024); } while (0)
; #define PG8_LDB(dst, b, h) do { _Pragma("unroll") for (int n = 0; n < 2; ++n) _Pragma("unroll") for (int k = 0; k < 2; ++k) dst[n][k] = *(const LAS bf16x8*)(lds + PG8_SB(b, h) + boff + n * 2048 + k * 1024); } while (0)
; #define PG8_MMA(ai, bj, At, Bt) do { __builtin_amdgcn_s_setprio(1); _Pragma("unroll") for (int m = 0; m < 4; ++m) _Pragma("unroll") for (int n = 0; n < 2; ++n) _Pragma("unroll") for (int k = 0; k < 2; ++k) \
;         acc[ai][bj][m][n] = __builtin_amdgcn_mfma_f32_16x16x32_bf16(Bt[n][k], At[m][k], acc[ai][bj][m][n], 0, 0, 0); __builtin_amdgcn_s_setprio(0); } while (0)
; #define PG8_WAIT_V(n) asm volatile("s_waitcnt vmcnt(" #n ")" ::: "memory")
; #define PG8_WAIT_L(n) asm volatile("s_waitcnt lgkmcnt(" #n ")" ::: "memory")
; #define PG8_BAR __builtin_amdgcn_s_barrier()
; template <class Epi, class Sched>
; __device__ __forceinline__ void gemm_phase(LAS unsigned char* lds, const Gemm g, const Sched& S, const Epi& E, const int tid, unsigned* last_sig = nullptr) {
;     ...
;         for (int t = 0; t < nt; t += 2) {
;             const bool last = (t == nt - 2);
;             const char* a1 = cA + (size_t)(t + 1) * kstep;
;             const char* a2 = last ? nA : cA + (size_t)(t + 2) * kstep; const char* b2 = last ? nB : cB + (size_t)(t + 2) * kstep;
;             const char* a3 = a2 + kstep; const char* b3 = b2 + kstep;
;             PG8_LDB(B0, 0, 0); PG8_LDB(B1, 0, 1); PG8_SCHED; PG8_LDA(At, 0, 0); PG8_STAGE(PG8_SA(1, 1), a1 + hstep, voffA);
;             PG8_WAIT_V(8); PG8_WAIT_L(0); PG8_BAR; PG8_MMA(0, 0, At, B0); PG8_MMA(0, 1, At, B1); PG8_BAR; PG8_SCHED;
;             PG8_LDA(At, 0, 1); PG8_STAGE(PG8_SB(0, 0), b2, voffB); PG8_STAGE(PG8_SB(0, 1), b2 + hstep, voffB); PG8_STAGE(PG8_SA(0, 0), a2, voffA);
;             PG8_WAIT_V(8); PG8_WAIT_L(0); PG8_BAR; PG8_MMA(1, 0, At, B0); PG8_MMA(1, 1, At, B1); PG8_BAR; PG8_SCHED;
.LBB0_1262:
	s_add_u32 s18, s16, 0x100
	s_addc_u32 s19, s17, 0
	s_add_i32 s14, 0, 0x10000
	s_cmp_eq_u32 s56, 52
	s_cselect_b32 s23, s5, s19
	s_cselect_b32 s22, s4, s18
	s_cselect_b32 s21, s13, s55
	s_cselect_b32 s20, s12, s54
	s_add_i32 s57, 0, 0x14000
	v_add_u32_e32 v156, s14, v141
	v_add_u32_e32 v172, s57, v141
	ds_read_b128 v[144:147], v156
	ds_read_b128 v[148:151], v156 offset:1024
	ds_read_b128 v[152:155], v156 offset:2048
	ds_read_b128 v[156:159], v156 offset:3072
	ds_read_b128 v[160:163], v172
	ds_read_b128 v[164:167], v172 offset:1024
	ds_read_b128 v[168:171], v172 offset:2048
	ds_read_b128 v[172:175], v172 offset:3072
	v_lshl_add_u64 v[184:185], s[16:17], 0, v[136:137]
	s_add_i32 m0, s42, 0xc000
	ds_read_b128 v[176:179], v143
	ds_read_b128 v[180:183], v143 offset:1024
	ds_read_b128 v[200:203], v143 offset:2048
	ds_read_b128 v[204:207], v143 offset:3072
	ds_read_b128 v[208:211], v143 offset:4096
	ds_read_b128 v[212:215], v143 offset:5120
	ds_read_b128 v[216:219], v143 offset:6144
	ds_read_b128 v[220:223], v143 offset:7168
	global_load_lds_dwordx4 v[184:185], off
	v_lshl_add_u64 v[184:185], s[16:17], 0, v[138:139]
	s_add_i32 m0, s42, 0xe000
	s_nop 0
	global_load_lds_dwordx4 v[184:185], off
	s_waitcnt vmcnt(8)
	s_waitcnt lgkmcnt(0)
	s_barrier
	s_setprio 1
	s_waitcnt lgkmcnt(0)
	v_mfma_f32_16x16x32_bf16 v[126:129], v[144:147], v[176:179], v[126:129]
	v_mfma_f32_16x16x32_bf16 v[122:125], v[152:155], v[176:179], v[122:125]
	v_mfma_f32_16x16x32_bf16 v[118:121], v[144:147], v[200:203], v[118:121]
	v_mfma_f32_16x16x32_bf16 v[114:117], v[152:155], v[200:203], v[114:117]
	v_mfma_f32_16x16x32_bf16 v[102:105], v[144:147], v[208:211], v[102:105]
	v_mfma_f32_16x16x32_bf16 v[98:101], v[152:155], v[208:211], v[98:101]
	v_mfma_f32_16x16x32_bf16 v[86:89], v[144:147], v[216:219], v[86:89]
	v_mfma_f32_16x16x32_bf16 v[82:85], v[152:155], v[216:219], v[82:85]
	s_setprio 0
	s_setprio 1
	v_mfma_f32_16x16x32_bf16 v[126:129], v[148:151], v[180:183], v[126:129]
	v_mfma_f32_16x16x32_bf16 v[122:125], v[156:159], v[180:183], v[122:125]
	v_mfma_f32_16x16x32_bf16 v[118:121], v[148:151], v[204:207], v[118:121]
	v_mfma_f32_16x16x32_bf16 v[114:117], v[156:159], v[204:207], v[114:117]
	v_mfma_f32_16x16x32_bf16 v[102:105], v[148:151], v[212:215], v[102:105]
	v_mfma_f32_16x16x32_bf16 v[98:101], v[156:159], v[212:215], v[98:101]
	v_mfma_f32_16x16x32_bf16 v[86:89], v[148:151], v[220:223], v[86:89]
	v_mfma_f32_16x16x32_bf16 v[82:85], v[156:159], v[220:223], v[82:85]
	s_setprio 0
	s_setprio 1
	v_mfma_f32_16x16x32_bf16 v[110:113], v[160:163], v[176:179], v[110:113]
	v_mfma_f32_16x16x32_bf16 v[106:109], v[168:171], v[176:179], v[106:109]
	v_mfma_f32_16x16x32_bf16 v[94:97], v[160:163], v[200:203], v[94:97]
	v_mfma_f32_16x16x32_bf16 v[90:93], v[168:171], v[200:203], v[90:93]
	v_mfma_f32_16x16x32_bf16 v[78:81], v[160:163], v[208:211], v[78:81]
	v_mfma_f32_16x16x32_bf16 v[74:77], v[168:171], v[208:211], v[74:77]
	v_mfma_f32_16x16x32_bf16 v[70:73], v[160:163], v[216:219], v[70:73]
	v_mfma_f32_16x16x32_bf16 v[66:69], v[168:171], v[216:219], v[66:69]
	s_setprio 0
	s_setprio 1
	v_mfma_f32_16x16x32_bf16 v[110:113], v[164:167], v[180:183], v[110:113]
	v_mfma_f32_16x16x32_bf16 v[106:109], v[172:175], v[180:183], v[106:109]
	v_mfma_f32_16x16x32_bf16 v[94:97], v[164:167], v[204:207], v[94:97]
	v_mfma_f32_16x16x32_bf16 v[90:93], v[172:175], v[204:207], v[90:93]
	v_mfma_f32_16x16x32_bf16 v[78:81], v[164:167], v[212:215], v[78:81]
	v_mfma_f32_16x16x32_bf16 v[74:77], v[172:175], v[212:215], v[74:77]
	v_mfma_f32_16x16x32_bf16 v[70:73], v[164:167], v[220:223], v[70:73]
	v_mfma_f32_16x16x32_bf16 v[66:69], v[172:175], v[220:223], v[66:69]
	s_setprio 0
	s_barrier
	s_add_i32 s14, s14, s40
	v_lshl_add_u64 v[184:185], s[20:21], 0, v[186:187]
	s_mov_b32 m0, s14
	ds_read_b128 v[176:179], v143 offset:16384
	ds_read_b128 v[180:183], v143 offset:17408
	ds_read_b128 v[200:203], v143 offset:18432
	ds_read_b128 v[204:207], v143 offset:19456
	ds_read_b128 v[208:211], v143 offset:20480
	ds_read_b128 v[212:215], v143 offset:21504
	ds_read_b128 v[216:219], v143 offset:22528
	ds_read_b128 v[220:223], v143 offset:23552
	global_load_lds_dwordx4 v[184:185], off
	s_add_i32 m0, s14, 0x2000
	s_add_u32 s14, s20, 0xe0000
	v_lshl_add_u64 v[232:233], s[20:21], 0, v[134:135]
	s_addc_u32 s15, s21, 0
	s_add_i32 s16, s57, s40
	global_load_lds_dwordx4 v[232:233], off
	v_lshl_add_u64 v[234:235], s[14:15], 0, v[186:187]
	s_mov_b32 m0, s16
	v_lshl_add_u64 v[236:237], s[22:23], 0, v[132:133]
	global_load_lds_dwordx4 v[234:235], off
	v_lshl_add_u64 v[234:235], s[14:15], 0, v[134:135]
	s_add_i32 m0, s16, 0x2000
	s_nop 0
	global_load_lds_dwordx4 v[234:235], off
	v_lshl_add_u64 v[234:235], s[22:23], 0, v[130:131]
	s_mov_b32 m0, s42
	s_nop 0
	global_load_lds_dwordx4 v[234:235], off
	s_mov_b32 m0, s43
	s_nop 0
	global_load_lds_dwordx4 v[236:237], off
	s_waitcnt vmcnt(8)
	s_waitcnt lgkmcnt(0)
	s_barrier
; #define PG8_STAGE(bufoff, gbase, voff) do { _Pragma("unroll") for (int _i = 0; _i < 2; ++_i) \
;         __builtin_amdgcn_global_load_lds((const unsigned*)((const char*)(gbase) + (voff)[_i]), (LAS unsigned*)(lds + (bufoff) + ldsw + _i * 8192), 16, 0, 0); } while (0)
; #define PG8_LDA(dst, b, h) do { _Pragma("unroll") for (int m = 0; m < 4; ++m) _Pragma("unroll") for (int k = 0; k < 2; ++k) dst[m][k] = *(const LAS bf16x8*)(lds + PG8_SA(b, h) + aoff + m * 2048 + k * 1024); } while (0)
; #define PG8_LDB(dst, b, h) do { _Pragma("unroll") for (int n = 0; n < 2; ++n) _Pragma("unroll") for (int k = 0; k < 2; ++k) dst[n][k] = *(const LAS bf16x8*)(lds + PG8_SB(b, h) + boff + n * 2048 + k * 1024); } while (0)
; #define PG8_MMA(ai, bj, At, Bt) do { __builtin_amdgcn_s_setprio(1); _Pragma("unroll") for (int m = 0; m < 4; ++m) _Pragma("unroll") for (int n = 0; n < 2; ++n) _Pragma("unroll") for (int k = 0; k < 2; ++k) \
;         acc[ai][bj][m][n] = __builtin_amdgcn_mfma_f32_16x16x32_bf16(Bt[n][k], At[m][k], acc[ai][bj][m][n], 0, 0, 0); __builtin_amdgcn_s_setprio(0); } while (0)
; #define PG8_WAIT_V(n) asm volatile("s_waitcnt vmcnt(" #n ")" ::: "memory")
; #define PG8_WAIT_L(n) asm volatile("s_waitcnt lgkmcnt(" #n ")" ::: "memory")
; #define PG8_BAR __builtin_amdgcn_s_barrier()
; #define PG8_SCHED __builtin_amdgcn_sched_barrier(0)
; template <class Epi, class Sched>
; __device__ __forceinline__ void gemm_phase(LAS unsigned char* lds, const Gemm g, const Sched& S, const Epi& E, const int tid, unsigned* last_sig = nullptr) {
;     ...
;             PG8_WAIT_V(8); PG8_WAIT_L(0); PG8_BAR; PG8_MMA(1, 0, At, B0); PG8_MMA(1, 1, At, B1); PG8_BAR; PG8_SCHED;
;             PG8_LDB(B0, 1, 0); PG8_LDB(B1, 1, 1); PG8_SCHED; PG8_LDA(At, 1, 0); PG8_STAGE(PG8_SA(0, 1), a2 + hstep, voffA);
;             PG8_WAIT_V(8); PG8_WAIT_L(0); PG8_BAR; PG8_MMA(0, 0, At, B0); PG8_MMA(0, 1, At, B1); PG8_BAR; PG8_SCHED;
	s_setprio 1
	s_waitcnt lgkmcnt(0)
	v_mfma_f32_16x16x32_bf16 v[62:65], v[144:147], v[176:179], v[62:65]
	v_mfma_f32_16x16x32_bf16 v[58:61], v[152:155], v[176:179], v[58:61]
	v_mfma_f32_16x16x32_bf16 v[54:57], v[144:147], v[200:203], v[54:57]
	v_mfma_f32_16x16x32_bf16 v[50:53], v[152:155], v[200:203], v[50:53]
	v_mfma_f32_16x16x32_bf16 v[38:41], v[144:147], v[208:211], v[38:41]
	v_mfma_f32_16x16x32_bf16 v[34:37], v[152:155], v[208:211], v[34:37]
	v_mfma_f32_16x16x32_bf16 v[22:25], v[144:147], v[216:219], v[22:25]
	v_mfma_f32_16x16x32_bf16 v[18:21], v[152:155], v[216:219], v[18:21]
	s_setprio 0
	s_setprio 1
	v_mfma_f32_16x16x32_bf16 v[62:65], v[148:151], v[180:183], v[62:65]
	v_mfma_f32_16x16x32_bf16 v[58:61], v[156:159], v[180:183], v[58:61]
	v_mfma_f32_16x16x32_bf16 v[54:57], v[148:151], v[204:207], v[54:57]
	v_mfma_f32_16x16x32_bf16 v[50:53], v[156:159], v[204:207], v[50:53]
	v_mfma_f32_16x16x32_bf16 v[38:41], v[148:151], v[212:215], v[38:41]
	v_mfma_f32_16x16x32_bf16 v[34:37], v[156:159], v[212:215], v[34:37]
	v_mfma_f32_16x16x32_bf16 v[22:25], v[148:151], v[220:223], v[22:25]
	v_mfma_f32_16x16x32_bf16 v[18:21], v[156:159], v[220:223], v[18:21]
	s_setprio 0
	s_setprio 1
	v_mfma_f32_16x16x32_bf16 v[46:49], v[160:163], v[176:179], v[46:49]
	v_mfma_f32_16x16x32_bf16 v[42:45], v[168:171], v[176:179], v[42:45]
	v_mfma_f32_16x16x32_bf16 v[30:33], v[160:163], v[200:203], v[30:33]
	v_mfma_f32_16x16x32_bf16 v[26:29], v[168:171], v[200:203], v[26:29]
	v_mfma_f32_16x16x32_bf16 v[14:17], v[160:163], v[208:211], v[14:17]
	v_mfma_f32_16x16x32_bf16 v[10:13], v[168:171], v[208:211], v[10:13]
	v_mfma_f32_16x16x32_bf16 v[6:9], v[160:163], v[216:219], v[6:9]
	v_mfma_f32_16x16x32_bf16 v[2:5], v[168:171], v[216:219], v[2:5]
	s_setprio 0
	s_setprio 1
	v_mfma_f32_16x16x32_bf16 v[46:49], v[164:167], v[180:183], v[46:49]
	v_mfma_f32_16x16x32_bf16 v[42:45], v[172:175], v[180:183], v[42:45]
	v_mfma_f32_16x16x32_bf16 v[30:33], v[164:167], v[204:207], v[30:33]
	v_mfma_f32_16x16x32_bf16 v[26:29], v[172:175], v[204:207], v[26:29]
	v_mfma_f32_16x16x32_bf16 v[14:17], v[164:167], v[212:215], v[14:17]
	v_mfma_f32_16x16x32_bf16 v[10:13], v[172:175], v[212:215], v[10:13]
	v_mfma_f32_16x16x32_bf16 v[6:9], v[164:167], v[220:223], v[6:9]
	v_mfma_f32_16x16x32_bf16 v[2:5], v[172:175], v[220:223], v[2:5]
	s_setprio 0
	s_barrier
	s_add_i32 s16, 0, 0x18000
	s_add_i32 s17, 0, 0x1c000
	v_add_u32_e32 v156, s16, v141
	v_add_u32_e32 v172, s17, v141
	ds_read_b128 v[144:147], v156
	ds_read_b128 v[148:151], v156 offset:1024
	ds_read_b128 v[152:155], v156 offset:2048
	ds_read_b128 v[156:159], v156 offset:3072
	ds_read_b128 v[160:163], v172
	ds_read_b128 v[164:167], v172 offset:1024
	ds_read_b128 v[168:171], v172 offset:2048
	ds_read_b128 v[172:175], v172 offset:3072
	s_add_u32 s14, s22, 0xe0000
	s_addc_u32 s15, s23, 0
	s_mov_b32 m0, s44
	v_lshl_add_u64 v[238:239], s[14:15], 0, v[130:131]
	ds_read_b128 v[176:179], v143 offset:32768
	ds_read_b128 v[180:183], v143 offset:33792
	ds_read_b128 v[200:203], v143 offset:34816
	ds_read_b128 v[204:207], v143 offset:35840
	ds_read_b128 v[208:211], v143 offset:36864
	ds_read_b128 v[212:215], v143 offset:37888
	ds_read_b128 v[216:219], v143 offset:38912
	ds_read_b128 v[220:223], v143 offset:39936
	global_load_lds_dwordx4 v[238:239], off
	v_lshl_add_u64 v[238:239], s[14:15], 0, v[132:133]
	s_mov_b32 m0, s45
	s_nop 0
	global_load_lds_dwordx4 v[238:239], off
	s_waitcnt vmcnt(8)
	s_waitcnt lgkmcnt(0)
	s_barrier
	s_setprio 1
	s_waitcnt lgkmcnt(0)
	v_mfma_f32_16x16x32_bf16 v[126:129], v[144:147], v[176:179], v[126:129]
	v_mfma_f32_16x16x32_bf16 v[122:125], v[152:155], v[176:179], v[122:125]
	v_mfma_f32_16x16x32_bf16 v[118:121], v[144:147], v[200:203], v[118:121]
	v_mfma_f32_16x16x32_bf16 v[114:117], v[152:155], v[200:203], v[114:117]
	v_mfma_f32_16x16x32_bf16 v[102:105], v[144:147], v[208:211], v[102:105]
	v_mfma_f32_16x16x32_bf16 v[98:101], v[152:155], v[208:211], v[98:101]
	v_mfma_f32_16x16x32_bf16 v[86:89], v[144:147], v[216:219], v[86:89]
	v_mfma_f32_16x16x32_bf16 v[82:85], v[152:155], v[216:219], v[82:85]
	s_setprio 0
	s_setprio 1
	v_mfma_f32_16x16x32_bf16 v[126:129], v[148:151], v[180:183], v[126:129]
	v_mfma_f32_16x16x32_bf16 v[122:125], v[156:159], v[180:183], v[122:125]
	v_mfma_f32_16x16x32_bf16 v[118:121], v[148:151], v[204:207], v[118:121]
	v_mfma_f32_16x16x32_bf16 v[114:117], v[156:159], v[204:207], v[114:117]
	v_mfma_f32_16x16x32_bf16 v[102:105], v[148:151], v[212:215], v[102:105]
	v_mfma_f32_16x16x32_bf16 v[98:101], v[156:159], v[212:215], v[98:101]
	v_mfma_f32_16x16x32_bf16 v[86:89], v[148:151], v[220:223], v[86:89]
	v_mfma_f32_16x16x32_bf16 v[82:85], v[156:159], v[220:223], v[82:85]
	s_setprio 0
	s_setprio 1
	v_mfma_f32_16x16x32_bf16 v[110:113], v[160:163], v[176:179], v[110:113]
	v_mfma_f32_16x16x32_bf16 v[106:109], v[168:171], v[176:179], v[106:109]
	v_mfma_f32_16x16x32_bf16 v[94:97], v[160:163], v[200:203], v[94:97]
	v_mfma_f32_16x16x32_bf16 v[90:93], v[168:171], v[200:203], v[90:93]
	v_mfma_f32_16x16x32_bf16 v[78:81], v[160:163], v[208:211], v[78:81]
	v_mfma_f32_16x16x32_bf16 v[74:77], v[168:171], v[208:211], v[74:77]
	v_mfma_f32_16x16x32_bf16 v[70:73], v[160:163], v[216:219], v[70:73]
	v_mfma_f32_16x16x32_bf16 v[66:69], v[168:171], v[216:219], v[66:69]
	s_setprio 0
	s_setprio 1
	v_mfma_f32_16x16x32_bf16 v[110:113], v[164:167], v[180:183], v[110:113]
	v_mfma_f32_16x16x32_bf16 v[106:109], v[172:175], v[180:183], v[106:109]
	v_mfma_f32_16x16x32_bf16 v[94:97], v[164:167], v[204:207], v[94:97]
	v_mfma_f32_16x16x32_bf16 v[90:93], v[172:175], v[204:207], v[90:93]
	v_mfma_f32_16x16x32_bf16 v[78:81], v[164:167], v[212:215], v[78:81]
	v_mfma_f32_16x16x32_bf16 v[74:77], v[172:175], v[212:215], v[74:77]
	v_mfma_f32_16x16x32_bf16 v[70:73], v[164:167], v[220:223], v[70:73]
	v_mfma_f32_16x16x32_bf16 v[66:69], v[172:175], v[220:223], v[66:69]
	s_setprio 0
	s_barrier
; #define PG8_STAGE(bufoff, gbase, voff) do { _Pragma("unroll") for (int _i = 0; _i < 2; ++_i) \
;         __builtin_amdgcn_global_load_lds((const unsigned*)((const char*)(gbase) + (voff)[_i]), (LAS unsigned*)(lds + (bufoff) + ldsw + _i * 8192), 16, 0, 0); } while (0)
; #define PG8_LDA(dst, b, h) do { _Pragma("unroll") for (int m = 0; m < 4; ++m) _Pragma("unroll") for (int k = 0; k < 2; ++k) dst[m][k] = *(const LAS bf16x8*)(lds + PG8_SA(b, h) + aoff + m * 2048 + k * 1024); } while (0)
; #define PG8_MMA(ai, bj, At, Bt) do { __builtin_amdgcn_s_setprio(1); _Pragma("unroll") for (int m = 0; m < 4; ++m) _Pragma("unroll") for (int n = 0; n < 2; ++n) _Pragma("unroll") for (int k = 0; k < 2; ++k) \
;         acc[ai][bj][m][n] = __builtin_amdgcn_mfma_f32_16x16x32_bf16(Bt[n][k], At[m][k], acc[ai][bj][m][n], 0, 0, 0); __builtin_amdgcn_s_setprio(0); } while (0)
; #define PG8_WAIT_V(n) asm volatile("s_waitcnt vmcnt(" #n ")" ::: "memory")
; #define PG8_WAIT_L(n) asm volatile("s_waitcnt lgkmcnt(" #n ")" ::: "memory")
; #define PG8_BAR __builtin_amdgcn_s_barrier()
; #define PG8_SCHED __builtin_amdgcn_sched_barrier(0)
; template <class Epi, class Sched>
; __device__ __forceinline__ void gemm_phase(LAS unsigned char* lds, const Gemm g, const Sched& S, const Epi& E, const int tid, unsigned* last_sig = nullptr) {
;     ...
;         for (int t = 0; t < nt; t += 2) {
;     ...
;             PG8_LDA(At, 1, 1); PG8_STAGE(PG8_SB(1, 0), b3, voffB); PG8_STAGE(PG8_SB(1, 1), b3 + hstep, voffB); PG8_STAGE(PG8_SA(1, 0), a3, voffA);
;             PG8_WAIT_V(8); PG8_WAIT_L(0); PG8_BAR; PG8_MMA(1, 0, At, B0); PG8_MMA(1, 1, At, B1); PG8_BAR; PG8_SCHED;
;         }
;         if (wr == 0) PG8_BAR;
	s_add_i32 s14, s16, s40
	v_lshl_add_u64 v[184:185], v[184:185], 0, s[34:35]
	s_mov_b32 m0, s14
	ds_read_b128 v[176:179], v143 offset:49152
	ds_read_b128 v[180:183], v143 offset:50176
	ds_read_b128 v[200:203], v143 offset:51200
	ds_read_b128 v[204:207], v143 offset:52224
	ds_read_b128 v[208:211], v143 offset:53248
	ds_read_b128 v[212:215], v143 offset:54272
	ds_read_b128 v[216:219], v143 offset:55296
	ds_read_b128 v[220:223], v143 offset:56320
	global_load_lds_dwordx4 v[184:185], off
	s_add_i32 m0, s14, 0x2000
	s_add_u32 s14, s20, 0xe0080
	v_lshl_add_u64 v[184:185], v[232:233], 0, s[34:35]
	s_addc_u32 s15, s21, 0
	s_add_i32 s16, s17, s40
	global_load_lds_dwordx4 v[184:185], off
	v_lshl_add_u64 v[184:185], s[14:15], 0, v[186:187]
	s_mov_b32 m0, s16
	s_nop 0
	global_load_lds_dwordx4 v[184:185], off
	v_lshl_add_u64 v[184:185], s[14:15], 0, v[134:135]
	s_add_i32 m0, s16, 0x2000
	s_nop 0
	global_load_lds_dwordx4 v[184:185], off
	v_lshl_add_u64 v[184:185], v[234:235], 0, s[34:35]
	s_mov_b32 m0, s47
	s_nop 0
	global_load_lds_dwordx4 v[184:185], off
	v_lshl_add_u64 v[184:185], v[236:237], 0, s[34:35]
	s_mov_b32 m0, s49
	s_nop 0
	global_load_lds_dwordx4 v[184:185], off
	s_waitcnt vmcnt(8)
	s_waitcnt lgkmcnt(0)
	s_barrier
	s_setprio 1
	s_waitcnt lgkmcnt(0)
	v_mfma_f32_16x16x32_bf16 v[62:65], v[144:147], v[176:179], v[62:65]
	v_mfma_f32_16x16x32_bf16 v[58:61], v[152:155], v[176:179], v[58:61]
	v_mfma_f32_16x16x32_bf16 v[54:57], v[144:147], v[200:203], v[54:57]
	v_mfma_f32_16x16x32_bf16 v[50:53], v[152:155], v[200:203], v[50:53]
	v_mfma_f32_16x16x32_bf16 v[38:41], v[144:147], v[208:211], v[38:41]
	v_mfma_f32_16x16x32_bf16 v[34:37], v[152:155], v[208:211], v[34:37]
	v_mfma_f32_16x16x32_bf16 v[22:25], v[144:147], v[216:219], v[22:25]
	v_mfma_f32_16x16x32_bf16 v[18:21], v[152:155], v[216:219], v[18:21]
	s_setprio 0
	s_setprio 1
	v_mfma_f32_16x16x32_bf16 v[62:65], v[148:151], v[180:183], v[62:65]
	v_mfma_f32_16x16x32_bf16 v[58:61], v[156:159], v[180:183], v[58:61]
	v_mfma_f32_16x16x32_bf16 v[54:57], v[148:151], v[204:207], v[54:57]
	v_mfma_f32_16x16x32_bf16 v[50:53], v[156:159], v[204:207], v[50:53]
	v_mfma_f32_16x16x32_bf16 v[38:41], v[148:151], v[212:215], v[38:41]
	v_mfma_f32_16x16x32_bf16 v[34:37], v[156:159], v[212:215], v[34:37]
	v_mfma_f32_16x16x32_bf16 v[22:25], v[148:151], v[220:223], v[22:25]
	v_mfma_f32_16x16x32_bf16 v[18:21], v[156:159], v[220:223], v[18:21]
	s_setprio 0
	s_setprio 1
	v_mfma_f32_16x16x32_bf16 v[46:49], v[160:163], v[176:179], v[46:49]
	v_mfma_f32_16x16x32_bf16 v[42:45], v[168:171], v[176:179], v[42:45]
	v_mfma_f32_16x16x32_bf16 v[30:33], v[160:163], v[200:203], v[30:33]
	v_mfma_f32_16x16x32_bf16 v[26:29], v[168:171], v[200:203], v[26:29]
	v_mfma_f32_16x16x32_bf16 v[14:17], v[160:163], v[208:211], v[14:17]
	v_mfma_f32_16x16x32_bf16 v[10:13], v[168:171], v[208:211], v[10:13]
	v_mfma_f32_16x16x32_bf16 v[6:9], v[160:163], v[216:219], v[6:9]
	v_mfma_f32_16x16x32_bf16 v[2:5], v[168:171], v[216:219], v[2:5]
	s_setprio 0
	s_setprio 1
	v_mfma_f32_16x16x32_bf16 v[46:49], v[164:167], v[180:183], v[46:49]
	v_mfma_f32_16x16x32_bf16 v[42:45], v[172:175], v[180:183], v[42:45]
	v_mfma_f32_16x16x32_bf16 v[30:33], v[164:167], v[204:207], v[30:33]
	v_mfma_f32_16x16x32_bf16 v[26:29], v[172:175], v[204:207], v[26:29]
	v_mfma_f32_16x16x32_bf16 v[14:17], v[164:167], v[212:215], v[14:17]
	v_mfma_f32_16x16x32_bf16 v[10:13], v[172:175], v[212:215], v[10:13]
	v_mfma_f32_16x16x32_bf16 v[6:9], v[164:167], v[220:223], v[6:9]
	v_mfma_f32_16x16x32_bf16 v[2:5], v[172:175], v[220:223], v[2:5]
	s_setprio 0
	s_barrier
	s_add_i32 s56, s56, 2
	s_add_u32 s54, s54, 0x100
	s_addc_u32 s55, s55, 0
	s_cmp_gt_u32 s56, 53
	s_mov_b64 s[16:17], s[18:19]
	s_cbranch_scc0 .LBB0_1262
	s_and_b64 vcc, exec, s[10:11]
	s_cbranch_vccz .LBB0_1265
	s_barrier

; #define PG8_STAGE(bufoff, gbase, voff) do { _Pragma("unroll") for (int _i = 0; _i < 2; ++_i) \
;         __builtin_amdgcn_global_load_lds((const unsigned*)((const char*)(gbase) + (voff)[_i]), (LAS unsigned*)(lds + (bufoff) + ldsw + _i * 8192), 16, 0, 0); } while (0)
; #define PG8_LDA(dst, b, h) do { _Pragma("unroll") for (int m = 0; m < 4; ++m) _Pragma("unroll") for (int k = 0; k < 2; ++k) dst[m][k] = *(const LAS bf16x8*)(lds + PG8_SA(b, h) + aoff + m * 2048 + k * 1024); } while (0)
; #define PG8_LDB(dst, b, h) do { _Pragma("unroll") for (int n = 0; n < 2; ++n) _Pragma("unroll") for (int k = 0; k < 2; ++k) dst[n][k] = *(const LAS bf16x8*)(lds + PG8_SB(b, h) + boff + n * 2048 + k * 1024); } while (0)
; #define PG8_MMA(ai, bj, At, Bt) do { __builtin_amdgcn_s_setprio(1); _Pragma("unroll") for (int m = 0; m < 4; ++m) _Pragma("unroll") for (int n = 0; n < 2; ++n) _Pragma("unroll") for (int k = 0; k < 2; ++k) \
;         acc[ai][bj][m][n] = __builtin_amdgcn_mfma_f32_16x16x32_bf16(Bt[n][k], At[m][k], acc[ai][bj][m][n], 0, 0, 0); __builtin_amdgcn_s_setprio(0); } while (0)
; #define PG8_WAIT_V(n) asm volatile("s_waitcnt vmcnt(" #n ")" ::: "memory")
; #define PG8_WAIT_L(n) asm volatile("s_waitcnt lgkmcnt(" #n ")" ::: "memory")
; #define PG8_BAR __builtin_amdgcn_s_barrier()
; template <class Epi, class Sched>
; __device__ __forceinline__ void gemm_phase(LAS unsigned char* lds, const Gemm g, const Sched& S, const Epi& E, const int tid, unsigned* last_sig = nullptr) {
;     ...
;         for (int t = 0; t < nt; t += 2) {
;             const bool last = (t == nt - 2);
;             const char* a1 = cA + (size_t)(t + 1) * kstep;
;             const char* a2 = last ? nA : cA + (size_t)(t + 2) * kstep; const char* b2 = last ? nB : cB + (size_t)(t + 2) * kstep;
;             const char* a3 = a2 + kstep; const char* b3 = b2 + kstep;
;             PG8_LDB(B0, 0, 0); PG8_LDB(B1, 0, 1); PG8_SCHED; PG8_LDA(At, 0, 0); PG8_STAGE(PG8_SA(1, 1), a1 + hstep, voffA);
;             PG8_WAIT_V(8); PG8_WAIT_L(0); PG8_BAR; PG8_MMA(0, 0, At, B0); PG8_MMA(0, 1, At, B1); PG8_BAR; PG8_SCHED;
;             PG8_LDA(At, 0, 1); PG8_STAGE(PG8_SB(0, 0), b2, voffB); PG8_STAGE(PG8_SB(0, 1), b2 + hstep, voffB); PG8_STAGE(PG8_SA(0, 0), a2, voffA);
;             PG8_WAIT_V(8); PG8_WAIT_L(0); PG8_BAR; PG8_MMA(1, 0, At, B0); PG8_MMA(1, 1, At, B1); PG8_BAR; PG8_SCHED;
.LBB0_1288:
	s_add_u32 s16, s12, 0x100
	s_addc_u32 s17, s13, 0
	s_add_i32 s14, 0, 0x10000
	s_cmpk_eq_i32 s50, 0x54
	s_cselect_b32 s21, s5, s17
	s_cselect_b32 s20, s4, s16
	v_add_u32_e32 v151, s14, v148
	s_cselect_b32 s19, s11, s49
	s_cselect_b32 s18, s10, s48
	s_add_i32 s15, 0, 0x14000
	ds_read_b128 v[136:139], v151
	ds_read_b128 v[140:143], v151 offset:1024
	ds_read_b128 v[144:147], v151 offset:2048
	ds_read_b128 v[152:155], v151 offset:3072
	v_add_u32_e32 v151, s15, v148
	ds_read_b128 v[156:159], v151
	ds_read_b128 v[160:163], v151 offset:1024
	ds_read_b128 v[164:167], v151 offset:2048
	ds_read_b128 v[168:171], v151 offset:3072
	v_lshl_add_u64 v[184:185], s[12:13], 0, v[132:133]
	s_add_i32 m0, s23, 0xc000
	ds_read_b128 v[172:175], v150
	ds_read_b128 v[176:179], v150 offset:1024
	ds_read_b128 v[180:183], v150 offset:2048
	ds_read_b128 v[200:203], v150 offset:3072
	ds_read_b128 v[204:207], v150 offset:4096
	ds_read_b128 v[208:211], v150 offset:5120
	ds_read_b128 v[212:215], v150 offset:6144
	ds_read_b128 v[216:219], v150 offset:7168
	global_load_lds_dwordx4 v[184:185], off
	v_lshl_add_u64 v[184:185], s[12:13], 0, v[134:135]
	s_add_i32 m0, s23, 0xe000
	s_nop 0
	global_load_lds_dwordx4 v[184:185], off
	s_waitcnt vmcnt(8)
	s_waitcnt lgkmcnt(0)
	s_barrier
	s_setprio 1
	s_waitcnt lgkmcnt(0)
	v_mfma_f32_16x16x32_bf16 v[126:129], v[136:139], v[172:175], v[126:129]
	v_mfma_f32_16x16x32_bf16 v[122:125], v[144:147], v[172:175], v[122:125]
	v_mfma_f32_16x16x32_bf16 v[118:121], v[136:139], v[180:183], v[118:121]
	v_mfma_f32_16x16x32_bf16 v[114:117], v[144:147], v[180:183], v[114:117]
	v_mfma_f32_16x16x32_bf16 v[106:109], v[136:139], v[204:207], v[106:109]
	v_mfma_f32_16x16x32_bf16 v[98:101], v[144:147], v[204:207], v[98:101]
	v_mfma_f32_16x16x32_bf16 v[90:93], v[136:139], v[212:215], v[90:93]
	v_mfma_f32_16x16x32_bf16 v[82:85], v[144:147], v[212:215], v[82:85]
	s_setprio 0
	s_setprio 1
	v_mfma_f32_16x16x32_bf16 v[126:129], v[140:143], v[176:179], v[126:129]
	v_mfma_f32_16x16x32_bf16 v[122:125], v[152:155], v[176:179], v[122:125]
	v_mfma_f32_16x16x32_bf16 v[118:121], v[140:143], v[200:203], v[118:121]
	v_mfma_f32_16x16x32_bf16 v[114:117], v[152:155], v[200:203], v[114:117]
	v_mfma_f32_16x16x32_bf16 v[106:109], v[140:143], v[208:211], v[106:109]
	v_mfma_f32_16x16x32_bf16 v[98:101], v[152:155], v[208:211], v[98:101]
	v_mfma_f32_16x16x32_bf16 v[90:93], v[140:143], v[216:219], v[90:93]
	v_mfma_f32_16x16x32_bf16 v[82:85], v[152:155], v[216:219], v[82:85]
	s_setprio 0
	s_setprio 1
	v_mfma_f32_16x16x32_bf16 v[110:113], v[156:159], v[172:175], v[110:113]
	v_mfma_f32_16x16x32_bf16 v[102:105], v[164:167], v[172:175], v[102:105]
	v_mfma_f32_16x16x32_bf16 v[94:97], v[156:159], v[180:183], v[94:97]
	v_mfma_f32_16x16x32_bf16 v[86:89], v[164:167], v[180:183], v[86:89]
	v_mfma_f32_16x16x32_bf16 v[78:81], v[156:159], v[204:207], v[78:81]
	v_mfma_f32_16x16x32_bf16 v[74:77], v[164:167], v[204:207], v[74:77]
	v_mfma_f32_16x16x32_bf16 v[70:73], v[156:159], v[212:215], v[70:73]
	v_mfma_f32_16x16x32_bf16 v[66:69], v[164:167], v[212:215], v[66:69]
	s_setprio 0
	s_setprio 1
	v_mfma_f32_16x16x32_bf16 v[110:113], v[160:163], v[176:179], v[110:113]
	v_mfma_f32_16x16x32_bf16 v[102:105], v[168:171], v[176:179], v[102:105]
	v_mfma_f32_16x16x32_bf16 v[94:97], v[160:163], v[200:203], v[94:97]
	v_mfma_f32_16x16x32_bf16 v[86:89], v[168:171], v[200:203], v[86:89]
	v_mfma_f32_16x16x32_bf16 v[78:81], v[160:163], v[208:211], v[78:81]
	v_mfma_f32_16x16x32_bf16 v[74:77], v[168:171], v[208:211], v[74:77]
	v_mfma_f32_16x16x32_bf16 v[70:73], v[160:163], v[216:219], v[70:73]
	v_mfma_f32_16x16x32_bf16 v[66:69], v[168:171], v[216:219], v[66:69]
	s_setprio 0
	s_barrier
	s_add_i32 s12, s14, s22
	v_lshl_add_u64 v[184:185], s[18:19], 0, v[186:187]
	s_mov_b32 m0, s12
	ds_read_b128 v[172:175], v150 offset:16384
	ds_read_b128 v[176:179], v150 offset:17408
	ds_read_b128 v[180:183], v150 offset:18432
	ds_read_b128 v[200:203], v150 offset:19456
	ds_read_b128 v[204:207], v150 offset:20480
	ds_read_b128 v[208:211], v150 offset:21504
	ds_read_b128 v[212:215], v150 offset:22528
	ds_read_b128 v[216:219], v150 offset:23552
	global_load_lds_dwordx4 v[184:185], off
	s_add_i32 m0, s12, 0x2000
	s_add_u32 s12, s18, 0x160000
	v_lshl_add_u64 v[220:221], s[18:19], 0, v[130:131]
	s_addc_u32 s13, s19, 0
	s_add_i32 s14, s15, s22
	global_load_lds_dwordx4 v[220:221], off
	v_lshl_add_u64 v[222:223], s[12:13], 0, v[186:187]
	s_mov_b32 m0, s14
	v_lshl_add_u64 v[232:233], s[20:21], 0, v[130:131]
	global_load_lds_dwordx4 v[222:223], off
	v_lshl_add_u64 v[222:223], s[12:13], 0, v[130:131]
	s_add_i32 m0, s14, 0x2000
	s_nop 0
	global_load_lds_dwordx4 v[222:223], off
	v_lshl_add_u64 v[222:223], s[20:21], 0, v[186:187]
	s_mov_b32 m0, s23
	s_nop 0
	global_load_lds_dwordx4 v[222:223], off
	s_mov_b32 m0, s28
	s_nop 0
	global_load_lds_dwordx4 v[232:233], off
	s_waitcnt vmcnt(8)
	s_waitcnt lgkmcnt(0)
	s_barrier
; #define PG8_STAGE(bufoff, gbase, voff) do { _Pragma("unroll") for (int _i = 0; _i < 2; ++_i) \
;         __builtin_amdgcn_global_load_lds((const unsigned*)((const char*)(gbase) + (voff)[_i]), (LAS unsigned*)(lds + (bufoff) + ldsw + _i * 8192), 16, 0, 0); } while (0)
; #define PG8_LDA(dst, b, h) do { _Pragma("unroll") for (int m = 0; m < 4; ++m) _Pragma("unroll") for (int k = 0; k < 2; ++k) dst[m][k] = *(const LAS bf16x8*)(lds + PG8_SA(b, h) + aoff + m * 2048 + k * 1024); } while (0)
; #define PG8_LDB(dst, b, h) do { _Pragma("unroll") for (int n = 0; n < 2; ++n) _Pragma("unroll") for (int k = 0; k < 2; ++k) dst[n][k] = *(const LAS bf16x8*)(lds + PG8_SB(b, h) + boff + n * 2048 + k * 1024); } while (0)
; #define PG8_MMA(ai, bj, At, Bt) do { __builtin_amdgcn_s_setprio(1); _Pragma("unroll") for (int m = 0; m < 4; ++m) _Pragma("unroll") for (int n = 0; n < 2; ++n) _Pragma("unroll") for (int k = 0; k < 2; ++k) \
;         acc[ai][bj][m][n] = __builtin_amdgcn_mfma_f32_16x16x32_bf16(Bt[n][k], At[m][k], acc[ai][bj][m][n], 0, 0, 0); __builtin_amdgcn_s_setprio(0); } while (0)
; #define PG8_WAIT_V(n) asm volatile("s_waitcnt vmcnt(" #n ")" ::: "memory")
; #define PG8_WAIT_L(n) asm volatile("s_waitcnt lgkmcnt(" #n ")" ::: "memory")
; #define PG8_BAR __builtin_amdgcn_s_barrier()
; #define PG8_SCHED __builtin_amdgcn_sched_barrier(0)
; template <class Epi, class Sched>
; __device__ __forceinline__ void gemm_phase(LAS unsigned char* lds, const Gemm g, const Sched& S, const Epi& E, const int tid, unsigned* last_sig = nullptr) {
;     ...
;             PG8_WAIT_V(8); PG8_WAIT_L(0); PG8_BAR; PG8_MMA(1, 0, At, B0); PG8_MMA(1, 1, At, B1); PG8_BAR; PG8_SCHED;
;             PG8_LDB(B0, 1, 0); PG8_LDB(B1, 1, 1); PG8_SCHED; PG8_LDA(At, 1, 0); PG8_STAGE(PG8_SA(0, 1), a2 + hstep, voffA);
;             PG8_WAIT_V(8); PG8_WAIT_L(0); PG8_BAR; PG8_MMA(0, 0, At, B0); PG8_MMA(0, 1, At, B1); PG8_BAR; PG8_SCHED;
	s_setprio 1
	s_waitcnt lgkmcnt(0)
	v_mfma_f32_16x16x32_bf16 v[62:65], v[136:139], v[172:175], v[62:65]
	v_mfma_f32_16x16x32_bf16 v[58:61], v[144:147], v[172:175], v[58:61]
	v_mfma_f32_16x16x32_bf16 v[54:57], v[136:139], v[180:183], v[54:57]
	v_mfma_f32_16x16x32_bf16 v[46:49], v[144:147], v[180:183], v[46:49]
	v_mfma_f32_16x16x32_bf16 v[38:41], v[136:139], v[204:207], v[38:41]
	v_mfma_f32_16x16x32_bf16 v[30:33], v[144:147], v[204:207], v[30:33]
	v_mfma_f32_16x16x32_bf16 v[22:25], v[136:139], v[212:215], v[22:25]
	v_mfma_f32_16x16x32_bf16 v[14:17], v[144:147], v[212:215], v[14:17]
	s_setprio 0
	s_setprio 1
	v_mfma_f32_16x16x32_bf16 v[62:65], v[140:143], v[176:179], v[62:65]
	v_mfma_f32_16x16x32_bf16 v[58:61], v[152:155], v[176:179], v[58:61]
	v_mfma_f32_16x16x32_bf16 v[54:57], v[140:143], v[200:203], v[54:57]
	v_mfma_f32_16x16x32_bf16 v[46:49], v[152:155], v[200:203], v[46:49]
	v_mfma_f32_16x16x32_bf16 v[38:41], v[140:143], v[208:211], v[38:41]
	v_mfma_f32_16x16x32_bf16 v[30:33], v[152:155], v[208:211], v[30:33]
	v_mfma_f32_16x16x32_bf16 v[22:25], v[140:143], v[216:219], v[22:25]
	v_mfma_f32_16x16x32_bf16 v[14:17], v[152:155], v[216:219], v[14:17]
	s_setprio 0
	s_setprio 1
	v_mfma_f32_16x16x32_bf16 v[50:53], v[156:159], v[172:175], v[50:53]
	v_mfma_f32_16x16x32_bf16 v[42:45], v[164:167], v[172:175], v[42:45]
	v_mfma_f32_16x16x32_bf16 v[34:37], v[156:159], v[180:183], v[34:37]
	v_mfma_f32_16x16x32_bf16 v[26:29], v[164:167], v[180:183], v[26:29]
	v_mfma_f32_16x16x32_bf16 v[18:21], v[156:159], v[204:207], v[18:21]
	v_mfma_f32_16x16x32_bf16 v[10:13], v[164:167], v[204:207], v[10:13]
	v_mfma_f32_16x16x32_bf16 v[6:9], v[156:159], v[212:215], v[6:9]
	v_mfma_f32_16x16x32_bf16 v[2:5], v[164:167], v[212:215], v[2:5]
	s_setprio 0
	s_setprio 1
	v_mfma_f32_16x16x32_bf16 v[50:53], v[160:163], v[176:179], v[50:53]
	v_mfma_f32_16x16x32_bf16 v[42:45], v[168:171], v[176:179], v[42:45]
	v_mfma_f32_16x16x32_bf16 v[34:37], v[160:163], v[200:203], v[34:37]
	v_mfma_f32_16x16x32_bf16 v[26:29], v[168:171], v[200:203], v[26:29]
	v_mfma_f32_16x16x32_bf16 v[18:21], v[160:163], v[208:211], v[18:21]
	v_mfma_f32_16x16x32_bf16 v[10:13], v[168:171], v[208:211], v[10:13]
	v_mfma_f32_16x16x32_bf16 v[6:9], v[160:163], v[216:219], v[6:9]
	v_mfma_f32_16x16x32_bf16 v[2:5], v[168:171], v[216:219], v[2:5]
	s_setprio 0
	s_barrier
	s_add_i32 s14, 0, 0x18000
	v_add_u32_e32 v151, s14, v148
	s_add_i32 s15, 0, 0x1c000
	ds_read_b128 v[136:139], v151
	ds_read_b128 v[140:143], v151 offset:1024
	ds_read_b128 v[144:147], v151 offset:2048
	ds_read_b128 v[152:155], v151 offset:3072
	v_add_u32_e32 v151, s15, v148
	ds_read_b128 v[156:159], v151
	ds_read_b128 v[160:163], v151 offset:1024
	ds_read_b128 v[164:167], v151 offset:2048
	ds_read_b128 v[168:171], v151 offset:3072
	s_add_u32 s12, s20, 0x160000
	s_addc_u32 s13, s21, 0
	s_mov_b32 m0, s31
	v_lshl_add_u64 v[234:235], s[12:13], 0, v[186:187]
	ds_read_b128 v[172:175], v150 offset:32768
	ds_read_b128 v[176:179], v150 offset:33792
	ds_read_b128 v[180:183], v150 offset:34816
	ds_read_b128 v[200:203], v150 offset:35840
	ds_read_b128 v[204:207], v150 offset:36864
	ds_read_b128 v[208:211], v150 offset:37888
	ds_read_b128 v[212:215], v150 offset:38912
	ds_read_b128 v[216:219], v150 offset:39936
	global_load_lds_dwordx4 v[234:235], off
	v_lshl_add_u64 v[234:235], s[12:13], 0, v[130:131]
	s_mov_b32 m0, s40
	s_nop 0
	global_load_lds_dwordx4 v[234:235], off
	s_waitcnt vmcnt(8)
	s_waitcnt lgkmcnt(0)
	s_barrier
	s_setprio 1
	s_waitcnt lgkmcnt(0)
	v_mfma_f32_16x16x32_bf16 v[126:129], v[136:139], v[172:175], v[126:129]
	v_mfma_f32_16x16x32_bf16 v[122:125], v[144:147], v[172:175], v[122:125]
	v_mfma_f32_16x16x32_bf16 v[118:121], v[136:139], v[180:183], v[118:121]
	v_mfma_f32_16x16x32_bf16 v[114:117], v[144:147], v[180:183], v[114:117]
	v_mfma_f32_16x16x32_bf16 v[106:109], v[136:139], v[204:207], v[106:109]
	v_mfma_f32_16x16x32_bf16 v[98:101], v[144:147], v[204:207], v[98:101]
	v_mfma_f32_16x16x32_bf16 v[90:93], v[136:139], v[212:215], v[90:93]
	v_mfma_f32_16x16x32_bf16 v[82:85], v[144:147], v[212:215], v[82:85]
	s_setprio 0
	s_setprio 1
	v_mfma_f32_16x16x32_bf16 v[126:129], v[140:143], v[176:179], v[126:129]
	v_mfma_f32_16x16x32_bf16 v[122:125], v[152:155], v[176:179], v[122:125]
	v_mfma_f32_16x16x32_bf16 v[118:121], v[140:143], v[200:203], v[118:121]
	v_mfma_f32_16x16x32_bf16 v[114:117], v[152:155], v[200:203], v[114:117]
	v_mfma_f32_16x16x32_bf16 v[106:109], v[140:143], v[208:211], v[106:109]
	v_mfma_f32_16x16x32_bf16 v[98:101], v[152:155], v[208:211], v[98:101]
	v_mfma_f32_16x16x32_bf16 v[90:93], v[140:143], v[216:219], v[90:93]
	v_mfma_f32_16x16x32_bf16 v[82:85], v[152:155], v[216:219], v[82:85]
	s_setprio 0
	s_setprio 1
	v_mfma_f32_16x16x32_bf16 v[110:113], v[156:159], v[172:175], v[110:113]
	v_mfma_f32_16x16x32_bf16 v[102:105], v[164:167], v[172:175], v[102:105]
	v_mfma_f32_16x16x32_bf16 v[94:97], v[156:159], v[180:183], v[94:97]
	v_mfma_f32_16x16x32_bf16 v[86:89], v[164:167], v[180:183], v[86:89]
	v_mfma_f32_16x16x32_bf16 v[78:81], v[156:159], v[204:207], v[78:81]
	v_mfma_f32_16x16x32_bf16 v[74:77], v[164:167], v[204:207], v[74:77]
	v_mfma_f32_16x16x32_bf16 v[70:73], v[156:159], v[212:215], v[70:73]
	v_mfma_f32_16x16x32_bf16 v[66:69], v[164:167], v[212:215], v[66:69]
	s_setprio 0
	s_setprio 1
	v_mfma_f32_16x16x32_bf16 v[110:113], v[160:163], v[176:179], v[110:113]
	v_mfma_f32_16x16x32_bf16 v[102:105], v[168:171], v[176:179], v[102:105]
	v_mfma_f32_16x16x32_bf16 v[94:97], v[160:163], v[200:203], v[94:97]
	v_mfma_f32_16x16x32_bf16 v[86:89], v[168:171], v[200:203], v[86:89]
	v_mfma_f32_16x16x32_bf16 v[78:81], v[160:163], v[208:211], v[78:81]
	v_mfma_f32_16x16x32_bf16 v[74:77], v[168:171], v[208:211], v[74:77]
	v_mfma_f32_16x16x32_bf16 v[70:73], v[160:163], v[216:219], v[70:73]
	v_mfma_f32_16x16x32_bf16 v[66:69], v[168:171], v[216:219], v[66:69]
	s_setprio 0
	s_barrier
; #define PG8_STAGE(bufoff, gbase, voff) do { _Pragma("unroll") for (int _i = 0; _i < 2; ++_i) \
;         __builtin_amdgcn_global_load_lds((const unsigned*)((const char*)(gbase) + (voff)[_i]), (LAS unsigned*)(lds + (bufoff) + ldsw + _i * 8192), 16, 0, 0); } while (0)
; #define PG8_LDA(dst, b, h) do { _Pragma("unroll") for (int m = 0; m < 4; ++m) _Pragma("unroll") for (int k = 0; k < 2; ++k) dst[m][k] = *(const LAS bf16x8*)(lds + PG8_SA(b, h) + aoff + m * 2048 + k * 1024); } while (0)
; #define PG8_MMA(ai, bj, At, Bt) do { __builtin_amdgcn_s_setprio(1); _Pragma("unroll") for (int m = 0; m < 4; ++m) _Pragma("unroll") for (int n = 0; n < 2; ++n) _Pragma("unroll") for (int k = 0; k < 2; ++k) \
;         acc[ai][bj][m][n] = __builtin_amdgcn_mfma_f32_16x16x32_bf16(Bt[n][k], At[m][k], acc[ai][bj][m][n], 0, 0, 0); __builtin_amdgcn_s_setprio(0); } while (0)
; #define PG8_WAIT_V(n) asm volatile("s_waitcnt vmcnt(" #n ")" ::: "memory")
; #define PG8_WAIT_L(n) asm volatile("s_waitcnt lgkmcnt(" #n ")" ::: "memory")
; #define PG8_BAR __builtin_amdgcn_s_barrier()
; #define PG8_SCHED __builtin_amdgcn_sched_barrier(0)
; template <class Epi, class Sched>
; __device__ __forceinline__ void gemm_phase(LAS unsigned char* lds, const Gemm g, const Sched& S, const Epi& E, const int tid, unsigned* last_sig = nullptr) {
;     ...
;         for (int t = 0; t < nt; t += 2) {
;     ...
;             PG8_LDA(At, 1, 1); PG8_STAGE(PG8_SB(1, 0), b3, voffB); PG8_STAGE(PG8_SB(1, 1), b3 + hstep, voffB); PG8_STAGE(PG8_SA(1, 0), a3, voffA);
;             PG8_WAIT_V(8); PG8_WAIT_L(0); PG8_BAR; PG8_MMA(1, 0, At, B0); PG8_MMA(1, 1, At, B1); PG8_BAR; PG8_SCHED;
;         }
;         if (wr == 0) PG8_BAR;
	s_add_i32 s12, s14, s22
	v_lshl_add_u64 v[184:185], v[184:185], 0, s[34:35]
	s_mov_b32 m0, s12
	ds_read_b128 v[172:175], v150 offset:49152
	ds_read_b128 v[176:179], v150 offset:50176
	ds_read_b128 v[180:183], v150 offset:51200
	ds_read_b128 v[200:203], v150 offset:52224
	ds_read_b128 v[204:207], v150 offset:53248
	ds_read_b128 v[208:211], v150 offset:54272
	ds_read_b128 v[212:215], v150 offset:55296
	ds_read_b128 v[216:219], v150 offset:56320
	global_load_lds_dwordx4 v[184:185], off
	s_add_i32 m0, s12, 0x2000
	s_add_u32 s12, s18, 0x160080
	v_lshl_add_u64 v[184:185], v[220:221], 0, s[34:35]
	s_addc_u32 s13, s19, 0
	s_add_i32 s14, s15, s22
	global_load_lds_dwordx4 v[184:185], off
	v_lshl_add_u64 v[184:185], s[12:13], 0, v[186:187]
	s_mov_b32 m0, s14
	s_nop 0
	global_load_lds_dwordx4 v[184:185], off
	v_lshl_add_u64 v[184:185], s[12:13], 0, v[130:131]
	s_add_i32 m0, s14, 0x2000
	s_nop 0
	global_load_lds_dwordx4 v[184:185], off
	v_lshl_add_u64 v[184:185], v[222:223], 0, s[34:35]
	s_mov_b32 m0, s41
	s_nop 0
	global_load_lds_dwordx4 v[184:185], off
	v_lshl_add_u64 v[184:185], v[232:233], 0, s[34:35]
	s_mov_b32 m0, s42
	s_nop 0
	global_load_lds_dwordx4 v[184:185], off
	s_waitcnt vmcnt(8)
	s_waitcnt lgkmcnt(0)
	s_barrier
	s_setprio 1
	s_waitcnt lgkmcnt(0)
	v_mfma_f32_16x16x32_bf16 v[62:65], v[136:139], v[172:175], v[62:65]
	v_mfma_f32_16x16x32_bf16 v[58:61], v[144:147], v[172:175], v[58:61]
	v_mfma_f32_16x16x32_bf16 v[54:57], v[136:139], v[180:183], v[54:57]
	v_mfma_f32_16x16x32_bf16 v[46:49], v[144:147], v[180:183], v[46:49]
	v_mfma_f32_16x16x32_bf16 v[38:41], v[136:139], v[204:207], v[38:41]
	v_mfma_f32_16x16x32_bf16 v[30:33], v[144:147], v[204:207], v[30:33]
	v_mfma_f32_16x16x32_bf16 v[22:25], v[136:139], v[212:215], v[22:25]
	v_mfma_f32_16x16x32_bf16 v[14:17], v[144:147], v[212:215], v[14:17]
	s_setprio 0
	s_setprio 1
	v_mfma_f32_16x16x32_bf16 v[62:65], v[140:143], v[176:179], v[62:65]
	v_mfma_f32_16x16x32_bf16 v[58:61], v[152:155], v[176:179], v[58:61]
	v_mfma_f32_16x16x32_bf16 v[54:57], v[140:143], v[200:203], v[54:57]
	v_mfma_f32_16x16x32_bf16 v[46:49], v[152:155], v[200:203], v[46:49]
	v_mfma_f32_16x16x32_bf16 v[38:41], v[140:143], v[208:211], v[38:41]
	v_mfma_f32_16x16x32_bf16 v[30:33], v[152:155], v[208:211], v[30:33]
	v_mfma_f32_16x16x32_bf16 v[22:25], v[140:143], v[216:219], v[22:25]
	v_mfma_f32_16x16x32_bf16 v[14:17], v[152:155], v[216:219], v[14:17]
	s_setprio 0
	s_setprio 1
	v_mfma_f32_16x16x32_bf16 v[50:53], v[156:159], v[172:175], v[50:53]
	v_mfma_f32_16x16x32_bf16 v[42:45], v[164:167], v[172:175], v[42:45]
	v_mfma_f32_16x16x32_bf16 v[34:37], v[156:159], v[180:183], v[34:37]
	v_mfma_f32_16x16x32_bf16 v[26:29], v[164:167], v[180:183], v[26:29]
	v_mfma_f32_16x16x32_bf16 v[18:21], v[156:159], v[204:207], v[18:21]
	v_mfma_f32_16x16x32_bf16 v[10:13], v[164:167], v[204:207], v[10:13]
	v_mfma_f32_16x16x32_bf16 v[6:9], v[156:159], v[212:215], v[6:9]
	v_mfma_f32_16x16x32_bf16 v[2:5], v[164:167], v[212:215], v[2:5]
	s_setprio 0
	s_setprio 1
	v_mfma_f32_16x16x32_bf16 v[50:53], v[160:163], v[176:179], v[50:53]
	v_mfma_f32_16x16x32_bf16 v[42:45], v[168:171], v[176:179], v[42:45]
	v_mfma_f32_16x16x32_bf16 v[34:37], v[160:163], v[200:203], v[34:37]
	v_mfma_f32_16x16x32_bf16 v[26:29], v[168:171], v[200:203], v[26:29]
	v_mfma_f32_16x16x32_bf16 v[18:21], v[160:163], v[208:211], v[18:21]
	v_mfma_f32_16x16x32_bf16 v[10:13], v[168:171], v[208:211], v[10:13]
	v_mfma_f32_16x16x32_bf16 v[6:9], v[160:163], v[216:219], v[6:9]
	v_mfma_f32_16x16x32_bf16 v[2:5], v[168:171], v[216:219], v[2:5]
	s_setprio 0
	s_barrier
	s_add_i32 s50, s50, 2
	s_add_u32 s48, s48, 0x100
	s_addc_u32 s49, s49, 0
	s_cmpk_gt_u32 s50, 0x55
	s_mov_b64 s[12:13], s[16:17]
	s_cbranch_scc0 .LBB0_1288
	s_and_b64 vcc, exec, s[8:9]
	s_cbranch_vccz .LBB0_1291
	s_barrier
